# stack12 with every per-segment s_setprio flip removed from the 9 GEMM K-loops (all waves stay at priority 0)
# speedup vs baseline: 1.0025x; 1.0025x over previous
.LBB0_159:
	s_setprio 0
	v_readlane_b32 s30, v254, 1
	v_readlane_b32 s31, v254, 2
	s_mov_b32 s15, s99
	s_add_i32 s63, s63, 1
	s_mul_i32 s12, s63, s54
	s_waitcnt lgkmcnt(0)
	s_mul_hi_u32 s13, s63, s15
	s_add_i32 s13, s13, s12
	s_mul_i32 s12, s63, s15
	v_readlane_b32 s15, v254, 14
	s_add_u32 s30, s12, s15
	s_addc_u32 s31, s13, s55
	v_cmp_gt_i64_e32 vcc, s[30:31], v[178:179]
	v_cmp_lt_i64_e64 s[12:13], s[30:31], v[176:177]
	s_cbranch_vccnz .LBB0_161
	s_ashr_i32 s15, s30, 31
	s_lshr_b32 s15, s15, 29
	s_add_i32 s15, s30, s15
	s_ashr_i32 s26, s15, 3
	s_and_b32 s15, s15, -8
	s_sub_i32 s15, s30, s15
	s_cmp_lt_i32 s15, 0
	s_cselect_b32 s27, s56, 0x140
	s_mul_i32 s15, s15, s27
	s_add_i32 s15, s15, s26
	s_mul_hi_i32 s26, s15, 0x66666667
	s_lshr_b32 s27, s26, 31
	s_ashr_i32 s26, s26, 6
	s_add_i32 s26, s26, s27
	s_lshl_b32 s27, s26, 3
	s_sub_i32 s28, 0x80, s27
	s_min_i32 s28, s28, 8
	s_abs_i32 s29, s28
	v_cvt_f32_u32_e32 v2, s29
	s_sub_i32 s31, 0, s29
	s_mulk_i32 s26, 0xa0
	s_sub_i32 s15, s15, s26
	v_rcp_iflag_f32_e32 v2, v2
	s_abs_i32 s26, s15
	s_xor_b32 s30, s15, s28
	s_ashr_i32 s30, s30, 31
	v_mul_f32_e32 v2, 0x4f7ffffe, v2
	v_cvt_u32_f32_e32 v2, v2
	s_nop 0
	v_readfirstlane_b32 s34, v2
	s_mul_i32 s31, s31, s34
	s_mul_hi_u32 s31, s34, s31
	s_add_i32 s34, s34, s31
	s_mul_hi_u32 s31, s26, s34
	s_mul_i32 s34, s31, s29
	s_sub_i32 s26, s26, s34
	s_add_i32 s35, s31, 1
	s_sub_i32 s34, s26, s29
	s_cmp_ge_u32 s26, s29
	s_cselect_b32 s31, s35, s31
	s_cselect_b32 s26, s34, s26
	s_add_i32 s34, s31, 1
	s_cmp_ge_u32 s26, s29
	s_cselect_b32 s26, s34, s31
	s_xor_b32 s26, s26, s30
	s_sub_i32 s26, s26, s30
	s_mul_i32 s28, s26, s28
	s_sub_i32 s15, s15, s28
	s_add_i32 s28, s27, s15
.LBB0_161:
	s_ashr_i32 s29, s28, 31
	s_lshl_b64 s[30:31], s[28:29], 20
	v_readlane_b32 s34, v254, 18
	v_readlane_b32 s35, v254, 19
	s_add_u32 s30, s34, s30
	s_addc_u32 s31, s35, s31
	s_and_b64 s[34:35], s[12:13], exec
	s_cselect_b32 s15, s31, s17
	s_cselect_b32 s29, s30, s16
	s_ashr_i32 s27, s26, 31
	s_lshl_b64 s[34:35], s[26:27], 20
	s_add_u32 s34, s33, s34
	s_addc_u32 s35, s42, s35
	s_and_b64 s[38:39], s[12:13], exec
	s_cselect_b32 s27, s35, s37
	s_cselect_b32 s40, s34, s36
	s_add_u32 s16, s16, 0x80080
	s_addc_u32 s17, s17, 0
	s_add_u32 s41, s36, 0x100
	s_addc_u32 s64, s37, 0
	s_mov_b32 s65, -2
	ds_read_b128 v[90:93], v197
	ds_read_b128 v[94:97], v197 offset:1024
	ds_read_b128 v[98:101], v197 offset:2048
	ds_read_b128 v[102:105], v197 offset:3072
	ds_read_b128 v[146:149], v198
	ds_read_b128 v[150:153], v198 offset:1024
	ds_read_b128 v[180:183], v198 offset:2048
	ds_read_b128 v[184:187], v198 offset:3072
	s_add_u32 s36, s16, 0xfff80080
	s_addc_u32 s37, s17, -1
	s_cmp_eq_u32 s65, 28
	s_cselect_b32 s39, s15, s37
	s_cselect_b32 s38, s29, s36
	s_cselect_b32 s37, s27, s64
	s_cselect_b32 s36, s40, s41
	v_lshl_add_u64 v[212:213], s[16:17], 0, v[172:173]
	s_add_i32 m0, s44, 0xc000
	ds_read_b128 v[188:191], v199
	ds_read_b128 v[192:195], v199 offset:1024
	ds_read_b128 v[200:203], v199 offset:2048
	ds_read_b128 v[204:207], v199 offset:3072
	ds_read_b128 v[208:211], v199 offset:4096
	ds_read_b128 v[216:219], v199 offset:5120
	ds_read_b128 v[220:223], v199 offset:6144
	ds_read_b128 v[224:227], v199 offset:7168
	global_load_lds_dwordx4 v[212:213], off
	v_lshl_add_u64 v[212:213], s[16:17], 0, v[174:175]
	s_add_i32 m0, s44, 0xe000
	s_nop 0
	global_load_lds_dwordx4 v[212:213], off
	s_waitcnt vmcnt(8)
	s_waitcnt lgkmcnt(0)
	s_barrier
	v_mfma_f32_16x16x32_bf16 v[70:73], v[90:93], v[188:191], 0
	v_mfma_f32_16x16x32_bf16 v[66:69], v[98:101], v[188:191], 0
	v_mfma_f32_16x16x32_bf16 v[54:57], v[90:93], v[200:203], 0
	v_mfma_f32_16x16x32_bf16 v[50:53], v[98:101], v[200:203], 0
	v_mfma_f32_16x16x32_bf16 v[46:49], v[90:93], v[208:211], 0
	v_mfma_f32_16x16x32_bf16 v[42:45], v[98:101], v[208:211], 0
	v_mfma_f32_16x16x32_bf16 v[38:41], v[90:93], v[220:223], 0
	v_mfma_f32_16x16x32_bf16 v[34:37], v[98:101], v[220:223], 0
	v_mfma_f32_16x16x32_bf16 v[70:73], v[94:97], v[192:195], v[70:73]
	v_mfma_f32_16x16x32_bf16 v[66:69], v[102:105], v[192:195], v[66:69]
	v_mfma_f32_16x16x32_bf16 v[54:57], v[94:97], v[204:207], v[54:57]
	v_mfma_f32_16x16x32_bf16 v[50:53], v[102:105], v[204:207], v[50:53]
	v_mfma_f32_16x16x32_bf16 v[46:49], v[94:97], v[216:219], v[46:49]
	v_mfma_f32_16x16x32_bf16 v[42:45], v[102:105], v[216:219], v[42:45]
	v_mfma_f32_16x16x32_bf16 v[38:41], v[94:97], v[224:227], v[38:41]
	v_mfma_f32_16x16x32_bf16 v[34:37], v[102:105], v[224:227], v[34:37]
	v_mfma_f32_16x16x32_bf16 v[142:145], v[146:149], v[188:191], 0
	v_mfma_f32_16x16x32_bf16 v[138:141], v[180:183], v[188:191], 0
	v_mfma_f32_16x16x32_bf16 v[134:137], v[146:149], v[200:203], 0
	v_mfma_f32_16x16x32_bf16 v[130:133], v[180:183], v[200:203], 0
	v_mfma_f32_16x16x32_bf16 v[126:129], v[146:149], v[208:211], 0
	v_mfma_f32_16x16x32_bf16 v[122:125], v[180:183], v[208:211], 0
	v_mfma_f32_16x16x32_bf16 v[118:121], v[146:149], v[220:223], 0
	v_mfma_f32_16x16x32_bf16 v[114:117], v[180:183], v[220:223], 0
	v_mfma_f32_16x16x32_bf16 v[142:145], v[150:153], v[192:195], v[142:145]
	v_mfma_f32_16x16x32_bf16 v[138:141], v[184:187], v[192:195], v[138:141]
	v_mfma_f32_16x16x32_bf16 v[134:137], v[150:153], v[204:207], v[134:137]
	v_mfma_f32_16x16x32_bf16 v[130:133], v[184:187], v[204:207], v[130:133]
	v_mfma_f32_16x16x32_bf16 v[126:129], v[150:153], v[216:219], v[126:129]
	v_mfma_f32_16x16x32_bf16 v[122:125], v[184:187], v[216:219], v[122:125]
	v_mfma_f32_16x16x32_bf16 v[118:121], v[150:153], v[224:227], v[118:121]
	v_mfma_f32_16x16x32_bf16 v[114:117], v[184:187], v[224:227], v[114:117]
	s_barrier
	s_add_i32 s66, s57, s43
	v_lshl_add_u64 v[212:213], s[36:37], 0, v[156:157]
	s_mov_b32 m0, s66
	ds_read_b128 v[188:191], v199 offset:16384
	ds_read_b128 v[192:195], v199 offset:17408
	ds_read_b128 v[200:203], v199 offset:18432
	ds_read_b128 v[204:207], v199 offset:19456
	ds_read_b128 v[208:211], v199 offset:20480
	ds_read_b128 v[216:219], v199 offset:21504
	ds_read_b128 v[220:223], v199 offset:22528
	ds_read_b128 v[224:227], v199 offset:23552
	global_load_lds_dwordx4 v[212:213], off
	s_add_i32 m0, s66, 0x2000
	s_add_u32 s66, s36, 0x80000
	v_lshl_add_u64 v[214:215], s[36:37], 0, v[160:161]
	s_addc_u32 s67, s37, 0
	s_add_i32 s68, s58, s43
	global_load_lds_dwordx4 v[214:215], off
	v_lshl_add_u64 v[228:229], s[66:67], 0, v[156:157]
	s_mov_b32 m0, s68
	v_lshl_add_u64 v[230:231], s[38:39], 0, v[158:159]
	global_load_lds_dwordx4 v[228:229], off
	v_lshl_add_u64 v[228:229], s[66:67], 0, v[160:161]
	s_add_i32 m0, s68, 0x2000
	s_nop 0
	global_load_lds_dwordx4 v[228:229], off
	v_lshl_add_u64 v[228:229], s[38:39], 0, v[154:155]
	s_mov_b32 m0, s44
	s_nop 0
	global_load_lds_dwordx4 v[228:229], off
	s_mov_b32 m0, s45
	s_nop 0
	global_load_lds_dwordx4 v[230:231], off
	s_waitcnt vmcnt(8)
	s_waitcnt lgkmcnt(0)
	s_barrier
	v_mfma_f32_16x16x32_bf16 v[30:33], v[90:93], v[188:191], 0
	v_mfma_f32_16x16x32_bf16 v[26:29], v[98:101], v[188:191], 0
	v_mfma_f32_16x16x32_bf16 v[22:25], v[90:93], v[200:203], 0
	v_mfma_f32_16x16x32_bf16 v[18:21], v[98:101], v[200:203], 0
	v_mfma_f32_16x16x32_bf16 v[14:17], v[90:93], v[208:211], 0
	v_mfma_f32_16x16x32_bf16 v[10:13], v[98:101], v[208:211], 0
	v_mfma_f32_16x16x32_bf16 v[6:9], v[90:93], v[220:223], 0
	v_mfma_f32_16x16x32_bf16 v[2:5], v[98:101], v[220:223], 0
	v_mfma_f32_16x16x32_bf16 v[30:33], v[94:97], v[192:195], v[30:33]
	v_mfma_f32_16x16x32_bf16 v[26:29], v[102:105], v[192:195], v[26:29]
	v_mfma_f32_16x16x32_bf16 v[22:25], v[94:97], v[204:207], v[22:25]
	v_mfma_f32_16x16x32_bf16 v[18:21], v[102:105], v[204:207], v[18:21]
	v_mfma_f32_16x16x32_bf16 v[14:17], v[94:97], v[216:219], v[14:17]
	v_mfma_f32_16x16x32_bf16 v[10:13], v[102:105], v[216:219], v[10:13]
	v_mfma_f32_16x16x32_bf16 v[6:9], v[94:97], v[224:227], v[6:9]
	v_mfma_f32_16x16x32_bf16 v[2:5], v[102:105], v[224:227], v[2:5]
	v_mfma_f32_16x16x32_bf16 v[86:89], v[146:149], v[200:203], 0
	v_mfma_f32_16x16x32_bf16 v[82:85], v[180:183], v[200:203], 0
	v_mfma_f32_16x16x32_bf16 v[78:81], v[146:149], v[208:211], 0
	v_mfma_f32_16x16x32_bf16 v[74:77], v[180:183], v[208:211], 0
	v_mfma_f32_16x16x32_bf16 v[62:65], v[146:149], v[220:223], 0
	v_mfma_f32_16x16x32_bf16 v[58:61], v[180:183], v[220:223], 0
	v_mfma_f32_16x16x32_bf16 v[90:93], v[146:149], v[188:191], 0
	v_mfma_f32_16x16x32_bf16 v[94:97], v[180:183], v[188:191], 0
	v_mfma_f32_16x16x32_bf16 v[86:89], v[150:153], v[204:207], v[86:89]
	v_mfma_f32_16x16x32_bf16 v[82:85], v[184:187], v[204:207], v[82:85]
	v_mfma_f32_16x16x32_bf16 v[78:81], v[150:153], v[216:219], v[78:81]
	v_mfma_f32_16x16x32_bf16 v[74:77], v[184:187], v[216:219], v[74:77]
	v_mfma_f32_16x16x32_bf16 v[62:65], v[150:153], v[224:227], v[62:65]
	v_mfma_f32_16x16x32_bf16 v[58:61], v[184:187], v[224:227], v[58:61]
	v_mfma_f32_16x16x32_bf16 v[90:93], v[150:153], v[192:195], v[90:93]
	v_mfma_f32_16x16x32_bf16 v[94:97], v[184:187], v[192:195], v[94:97]
	s_barrier
	s_add_i32 s66, 0, 0x18000
	s_add_i32 s67, 0, 0x1c000
	v_add_u32_e32 v110, s66, v165
	v_add_u32_e32 v162, s67, v165
	ds_read_b128 v[98:101], v110
	ds_read_b128 v[102:105], v110 offset:1024
	ds_read_b128 v[106:109], v110 offset:2048
	ds_read_b128 v[110:113], v110 offset:3072
	ds_read_b128 v[146:149], v162
	ds_read_b128 v[150:153], v162 offset:1024
	ds_read_b128 v[180:183], v162 offset:2048
	ds_read_b128 v[184:187], v162 offset:3072
	s_add_u32 s38, s38, 0x80000
	s_addc_u32 s39, s39, 0
	s_mov_b32 m0, s47
	v_lshl_add_u64 v[232:233], s[38:39], 0, v[154:155]
	ds_read_b128 v[188:191], v199 offset:32768
	ds_read_b128 v[192:195], v199 offset:33792
	ds_read_b128 v[200:203], v199 offset:34816
	ds_read_b128 v[204:207], v199 offset:35840
	ds_read_b128 v[208:211], v199 offset:36864
	ds_read_b128 v[216:219], v199 offset:37888
	ds_read_b128 v[220:223], v199 offset:38912
	ds_read_b128 v[224:227], v199 offset:39936
	global_load_lds_dwordx4 v[232:233], off
	v_lshl_add_u64 v[232:233], s[38:39], 0, v[158:159]
	s_mov_b32 m0, s48
	s_nop 0
	global_load_lds_dwordx4 v[232:233], off
	s_waitcnt vmcnt(8)
	s_waitcnt lgkmcnt(0)
	s_barrier
	v_mfma_f32_16x16x32_bf16 v[70:73], v[98:101], v[188:191], v[70:73]
	v_mfma_f32_16x16x32_bf16 v[66:69], v[106:109], v[188:191], v[66:69]
	v_mfma_f32_16x16x32_bf16 v[54:57], v[98:101], v[200:203], v[54:57]
	v_mfma_f32_16x16x32_bf16 v[50:53], v[106:109], v[200:203], v[50:53]
	v_mfma_f32_16x16x32_bf16 v[46:49], v[98:101], v[208:211], v[46:49]
	v_mfma_f32_16x16x32_bf16 v[42:45], v[106:109], v[208:211], v[42:45]
	v_mfma_f32_16x16x32_bf16 v[38:41], v[98:101], v[220:223], v[38:41]
	v_mfma_f32_16x16x32_bf16 v[34:37], v[106:109], v[220:223], v[34:37]
	v_mfma_f32_16x16x32_bf16 v[70:73], v[102:105], v[192:195], v[70:73]
	v_mfma_f32_16x16x32_bf16 v[66:69], v[110:113], v[192:195], v[66:69]
	v_mfma_f32_16x16x32_bf16 v[54:57], v[102:105], v[204:207], v[54:57]
	v_mfma_f32_16x16x32_bf16 v[50:53], v[110:113], v[204:207], v[50:53]
	v_mfma_f32_16x16x32_bf16 v[46:49], v[102:105], v[216:219], v[46:49]
	v_mfma_f32_16x16x32_bf16 v[42:45], v[110:113], v[216:219], v[42:45]
	v_mfma_f32_16x16x32_bf16 v[38:41], v[102:105], v[224:227], v[38:41]
	v_mfma_f32_16x16x32_bf16 v[34:37], v[110:113], v[224:227], v[34:37]
	v_mfma_f32_16x16x32_bf16 v[142:145], v[146:149], v[188:191], v[142:145]
	v_mfma_f32_16x16x32_bf16 v[138:141], v[180:183], v[188:191], v[138:141]
	v_mfma_f32_16x16x32_bf16 v[134:137], v[146:149], v[200:203], v[134:137]
	v_mfma_f32_16x16x32_bf16 v[130:133], v[180:183], v[200:203], v[130:133]
	v_mfma_f32_16x16x32_bf16 v[126:129], v[146:149], v[208:211], v[126:129]
	v_mfma_f32_16x16x32_bf16 v[122:125], v[180:183], v[208:211], v[122:125]
	v_mfma_f32_16x16x32_bf16 v[118:121], v[146:149], v[220:223], v[118:121]
	v_mfma_f32_16x16x32_bf16 v[114:117], v[180:183], v[220:223], v[114:117]
	v_mfma_f32_16x16x32_bf16 v[142:145], v[150:153], v[192:195], v[142:145]
	v_mfma_f32_16x16x32_bf16 v[138:141], v[184:187], v[192:195], v[138:141]
	v_mfma_f32_16x16x32_bf16 v[134:137], v[150:153], v[204:207], v[134:137]
	v_mfma_f32_16x16x32_bf16 v[130:133], v[184:187], v[204:207], v[130:133]
	v_mfma_f32_16x16x32_bf16 v[126:129], v[150:153], v[216:219], v[126:129]
	v_mfma_f32_16x16x32_bf16 v[122:125], v[184:187], v[216:219], v[122:125]
	v_mfma_f32_16x16x32_bf16 v[118:121], v[150:153], v[224:227], v[118:121]
	v_mfma_f32_16x16x32_bf16 v[114:117], v[184:187], v[224:227], v[114:117]
	s_barrier
	s_add_i32 s38, s66, s43
	v_lshl_add_u64 v[212:213], v[212:213], 0, s[18:19]
	s_mov_b32 m0, s38
	ds_read_b128 v[188:191], v199 offset:49152
	ds_read_b128 v[192:195], v199 offset:50176
	ds_read_b128 v[200:203], v199 offset:51200
	ds_read_b128 v[204:207], v199 offset:52224
	ds_read_b128 v[208:211], v199 offset:53248
	ds_read_b128 v[216:219], v199 offset:54272
	ds_read_b128 v[220:223], v199 offset:55296
	ds_read_b128 v[224:227], v199 offset:56320
	global_load_lds_dwordx4 v[212:213], off
	s_add_i32 m0, s38, 0x2000
	s_add_u32 s36, s36, 0x80080
	v_lshl_add_u64 v[212:213], v[214:215], 0, s[18:19]
	s_addc_u32 s37, s37, 0
	s_add_i32 s38, s67, s43
	global_load_lds_dwordx4 v[212:213], off
	v_lshl_add_u64 v[212:213], s[36:37], 0, v[156:157]
	s_mov_b32 m0, s38
	s_nop 0
	global_load_lds_dwordx4 v[212:213], off
	v_lshl_add_u64 v[212:213], s[36:37], 0, v[160:161]
	s_add_i32 m0, s38, 0x2000
	s_nop 0
	global_load_lds_dwordx4 v[212:213], off
	v_lshl_add_u64 v[212:213], v[228:229], 0, s[18:19]
	s_mov_b32 m0, s52
	s_nop 0
	global_load_lds_dwordx4 v[212:213], off
	v_lshl_add_u64 v[212:213], v[230:231], 0, s[18:19]
	s_mov_b32 m0, s53
	s_nop 0
	global_load_lds_dwordx4 v[212:213], off
	s_waitcnt vmcnt(8)
	s_waitcnt lgkmcnt(0)
	s_barrier
	v_mfma_f32_16x16x32_bf16 v[30:33], v[98:101], v[188:191], v[30:33]
	v_mfma_f32_16x16x32_bf16 v[26:29], v[106:109], v[188:191], v[26:29]
	v_mfma_f32_16x16x32_bf16 v[22:25], v[98:101], v[200:203], v[22:25]
	v_mfma_f32_16x16x32_bf16 v[18:21], v[106:109], v[200:203], v[18:21]
	v_mfma_f32_16x16x32_bf16 v[14:17], v[98:101], v[208:211], v[14:17]
	v_mfma_f32_16x16x32_bf16 v[10:13], v[106:109], v[208:211], v[10:13]
	v_mfma_f32_16x16x32_bf16 v[6:9], v[98:101], v[220:223], v[6:9]
	v_mfma_f32_16x16x32_bf16 v[2:5], v[106:109], v[220:223], v[2:5]
	v_mfma_f32_16x16x32_bf16 v[30:33], v[102:105], v[192:195], v[30:33]
	v_mfma_f32_16x16x32_bf16 v[26:29], v[110:113], v[192:195], v[26:29]
	v_mfma_f32_16x16x32_bf16 v[22:25], v[102:105], v[204:207], v[22:25]
	v_mfma_f32_16x16x32_bf16 v[18:21], v[110:113], v[204:207], v[18:21]
	v_mfma_f32_16x16x32_bf16 v[14:17], v[102:105], v[216:219], v[14:17]
	v_mfma_f32_16x16x32_bf16 v[10:13], v[110:113], v[216:219], v[10:13]
	v_mfma_f32_16x16x32_bf16 v[6:9], v[102:105], v[224:227], v[6:9]
	v_mfma_f32_16x16x32_bf16 v[2:5], v[110:113], v[224:227], v[2:5]
	v_mfma_f32_16x16x32_bf16 v[90:93], v[146:149], v[188:191], v[90:93]
	v_mfma_f32_16x16x32_bf16 v[110:113], v[150:153], v[192:195], v[90:93]
	v_mfma_f32_16x16x32_bf16 v[90:93], v[180:183], v[188:191], v[94:97]
	v_mfma_f32_16x16x32_bf16 v[86:89], v[146:149], v[200:203], v[86:89]
	v_mfma_f32_16x16x32_bf16 v[82:85], v[180:183], v[200:203], v[82:85]
	v_mfma_f32_16x16x32_bf16 v[78:81], v[146:149], v[208:211], v[78:81]
	v_mfma_f32_16x16x32_bf16 v[74:77], v[180:183], v[208:211], v[74:77]
	v_mfma_f32_16x16x32_bf16 v[62:65], v[146:149], v[220:223], v[62:65]
	v_mfma_f32_16x16x32_bf16 v[58:61], v[180:183], v[220:223], v[58:61]
	v_mfma_f32_16x16x32_bf16 v[106:109], v[184:187], v[192:195], v[90:93]
	v_mfma_f32_16x16x32_bf16 v[86:89], v[150:153], v[204:207], v[86:89]
	v_mfma_f32_16x16x32_bf16 v[82:85], v[184:187], v[204:207], v[82:85]
	v_mfma_f32_16x16x32_bf16 v[78:81], v[150:153], v[216:219], v[78:81]
	v_mfma_f32_16x16x32_bf16 v[74:77], v[184:187], v[216:219], v[74:77]
	v_mfma_f32_16x16x32_bf16 v[62:65], v[150:153], v[224:227], v[62:65]
	v_mfma_f32_16x16x32_bf16 v[58:61], v[184:187], v[224:227], v[58:61]
	s_barrier
	s_add_i32 s65, s65, 2
	s_add_u32 s16, s16, 0x100
	s_addc_u32 s17, s17, 0
	s_add_u32 s41, s41, 0x100
	s_addc_u32 s64, s64, 0
	s_cmp_gt_u32 s65, 29
.LBB0_162:
	ds_read_b128 v[90:93], v197
	ds_read_b128 v[94:97], v197 offset:1024
	ds_read_b128 v[98:101], v197 offset:2048
	ds_read_b128 v[102:105], v197 offset:3072
	ds_read_b128 v[146:149], v198
	ds_read_b128 v[150:153], v198 offset:1024
	ds_read_b128 v[180:183], v198 offset:2048
	ds_read_b128 v[184:187], v198 offset:3072
	s_add_u32 s36, s16, 0xfff80080
	s_addc_u32 s37, s17, -1
	s_cmp_eq_u32 s65, 28
	s_cselect_b32 s39, s15, s37
	s_cselect_b32 s38, s29, s36
	s_cselect_b32 s37, s27, s64
	s_cselect_b32 s36, s40, s41
	v_lshl_add_u64 v[212:213], s[16:17], 0, v[172:173]
	s_add_i32 m0, s44, 0xc000
	ds_read_b128 v[188:191], v199
	ds_read_b128 v[192:195], v199 offset:1024
	ds_read_b128 v[200:203], v199 offset:2048
	ds_read_b128 v[204:207], v199 offset:3072
	ds_read_b128 v[208:211], v199 offset:4096
	ds_read_b128 v[216:219], v199 offset:5120
	ds_read_b128 v[220:223], v199 offset:6144
	ds_read_b128 v[224:227], v199 offset:7168
	global_load_lds_dwordx4 v[212:213], off
	v_lshl_add_u64 v[212:213], s[16:17], 0, v[174:175]
	s_add_i32 m0, s44, 0xe000
	s_nop 0
	global_load_lds_dwordx4 v[212:213], off
	s_waitcnt vmcnt(8)
	s_waitcnt lgkmcnt(0)
	s_barrier
	v_mfma_f32_16x16x32_bf16 v[70:73], v[90:93], v[188:191], v[70:73]
	v_mfma_f32_16x16x32_bf16 v[66:69], v[98:101], v[188:191], v[66:69]
	v_mfma_f32_16x16x32_bf16 v[54:57], v[90:93], v[200:203], v[54:57]
	v_mfma_f32_16x16x32_bf16 v[50:53], v[98:101], v[200:203], v[50:53]
	v_mfma_f32_16x16x32_bf16 v[46:49], v[90:93], v[208:211], v[46:49]
	v_mfma_f32_16x16x32_bf16 v[42:45], v[98:101], v[208:211], v[42:45]
	v_mfma_f32_16x16x32_bf16 v[38:41], v[90:93], v[220:223], v[38:41]
	v_mfma_f32_16x16x32_bf16 v[34:37], v[98:101], v[220:223], v[34:37]
	v_mfma_f32_16x16x32_bf16 v[70:73], v[94:97], v[192:195], v[70:73]
	v_mfma_f32_16x16x32_bf16 v[66:69], v[102:105], v[192:195], v[66:69]
	v_mfma_f32_16x16x32_bf16 v[54:57], v[94:97], v[204:207], v[54:57]
	v_mfma_f32_16x16x32_bf16 v[50:53], v[102:105], v[204:207], v[50:53]
	v_mfma_f32_16x16x32_bf16 v[46:49], v[94:97], v[216:219], v[46:49]
	v_mfma_f32_16x16x32_bf16 v[42:45], v[102:105], v[216:219], v[42:45]
	v_mfma_f32_16x16x32_bf16 v[38:41], v[94:97], v[224:227], v[38:41]
	v_mfma_f32_16x16x32_bf16 v[34:37], v[102:105], v[224:227], v[34:37]
	v_mfma_f32_16x16x32_bf16 v[142:145], v[146:149], v[188:191], v[142:145]
	v_mfma_f32_16x16x32_bf16 v[138:141], v[180:183], v[188:191], v[138:141]
	v_mfma_f32_16x16x32_bf16 v[134:137], v[146:149], v[200:203], v[134:137]
	v_mfma_f32_16x16x32_bf16 v[130:133], v[180:183], v[200:203], v[130:133]
	v_mfma_f32_16x16x32_bf16 v[126:129], v[146:149], v[208:211], v[126:129]
	v_mfma_f32_16x16x32_bf16 v[122:125], v[180:183], v[208:211], v[122:125]
	v_mfma_f32_16x16x32_bf16 v[118:121], v[146:149], v[220:223], v[118:121]
	v_mfma_f32_16x16x32_bf16 v[114:117], v[180:183], v[220:223], v[114:117]
	v_mfma_f32_16x16x32_bf16 v[142:145], v[150:153], v[192:195], v[142:145]
	v_mfma_f32_16x16x32_bf16 v[138:141], v[184:187], v[192:195], v[138:141]
	v_mfma_f32_16x16x32_bf16 v[134:137], v[150:153], v[204:207], v[134:137]
	v_mfma_f32_16x16x32_bf16 v[130:133], v[184:187], v[204:207], v[130:133]
	v_mfma_f32_16x16x32_bf16 v[126:129], v[150:153], v[216:219], v[126:129]
	v_mfma_f32_16x16x32_bf16 v[122:125], v[184:187], v[216:219], v[122:125]
	v_mfma_f32_16x16x32_bf16 v[118:121], v[150:153], v[224:227], v[118:121]
	v_mfma_f32_16x16x32_bf16 v[114:117], v[184:187], v[224:227], v[114:117]
	s_barrier
	s_add_i32 s66, s57, s43
	v_lshl_add_u64 v[212:213], s[36:37], 0, v[156:157]
	s_mov_b32 m0, s66
	ds_read_b128 v[188:191], v199 offset:16384
	ds_read_b128 v[192:195], v199 offset:17408
	ds_read_b128 v[200:203], v199 offset:18432
	ds_read_b128 v[204:207], v199 offset:19456
	ds_read_b128 v[208:211], v199 offset:20480
	ds_read_b128 v[216:219], v199 offset:21504
	ds_read_b128 v[220:223], v199 offset:22528
	ds_read_b128 v[224:227], v199 offset:23552
	global_load_lds_dwordx4 v[212:213], off
	s_add_i32 m0, s66, 0x2000
	s_add_u32 s66, s36, 0x80000
	v_lshl_add_u64 v[214:215], s[36:37], 0, v[160:161]
	s_addc_u32 s67, s37, 0
	s_add_i32 s68, s58, s43
	global_load_lds_dwordx4 v[214:215], off
	v_lshl_add_u64 v[228:229], s[66:67], 0, v[156:157]
	s_mov_b32 m0, s68
	v_lshl_add_u64 v[230:231], s[38:39], 0, v[158:159]
	global_load_lds_dwordx4 v[228:229], off
	v_lshl_add_u64 v[228:229], s[66:67], 0, v[160:161]
	s_add_i32 m0, s68, 0x2000
	s_nop 0
	global_load_lds_dwordx4 v[228:229], off
	v_lshl_add_u64 v[228:229], s[38:39], 0, v[154:155]
	s_mov_b32 m0, s44
	s_nop 0
	global_load_lds_dwordx4 v[228:229], off
	s_mov_b32 m0, s45
	s_nop 0
	global_load_lds_dwordx4 v[230:231], off
	s_waitcnt vmcnt(8)
	s_waitcnt lgkmcnt(0)
	s_barrier
	v_mfma_f32_16x16x32_bf16 v[30:33], v[90:93], v[188:191], v[30:33]
	v_mfma_f32_16x16x32_bf16 v[26:29], v[98:101], v[188:191], v[26:29]
	v_mfma_f32_16x16x32_bf16 v[22:25], v[90:93], v[200:203], v[22:25]
	v_mfma_f32_16x16x32_bf16 v[18:21], v[98:101], v[200:203], v[18:21]
	v_mfma_f32_16x16x32_bf16 v[14:17], v[90:93], v[208:211], v[14:17]
	v_mfma_f32_16x16x32_bf16 v[10:13], v[98:101], v[208:211], v[10:13]
	v_mfma_f32_16x16x32_bf16 v[6:9], v[90:93], v[220:223], v[6:9]
	v_mfma_f32_16x16x32_bf16 v[2:5], v[98:101], v[220:223], v[2:5]
	v_mfma_f32_16x16x32_bf16 v[30:33], v[94:97], v[192:195], v[30:33]
	v_mfma_f32_16x16x32_bf16 v[26:29], v[102:105], v[192:195], v[26:29]
	v_mfma_f32_16x16x32_bf16 v[22:25], v[94:97], v[204:207], v[22:25]
	v_mfma_f32_16x16x32_bf16 v[18:21], v[102:105], v[204:207], v[18:21]
	v_mfma_f32_16x16x32_bf16 v[14:17], v[94:97], v[216:219], v[14:17]
	v_mfma_f32_16x16x32_bf16 v[10:13], v[102:105], v[216:219], v[10:13]
	v_mfma_f32_16x16x32_bf16 v[6:9], v[94:97], v[224:227], v[6:9]
	v_mfma_f32_16x16x32_bf16 v[2:5], v[102:105], v[224:227], v[2:5]
	v_mfma_f32_16x16x32_bf16 v[86:89], v[146:149], v[200:203], v[86:89]
	v_mfma_f32_16x16x32_bf16 v[82:85], v[180:183], v[200:203], v[82:85]
	v_mfma_f32_16x16x32_bf16 v[78:81], v[146:149], v[208:211], v[78:81]
	v_mfma_f32_16x16x32_bf16 v[74:77], v[180:183], v[208:211], v[74:77]
	v_mfma_f32_16x16x32_bf16 v[62:65], v[146:149], v[220:223], v[62:65]
	v_mfma_f32_16x16x32_bf16 v[58:61], v[180:183], v[220:223], v[58:61]
	v_mfma_f32_16x16x32_bf16 v[90:93], v[146:149], v[188:191], v[110:113]
	v_mfma_f32_16x16x32_bf16 v[94:97], v[180:183], v[188:191], v[106:109]
	v_mfma_f32_16x16x32_bf16 v[86:89], v[150:153], v[204:207], v[86:89]
	v_mfma_f32_16x16x32_bf16 v[82:85], v[184:187], v[204:207], v[82:85]
	v_mfma_f32_16x16x32_bf16 v[78:81], v[150:153], v[216:219], v[78:81]
	v_mfma_f32_16x16x32_bf16 v[74:77], v[184:187], v[216:219], v[74:77]
	v_mfma_f32_16x16x32_bf16 v[62:65], v[150:153], v[224:227], v[62:65]
	v_mfma_f32_16x16x32_bf16 v[58:61], v[184:187], v[224:227], v[58:61]
	v_mfma_f32_16x16x32_bf16 v[90:93], v[150:153], v[192:195], v[90:93]
	v_mfma_f32_16x16x32_bf16 v[94:97], v[184:187], v[192:195], v[94:97]
	s_barrier
	s_add_i32 s66, 0, 0x18000
	s_add_i32 s67, 0, 0x1c000
	v_add_u32_e32 v110, s66, v165
	v_add_u32_e32 v162, s67, v165
	ds_read_b128 v[98:101], v110
	ds_read_b128 v[102:105], v110 offset:1024
	ds_read_b128 v[106:109], v110 offset:2048
	ds_read_b128 v[110:113], v110 offset:3072
	ds_read_b128 v[146:149], v162
	ds_read_b128 v[150:153], v162 offset:1024
	ds_read_b128 v[180:183], v162 offset:2048
	ds_read_b128 v[184:187], v162 offset:3072
	s_add_u32 s38, s38, 0x80000
	s_addc_u32 s39, s39, 0
	s_mov_b32 m0, s47
	v_lshl_add_u64 v[232:233], s[38:39], 0, v[154:155]
	ds_read_b128 v[188:191], v199 offset:32768
	ds_read_b128 v[192:195], v199 offset:33792
	ds_read_b128 v[200:203], v199 offset:34816
	ds_read_b128 v[204:207], v199 offset:35840
	ds_read_b128 v[208:211], v199 offset:36864
	ds_read_b128 v[216:219], v199 offset:37888
	ds_read_b128 v[220:223], v199 offset:38912
	ds_read_b128 v[224:227], v199 offset:39936
	global_load_lds_dwordx4 v[232:233], off
	v_lshl_add_u64 v[232:233], s[38:39], 0, v[158:159]
	s_mov_b32 m0, s48
	s_nop 0
	global_load_lds_dwordx4 v[232:233], off
	s_waitcnt vmcnt(8)
	s_waitcnt lgkmcnt(0)
	s_barrier
	v_mfma_f32_16x16x32_bf16 v[70:73], v[98:101], v[188:191], v[70:73]
	v_mfma_f32_16x16x32_bf16 v[66:69], v[106:109], v[188:191], v[66:69]
	v_mfma_f32_16x16x32_bf16 v[54:57], v[98:101], v[200:203], v[54:57]
	v_mfma_f32_16x16x32_bf16 v[50:53], v[106:109], v[200:203], v[50:53]
	v_mfma_f32_16x16x32_bf16 v[46:49], v[98:101], v[208:211], v[46:49]
	v_mfma_f32_16x16x32_bf16 v[42:45], v[106:109], v[208:211], v[42:45]
	v_mfma_f32_16x16x32_bf16 v[38:41], v[98:101], v[220:223], v[38:41]
	v_mfma_f32_16x16x32_bf16 v[34:37], v[106:109], v[220:223], v[34:37]
	v_mfma_f32_16x16x32_bf16 v[70:73], v[102:105], v[192:195], v[70:73]
	v_mfma_f32_16x16x32_bf16 v[66:69], v[110:113], v[192:195], v[66:69]
	v_mfma_f32_16x16x32_bf16 v[54:57], v[102:105], v[204:207], v[54:57]
	v_mfma_f32_16x16x32_bf16 v[50:53], v[110:113], v[204:207], v[50:53]
	v_mfma_f32_16x16x32_bf16 v[46:49], v[102:105], v[216:219], v[46:49]
	v_mfma_f32_16x16x32_bf16 v[42:45], v[110:113], v[216:219], v[42:45]
	v_mfma_f32_16x16x32_bf16 v[38:41], v[102:105], v[224:227], v[38:41]
	v_mfma_f32_16x16x32_bf16 v[34:37], v[110:113], v[224:227], v[34:37]
	v_mfma_f32_16x16x32_bf16 v[142:145], v[146:149], v[188:191], v[142:145]
	v_mfma_f32_16x16x32_bf16 v[138:141], v[180:183], v[188:191], v[138:141]
	v_mfma_f32_16x16x32_bf16 v[134:137], v[146:149], v[200:203], v[134:137]
	v_mfma_f32_16x16x32_bf16 v[130:133], v[180:183], v[200:203], v[130:133]
	v_mfma_f32_16x16x32_bf16 v[126:129], v[146:149], v[208:211], v[126:129]
	v_mfma_f32_16x16x32_bf16 v[122:125], v[180:183], v[208:211], v[122:125]
	v_mfma_f32_16x16x32_bf16 v[118:121], v[146:149], v[220:223], v[118:121]
	v_mfma_f32_16x16x32_bf16 v[114:117], v[180:183], v[220:223], v[114:117]
	v_mfma_f32_16x16x32_bf16 v[142:145], v[150:153], v[192:195], v[142:145]
	v_mfma_f32_16x16x32_bf16 v[138:141], v[184:187], v[192:195], v[138:141]
	v_mfma_f32_16x16x32_bf16 v[134:137], v[150:153], v[204:207], v[134:137]
	v_mfma_f32_16x16x32_bf16 v[130:133], v[184:187], v[204:207], v[130:133]
	v_mfma_f32_16x16x32_bf16 v[126:129], v[150:153], v[216:219], v[126:129]
	v_mfma_f32_16x16x32_bf16 v[122:125], v[184:187], v[216:219], v[122:125]
	v_mfma_f32_16x16x32_bf16 v[118:121], v[150:153], v[224:227], v[118:121]
	v_mfma_f32_16x16x32_bf16 v[114:117], v[184:187], v[224:227], v[114:117]
	s_barrier
	s_add_i32 s38, s66, s43
	v_lshl_add_u64 v[212:213], v[212:213], 0, s[18:19]
	s_mov_b32 m0, s38
	ds_read_b128 v[188:191], v199 offset:49152
	ds_read_b128 v[192:195], v199 offset:50176
	ds_read_b128 v[200:203], v199 offset:51200
	ds_read_b128 v[204:207], v199 offset:52224
	ds_read_b128 v[208:211], v199 offset:53248
	ds_read_b128 v[216:219], v199 offset:54272
	ds_read_b128 v[220:223], v199 offset:55296
	ds_read_b128 v[224:227], v199 offset:56320
	global_load_lds_dwordx4 v[212:213], off
	s_add_i32 m0, s38, 0x2000
	s_add_u32 s36, s36, 0x80080
	v_lshl_add_u64 v[212:213], v[214:215], 0, s[18:19]
	s_addc_u32 s37, s37, 0
	s_add_i32 s38, s67, s43
	global_load_lds_dwordx4 v[212:213], off
	v_lshl_add_u64 v[212:213], s[36:37], 0, v[156:157]
	s_mov_b32 m0, s38
	s_nop 0
	global_load_lds_dwordx4 v[212:213], off
	v_lshl_add_u64 v[212:213], s[36:37], 0, v[160:161]
	s_add_i32 m0, s38, 0x2000
	s_nop 0
	global_load_lds_dwordx4 v[212:213], off
	v_lshl_add_u64 v[212:213], v[228:229], 0, s[18:19]
	s_mov_b32 m0, s52
	s_nop 0
	global_load_lds_dwordx4 v[212:213], off
	v_lshl_add_u64 v[212:213], v[230:231], 0, s[18:19]
	s_mov_b32 m0, s53
	s_nop 0
	global_load_lds_dwordx4 v[212:213], off
	s_waitcnt vmcnt(8)
	s_waitcnt lgkmcnt(0)
	s_barrier
	v_mfma_f32_16x16x32_bf16 v[30:33], v[98:101], v[188:191], v[30:33]
	v_mfma_f32_16x16x32_bf16 v[26:29], v[106:109], v[188:191], v[26:29]
	v_mfma_f32_16x16x32_bf16 v[22:25], v[98:101], v[200:203], v[22:25]
	v_mfma_f32_16x16x32_bf16 v[18:21], v[106:109], v[200:203], v[18:21]
	v_mfma_f32_16x16x32_bf16 v[14:17], v[98:101], v[208:211], v[14:17]
	v_mfma_f32_16x16x32_bf16 v[10:13], v[106:109], v[208:211], v[10:13]
	v_mfma_f32_16x16x32_bf16 v[6:9], v[98:101], v[220:223], v[6:9]
	v_mfma_f32_16x16x32_bf16 v[2:5], v[106:109], v[220:223], v[2:5]
	v_mfma_f32_16x16x32_bf16 v[30:33], v[102:105], v[192:195], v[30:33]
	v_mfma_f32_16x16x32_bf16 v[26:29], v[110:113], v[192:195], v[26:29]
	v_mfma_f32_16x16x32_bf16 v[22:25], v[102:105], v[204:207], v[22:25]
	v_mfma_f32_16x16x32_bf16 v[18:21], v[110:113], v[204:207], v[18:21]
	v_mfma_f32_16x16x32_bf16 v[14:17], v[102:105], v[216:219], v[14:17]
	v_mfma_f32_16x16x32_bf16 v[10:13], v[110:113], v[216:219], v[10:13]
	v_mfma_f32_16x16x32_bf16 v[6:9], v[102:105], v[224:227], v[6:9]
	v_mfma_f32_16x16x32_bf16 v[2:5], v[110:113], v[224:227], v[2:5]
	v_mfma_f32_16x16x32_bf16 v[90:93], v[146:149], v[188:191], v[90:93]
	v_mfma_f32_16x16x32_bf16 v[110:113], v[150:153], v[192:195], v[90:93]
	v_mfma_f32_16x16x32_bf16 v[90:93], v[180:183], v[188:191], v[94:97]
	v_mfma_f32_16x16x32_bf16 v[86:89], v[146:149], v[200:203], v[86:89]
	v_mfma_f32_16x16x32_bf16 v[82:85], v[180:183], v[200:203], v[82:85]
	v_mfma_f32_16x16x32_bf16 v[78:81], v[146:149], v[208:211], v[78:81]
	v_mfma_f32_16x16x32_bf16 v[74:77], v[180:183], v[208:211], v[74:77]
	v_mfma_f32_16x16x32_bf16 v[62:65], v[146:149], v[220:223], v[62:65]
	v_mfma_f32_16x16x32_bf16 v[58:61], v[180:183], v[220:223], v[58:61]
	v_mfma_f32_16x16x32_bf16 v[106:109], v[184:187], v[192:195], v[90:93]
	v_mfma_f32_16x16x32_bf16 v[86:89], v[150:153], v[204:207], v[86:89]
	v_mfma_f32_16x16x32_bf16 v[82:85], v[184:187], v[204:207], v[82:85]
	v_mfma_f32_16x16x32_bf16 v[78:81], v[150:153], v[216:219], v[78:81]
	v_mfma_f32_16x16x32_bf16 v[74:77], v[184:187], v[216:219], v[74:77]
	v_mfma_f32_16x16x32_bf16 v[62:65], v[150:153], v[224:227], v[62:65]
	v_mfma_f32_16x16x32_bf16 v[58:61], v[184:187], v[224:227], v[58:61]
	s_barrier
	s_add_i32 s65, s65, 2
	s_add_u32 s16, s16, 0x100
	s_addc_u32 s17, s17, 0
	s_add_u32 s41, s41, 0x100
	s_addc_u32 s64, s64, 0
	s_cmp_gt_u32 s65, 29
	s_cbranch_scc0 .LBB0_162
	s_and_b64 vcc, exec, s[20:21]
	s_cbranch_vccz .LBB0_165
	s_barrier

.LBB0_421:
	s_setprio 0
	s_mov_b64 s[30:31], s[8:9]
	v_readlane_b32 s8, v254, 1
	v_readlane_b32 s9, v254, 2
	s_mov_b32 s8, s99
	s_add_i32 s43, s43, 1
	s_mov_b64 s[0:1], s[10:11]
	s_mov_b32 s54, s36
	s_mov_b32 s53, s37
	s_waitcnt lgkmcnt(0)
	s_mul_i32 s10, s43, s8
	v_readlane_b32 s8, v254, 14
	s_add_i32 s10, s10, s8
	s_cmpk_lt_i32 s10, 0x100
	s_cselect_b64 s[34:35], -1, 0
	s_cmpk_gt_i32 s10, 0xff
	s_cselect_b64 s[28:29], -1, 0
	s_and_b64 vcc, exec, s[28:29]
	s_cbranch_vccnz .LBB0_427
	s_cmpk_gt_i32 s10, 0x7f
	s_mov_b64 s[8:9], -1
	s_cbranch_scc0 .LBB0_424
	s_add_i32 s36, s10, 0xffffff80
	s_add_i32 s24, s10, 0x158
	s_mov_b64 s[8:9], 0

.LBB0_427:
	s_ashr_i32 s25, s24, 31
	s_lshl_b64 s[8:9], s[24:25], 20
	s_add_u32 s10, s86, s8
	s_addc_u32 s11, s87, s9
	s_and_b64 s[8:9], s[34:35], exec
	s_cselect_b32 s25, s11, s1
	s_cselect_b32 s55, s10, s0
	s_ashr_i32 s27, s26, 31
	s_lshl_b64 s[8:9], s[26:27], 20
	s_add_u32 s8, s86, s8
	s_addc_u32 s9, s87, s9
	s_and_b64 s[34:35], s[34:35], exec
	s_cselect_b32 s27, s9, s31
	s_cselect_b32 s56, s8, s30
	s_add_u32 s0, s0, 0x80080
	s_addc_u32 s1, s1, 0
	s_add_u32 s57, s30, 0x100
	s_addc_u32 s58, s31, 0
	s_mov_b32 s59, -2
	ds_read_b128 v[150:153], v146
	ds_read_b128 v[154:157], v146 offset:1024
	ds_read_b128 v[158:161], v146 offset:2048
	ds_read_b128 v[162:165], v146 offset:3072
	ds_read_b128 v[166:169], v147
	ds_read_b128 v[170:173], v147 offset:1024
	ds_read_b128 v[174:177], v147 offset:2048
	ds_read_b128 v[178:181], v147 offset:3072
	s_add_u32 s30, s0, 0xfff80080
	s_addc_u32 s31, s1, -1
	s_cmp_eq_u32 s59, 28
	s_cselect_b32 s35, s25, s31
	s_cselect_b32 s34, s55, s30
	s_cselect_b32 s31, s27, s58
	s_cselect_b32 s30, s56, s57
	v_lshl_add_u64 v[142:143], s[0:1], 0, v[138:139]
	s_add_i32 m0, s39, 0xc000
	ds_read_b128 v[182:185], v148
	ds_read_b128 v[186:189], v148 offset:1024
	ds_read_b128 v[190:193], v148 offset:2048
	ds_read_b128 v[194:197], v148 offset:3072
	ds_read_b128 v[198:201], v148 offset:4096
	ds_read_b128 v[202:205], v148 offset:5120
	ds_read_b128 v[206:209], v148 offset:6144
	ds_read_b128 v[210:213], v148 offset:7168
	global_load_lds_dwordx4 v[142:143], off
	v_lshl_add_u64 v[142:143], s[0:1], 0, v[140:141]
	s_add_i32 m0, s39, 0xe000
	s_nop 0
	global_load_lds_dwordx4 v[142:143], off
	s_waitcnt vmcnt(8)
	s_waitcnt lgkmcnt(0)
	s_barrier
	v_mfma_f32_16x16x32_bf16 v[94:97], v[150:153], v[182:185], 0
	v_mfma_f32_16x16x32_bf16 v[86:89], v[158:161], v[182:185], 0
	v_mfma_f32_16x16x32_bf16 v[66:69], v[150:153], v[190:193], 0
	v_mfma_f32_16x16x32_bf16 v[50:53], v[158:161], v[190:193], 0
	v_mfma_f32_16x16x32_bf16 v[46:49], v[150:153], v[198:201], 0
	v_mfma_f32_16x16x32_bf16 v[42:45], v[158:161], v[198:201], 0
	v_mfma_f32_16x16x32_bf16 v[38:41], v[150:153], v[206:209], 0
	v_mfma_f32_16x16x32_bf16 v[34:37], v[158:161], v[206:209], 0
	v_mfma_f32_16x16x32_bf16 v[94:97], v[154:157], v[186:189], v[94:97]
	v_mfma_f32_16x16x32_bf16 v[86:89], v[162:165], v[186:189], v[86:89]
	v_mfma_f32_16x16x32_bf16 v[66:69], v[154:157], v[194:197], v[66:69]
	v_mfma_f32_16x16x32_bf16 v[50:53], v[162:165], v[194:197], v[50:53]
	v_mfma_f32_16x16x32_bf16 v[46:49], v[154:157], v[202:205], v[46:49]
	v_mfma_f32_16x16x32_bf16 v[42:45], v[162:165], v[202:205], v[42:45]
	v_mfma_f32_16x16x32_bf16 v[38:41], v[154:157], v[210:213], v[38:41]
	v_mfma_f32_16x16x32_bf16 v[34:37], v[162:165], v[210:213], v[34:37]
	v_mfma_f32_16x16x32_bf16 v[126:129], v[166:169], v[182:185], 0
	v_mfma_f32_16x16x32_bf16 v[122:125], v[174:177], v[182:185], 0
	v_mfma_f32_16x16x32_bf16 v[118:121], v[166:169], v[190:193], 0
	v_mfma_f32_16x16x32_bf16 v[114:117], v[174:177], v[190:193], 0
	v_mfma_f32_16x16x32_bf16 v[110:113], v[166:169], v[198:201], 0
	v_mfma_f32_16x16x32_bf16 v[106:109], v[174:177], v[198:201], 0
	v_mfma_f32_16x16x32_bf16 v[102:105], v[166:169], v[206:209], 0
	v_mfma_f32_16x16x32_bf16 v[98:101], v[174:177], v[206:209], 0
	v_mfma_f32_16x16x32_bf16 v[126:129], v[170:173], v[186:189], v[126:129]
	v_mfma_f32_16x16x32_bf16 v[122:125], v[178:181], v[186:189], v[122:125]
	v_mfma_f32_16x16x32_bf16 v[118:121], v[170:173], v[194:197], v[118:121]
	v_mfma_f32_16x16x32_bf16 v[114:117], v[178:181], v[194:197], v[114:117]
	v_mfma_f32_16x16x32_bf16 v[110:113], v[170:173], v[202:205], v[110:113]
	v_mfma_f32_16x16x32_bf16 v[106:109], v[178:181], v[202:205], v[106:109]
	v_mfma_f32_16x16x32_bf16 v[102:105], v[170:173], v[210:213], v[102:105]
	v_mfma_f32_16x16x32_bf16 v[98:101], v[178:181], v[210:213], v[98:101]
	s_barrier
	s_add_i32 s60, s47, s38
	v_lshl_add_u64 v[142:143], s[30:31], 0, v[130:131]
	s_mov_b32 m0, s60
	ds_read_b128 v[182:185], v148 offset:16384
	ds_read_b128 v[186:189], v148 offset:17408
	ds_read_b128 v[190:193], v148 offset:18432
	ds_read_b128 v[194:197], v148 offset:19456
	ds_read_b128 v[198:201], v148 offset:20480
	ds_read_b128 v[202:205], v148 offset:21504
	ds_read_b128 v[206:209], v148 offset:22528
	ds_read_b128 v[210:213], v148 offset:23552
	global_load_lds_dwordx4 v[142:143], off
	s_add_i32 m0, s60, 0x2000
	s_add_u32 s60, s30, 0x80000
	v_lshl_add_u64 v[214:215], s[30:31], 0, v[132:133]
	s_addc_u32 s61, s31, 0
	s_add_i32 s62, s48, s38
	global_load_lds_dwordx4 v[214:215], off
	v_lshl_add_u64 v[216:217], s[60:61], 0, v[130:131]
	s_mov_b32 m0, s62
	v_lshl_add_u64 v[218:219], s[34:35], 0, v[132:133]
	global_load_lds_dwordx4 v[216:217], off
	v_lshl_add_u64 v[216:217], s[60:61], 0, v[132:133]
	s_add_i32 m0, s62, 0x2000
	s_nop 0
	global_load_lds_dwordx4 v[216:217], off
	v_lshl_add_u64 v[216:217], s[34:35], 0, v[130:131]
	s_mov_b32 m0, s39
	s_nop 0
	global_load_lds_dwordx4 v[216:217], off
	s_mov_b32 m0, s40
	s_nop 0
	global_load_lds_dwordx4 v[218:219], off
	s_waitcnt vmcnt(8)
	s_waitcnt lgkmcnt(0)
	s_barrier
	v_mfma_f32_16x16x32_bf16 v[30:33], v[150:153], v[182:185], 0
	v_mfma_f32_16x16x32_bf16 v[26:29], v[158:161], v[182:185], 0
	v_mfma_f32_16x16x32_bf16 v[22:25], v[150:153], v[190:193], 0
	v_mfma_f32_16x16x32_bf16 v[18:21], v[158:161], v[190:193], 0
	v_mfma_f32_16x16x32_bf16 v[14:17], v[150:153], v[198:201], 0
	v_mfma_f32_16x16x32_bf16 v[10:13], v[158:161], v[198:201], 0
	v_mfma_f32_16x16x32_bf16 v[6:9], v[150:153], v[206:209], 0
	v_mfma_f32_16x16x32_bf16 v[2:5], v[158:161], v[206:209], 0
	v_mfma_f32_16x16x32_bf16 v[30:33], v[154:157], v[186:189], v[30:33]
	v_mfma_f32_16x16x32_bf16 v[26:29], v[162:165], v[186:189], v[26:29]
	v_mfma_f32_16x16x32_bf16 v[22:25], v[154:157], v[194:197], v[22:25]
	v_mfma_f32_16x16x32_bf16 v[18:21], v[162:165], v[194:197], v[18:21]
	v_mfma_f32_16x16x32_bf16 v[14:17], v[154:157], v[202:205], v[14:17]
	v_mfma_f32_16x16x32_bf16 v[10:13], v[162:165], v[202:205], v[10:13]
	v_mfma_f32_16x16x32_bf16 v[6:9], v[154:157], v[210:213], v[6:9]
	v_mfma_f32_16x16x32_bf16 v[2:5], v[162:165], v[210:213], v[2:5]
	v_mfma_f32_16x16x32_bf16 v[90:93], v[166:169], v[182:185], 0
	v_mfma_f32_16x16x32_bf16 v[82:85], v[174:177], v[182:185], 0
	v_mfma_f32_16x16x32_bf16 v[78:81], v[166:169], v[190:193], 0
	v_mfma_f32_16x16x32_bf16 v[74:77], v[174:177], v[190:193], 0
	v_mfma_f32_16x16x32_bf16 v[70:73], v[166:169], v[198:201], 0
	v_mfma_f32_16x16x32_bf16 v[62:65], v[174:177], v[198:201], 0
	v_mfma_f32_16x16x32_bf16 v[58:61], v[166:169], v[206:209], 0
	v_mfma_f32_16x16x32_bf16 v[54:57], v[174:177], v[206:209], 0
	v_mfma_f32_16x16x32_bf16 v[90:93], v[170:173], v[186:189], v[90:93]
	v_mfma_f32_16x16x32_bf16 v[82:85], v[178:181], v[186:189], v[82:85]
	v_mfma_f32_16x16x32_bf16 v[78:81], v[170:173], v[194:197], v[78:81]
	v_mfma_f32_16x16x32_bf16 v[74:77], v[178:181], v[194:197], v[74:77]
	v_mfma_f32_16x16x32_bf16 v[70:73], v[170:173], v[202:205], v[70:73]
	v_mfma_f32_16x16x32_bf16 v[62:65], v[178:181], v[202:205], v[62:65]
	v_mfma_f32_16x16x32_bf16 v[58:61], v[170:173], v[210:213], v[58:61]
	v_mfma_f32_16x16x32_bf16 v[54:57], v[178:181], v[210:213], v[54:57]
	s_barrier
	s_add_i32 s60, 0, 0x18000
	v_add_u32_e32 v134, s60, v144
	s_add_i32 s61, 0, 0x1c000
	ds_read_b128 v[150:153], v134
	ds_read_b128 v[154:157], v134 offset:1024
	ds_read_b128 v[158:161], v134 offset:2048
	ds_read_b128 v[162:165], v134 offset:3072
	v_add_u32_e32 v134, s61, v144
	ds_read_b128 v[166:169], v134
	ds_read_b128 v[170:173], v134 offset:1024
	ds_read_b128 v[174:177], v134 offset:2048
	ds_read_b128 v[178:181], v134 offset:3072
	s_add_u32 s34, s34, 0x80000
	s_addc_u32 s35, s35, 0
	s_mov_b32 m0, s41
	v_lshl_add_u64 v[220:221], s[34:35], 0, v[130:131]
	ds_read_b128 v[182:185], v148 offset:32768
	ds_read_b128 v[186:189], v148 offset:33792
	ds_read_b128 v[190:193], v148 offset:34816
	ds_read_b128 v[194:197], v148 offset:35840
	ds_read_b128 v[198:201], v148 offset:36864
	ds_read_b128 v[202:205], v148 offset:37888
	ds_read_b128 v[206:209], v148 offset:38912
	ds_read_b128 v[210:213], v148 offset:39936
	global_load_lds_dwordx4 v[220:221], off
	v_lshl_add_u64 v[220:221], s[34:35], 0, v[132:133]
	s_mov_b32 m0, s42
	s_nop 0
	global_load_lds_dwordx4 v[220:221], off
	s_waitcnt vmcnt(8)
	s_waitcnt lgkmcnt(0)
	s_barrier
	v_mfma_f32_16x16x32_bf16 v[94:97], v[150:153], v[182:185], v[94:97]
	v_mfma_f32_16x16x32_bf16 v[86:89], v[158:161], v[182:185], v[86:89]
	v_mfma_f32_16x16x32_bf16 v[66:69], v[150:153], v[190:193], v[66:69]
	v_mfma_f32_16x16x32_bf16 v[50:53], v[158:161], v[190:193], v[50:53]
	v_mfma_f32_16x16x32_bf16 v[46:49], v[150:153], v[198:201], v[46:49]
	v_mfma_f32_16x16x32_bf16 v[42:45], v[158:161], v[198:201], v[42:45]
	v_mfma_f32_16x16x32_bf16 v[38:41], v[150:153], v[206:209], v[38:41]
	v_mfma_f32_16x16x32_bf16 v[34:37], v[158:161], v[206:209], v[34:37]
	v_mfma_f32_16x16x32_bf16 v[94:97], v[154:157], v[186:189], v[94:97]
	v_mfma_f32_16x16x32_bf16 v[86:89], v[162:165], v[186:189], v[86:89]
	v_mfma_f32_16x16x32_bf16 v[66:69], v[154:157], v[194:197], v[66:69]
	v_mfma_f32_16x16x32_bf16 v[50:53], v[162:165], v[194:197], v[50:53]
	v_mfma_f32_16x16x32_bf16 v[46:49], v[154:157], v[202:205], v[46:49]
	v_mfma_f32_16x16x32_bf16 v[42:45], v[162:165], v[202:205], v[42:45]
	v_mfma_f32_16x16x32_bf16 v[38:41], v[154:157], v[210:213], v[38:41]
	v_mfma_f32_16x16x32_bf16 v[34:37], v[162:165], v[210:213], v[34:37]
	v_mfma_f32_16x16x32_bf16 v[126:129], v[166:169], v[182:185], v[126:129]
	v_mfma_f32_16x16x32_bf16 v[122:125], v[174:177], v[182:185], v[122:125]
	v_mfma_f32_16x16x32_bf16 v[118:121], v[166:169], v[190:193], v[118:121]
	v_mfma_f32_16x16x32_bf16 v[114:117], v[174:177], v[190:193], v[114:117]
	v_mfma_f32_16x16x32_bf16 v[110:113], v[166:169], v[198:201], v[110:113]
	v_mfma_f32_16x16x32_bf16 v[106:109], v[174:177], v[198:201], v[106:109]
	v_mfma_f32_16x16x32_bf16 v[102:105], v[166:169], v[206:209], v[102:105]
	v_mfma_f32_16x16x32_bf16 v[98:101], v[174:177], v[206:209], v[98:101]
	v_mfma_f32_16x16x32_bf16 v[126:129], v[170:173], v[186:189], v[126:129]
	v_mfma_f32_16x16x32_bf16 v[122:125], v[178:181], v[186:189], v[122:125]
	v_mfma_f32_16x16x32_bf16 v[118:121], v[170:173], v[194:197], v[118:121]
	v_mfma_f32_16x16x32_bf16 v[114:117], v[178:181], v[194:197], v[114:117]
	v_mfma_f32_16x16x32_bf16 v[110:113], v[170:173], v[202:205], v[110:113]
	v_mfma_f32_16x16x32_bf16 v[106:109], v[178:181], v[202:205], v[106:109]
	v_mfma_f32_16x16x32_bf16 v[102:105], v[170:173], v[210:213], v[102:105]
	v_mfma_f32_16x16x32_bf16 v[98:101], v[178:181], v[210:213], v[98:101]
	s_barrier
	s_add_i32 s34, s60, s38
	v_lshl_add_u64 v[142:143], v[142:143], 0, s[6:7]
	s_mov_b32 m0, s34
	ds_read_b128 v[182:185], v148 offset:49152
	ds_read_b128 v[186:189], v148 offset:50176
	ds_read_b128 v[190:193], v148 offset:51200
	ds_read_b128 v[194:197], v148 offset:52224
	ds_read_b128 v[198:201], v148 offset:53248
	ds_read_b128 v[202:205], v148 offset:54272
	ds_read_b128 v[206:209], v148 offset:55296
	ds_read_b128 v[210:213], v148 offset:56320
	global_load_lds_dwordx4 v[142:143], off
	s_add_i32 m0, s34, 0x2000
	s_add_u32 s30, s30, 0x80080
	v_lshl_add_u64 v[142:143], v[214:215], 0, s[6:7]
	s_addc_u32 s31, s31, 0
	s_add_i32 s34, s61, s38
	global_load_lds_dwordx4 v[142:143], off
	v_lshl_add_u64 v[142:143], s[30:31], 0, v[130:131]
	s_mov_b32 m0, s34
	s_nop 0
	global_load_lds_dwordx4 v[142:143], off
	v_lshl_add_u64 v[142:143], s[30:31], 0, v[132:133]
	s_add_i32 m0, s34, 0x2000
	s_nop 0
	global_load_lds_dwordx4 v[142:143], off
	v_lshl_add_u64 v[142:143], v[216:217], 0, s[6:7]
	s_mov_b32 m0, s44
	s_nop 0
	global_load_lds_dwordx4 v[142:143], off
	v_lshl_add_u64 v[142:143], v[218:219], 0, s[6:7]
	s_mov_b32 m0, s45
	s_nop 0
	global_load_lds_dwordx4 v[142:143], off
	s_waitcnt vmcnt(8)
	s_waitcnt lgkmcnt(0)
	s_barrier
	v_mfma_f32_16x16x32_bf16 v[30:33], v[150:153], v[182:185], v[30:33]
	v_mfma_f32_16x16x32_bf16 v[26:29], v[158:161], v[182:185], v[26:29]
	v_mfma_f32_16x16x32_bf16 v[22:25], v[150:153], v[190:193], v[22:25]
	v_mfma_f32_16x16x32_bf16 v[18:21], v[158:161], v[190:193], v[18:21]
	v_mfma_f32_16x16x32_bf16 v[14:17], v[150:153], v[198:201], v[14:17]
	v_mfma_f32_16x16x32_bf16 v[10:13], v[158:161], v[198:201], v[10:13]
	v_mfma_f32_16x16x32_bf16 v[6:9], v[150:153], v[206:209], v[6:9]
	v_mfma_f32_16x16x32_bf16 v[2:5], v[158:161], v[206:209], v[2:5]
	v_mfma_f32_16x16x32_bf16 v[30:33], v[154:157], v[186:189], v[30:33]
	v_mfma_f32_16x16x32_bf16 v[26:29], v[162:165], v[186:189], v[26:29]
	v_mfma_f32_16x16x32_bf16 v[22:25], v[154:157], v[194:197], v[22:25]
	v_mfma_f32_16x16x32_bf16 v[18:21], v[162:165], v[194:197], v[18:21]
	v_mfma_f32_16x16x32_bf16 v[14:17], v[154:157], v[202:205], v[14:17]
	v_mfma_f32_16x16x32_bf16 v[10:13], v[162:165], v[202:205], v[10:13]
	v_mfma_f32_16x16x32_bf16 v[6:9], v[154:157], v[210:213], v[6:9]
	v_mfma_f32_16x16x32_bf16 v[2:5], v[162:165], v[210:213], v[2:5]
	v_mfma_f32_16x16x32_bf16 v[90:93], v[166:169], v[182:185], v[90:93]
	v_mfma_f32_16x16x32_bf16 v[82:85], v[174:177], v[182:185], v[82:85]
	v_mfma_f32_16x16x32_bf16 v[78:81], v[166:169], v[190:193], v[78:81]
	v_mfma_f32_16x16x32_bf16 v[74:77], v[174:177], v[190:193], v[74:77]
	v_mfma_f32_16x16x32_bf16 v[70:73], v[166:169], v[198:201], v[70:73]
	v_mfma_f32_16x16x32_bf16 v[62:65], v[174:177], v[198:201], v[62:65]
	v_mfma_f32_16x16x32_bf16 v[58:61], v[166:169], v[206:209], v[58:61]
	v_mfma_f32_16x16x32_bf16 v[54:57], v[174:177], v[206:209], v[54:57]
	v_mfma_f32_16x16x32_bf16 v[90:93], v[170:173], v[186:189], v[90:93]
	v_mfma_f32_16x16x32_bf16 v[82:85], v[178:181], v[186:189], v[82:85]
	v_mfma_f32_16x16x32_bf16 v[78:81], v[170:173], v[194:197], v[78:81]
	v_mfma_f32_16x16x32_bf16 v[74:77], v[178:181], v[194:197], v[74:77]
	v_mfma_f32_16x16x32_bf16 v[70:73], v[170:173], v[202:205], v[70:73]
	v_mfma_f32_16x16x32_bf16 v[62:65], v[178:181], v[202:205], v[62:65]
	v_mfma_f32_16x16x32_bf16 v[58:61], v[170:173], v[210:213], v[58:61]
	v_mfma_f32_16x16x32_bf16 v[54:57], v[178:181], v[210:213], v[54:57]
	s_barrier
	s_add_i32 s59, s59, 2
	s_add_u32 s0, s0, 0x100
	s_addc_u32 s1, s1, 0
	s_add_u32 s57, s57, 0x100
	s_addc_u32 s58, s58, 0
	s_cmp_gt_u32 s59, 29
.LBB0_428:
	ds_read_b128 v[150:153], v146
	ds_read_b128 v[154:157], v146 offset:1024
	ds_read_b128 v[158:161], v146 offset:2048
	ds_read_b128 v[162:165], v146 offset:3072
	ds_read_b128 v[166:169], v147
	ds_read_b128 v[170:173], v147 offset:1024
	ds_read_b128 v[174:177], v147 offset:2048
	ds_read_b128 v[178:181], v147 offset:3072
	s_add_u32 s30, s0, 0xfff80080
	s_addc_u32 s31, s1, -1
	s_cmp_eq_u32 s59, 28
	s_cselect_b32 s35, s25, s31
	s_cselect_b32 s34, s55, s30
	s_cselect_b32 s31, s27, s58
	s_cselect_b32 s30, s56, s57
	v_lshl_add_u64 v[142:143], s[0:1], 0, v[138:139]
	s_add_i32 m0, s39, 0xc000
	ds_read_b128 v[182:185], v148
	ds_read_b128 v[186:189], v148 offset:1024
	ds_read_b128 v[190:193], v148 offset:2048
	ds_read_b128 v[194:197], v148 offset:3072
	ds_read_b128 v[198:201], v148 offset:4096
	ds_read_b128 v[202:205], v148 offset:5120
	ds_read_b128 v[206:209], v148 offset:6144
	ds_read_b128 v[210:213], v148 offset:7168
	global_load_lds_dwordx4 v[142:143], off
	v_lshl_add_u64 v[142:143], s[0:1], 0, v[140:141]
	s_add_i32 m0, s39, 0xe000
	s_nop 0
	global_load_lds_dwordx4 v[142:143], off
	s_waitcnt vmcnt(8)
	s_waitcnt lgkmcnt(0)
	s_barrier
	v_mfma_f32_16x16x32_bf16 v[94:97], v[150:153], v[182:185], v[94:97]
	v_mfma_f32_16x16x32_bf16 v[86:89], v[158:161], v[182:185], v[86:89]
	v_mfma_f32_16x16x32_bf16 v[66:69], v[150:153], v[190:193], v[66:69]
	v_mfma_f32_16x16x32_bf16 v[50:53], v[158:161], v[190:193], v[50:53]
	v_mfma_f32_16x16x32_bf16 v[46:49], v[150:153], v[198:201], v[46:49]
	v_mfma_f32_16x16x32_bf16 v[42:45], v[158:161], v[198:201], v[42:45]
	v_mfma_f32_16x16x32_bf16 v[38:41], v[150:153], v[206:209], v[38:41]
	v_mfma_f32_16x16x32_bf16 v[34:37], v[158:161], v[206:209], v[34:37]
	v_mfma_f32_16x16x32_bf16 v[94:97], v[154:157], v[186:189], v[94:97]
	v_mfma_f32_16x16x32_bf16 v[86:89], v[162:165], v[186:189], v[86:89]
	v_mfma_f32_16x16x32_bf16 v[66:69], v[154:157], v[194:197], v[66:69]
	v_mfma_f32_16x16x32_bf16 v[50:53], v[162:165], v[194:197], v[50:53]
	v_mfma_f32_16x16x32_bf16 v[46:49], v[154:157], v[202:205], v[46:49]
	v_mfma_f32_16x16x32_bf16 v[42:45], v[162:165], v[202:205], v[42:45]
	v_mfma_f32_16x16x32_bf16 v[38:41], v[154:157], v[210:213], v[38:41]
	v_mfma_f32_16x16x32_bf16 v[34:37], v[162:165], v[210:213], v[34:37]
	v_mfma_f32_16x16x32_bf16 v[126:129], v[166:169], v[182:185], v[126:129]
	v_mfma_f32_16x16x32_bf16 v[122:125], v[174:177], v[182:185], v[122:125]
	v_mfma_f32_16x16x32_bf16 v[118:121], v[166:169], v[190:193], v[118:121]
	v_mfma_f32_16x16x32_bf16 v[114:117], v[174:177], v[190:193], v[114:117]
	v_mfma_f32_16x16x32_bf16 v[110:113], v[166:169], v[198:201], v[110:113]
	v_mfma_f32_16x16x32_bf16 v[106:109], v[174:177], v[198:201], v[106:109]
	v_mfma_f32_16x16x32_bf16 v[102:105], v[166:169], v[206:209], v[102:105]
	v_mfma_f32_16x16x32_bf16 v[98:101], v[174:177], v[206:209], v[98:101]
	v_mfma_f32_16x16x32_bf16 v[126:129], v[170:173], v[186:189], v[126:129]
	v_mfma_f32_16x16x32_bf16 v[122:125], v[178:181], v[186:189], v[122:125]
	v_mfma_f32_16x16x32_bf16 v[118:121], v[170:173], v[194:197], v[118:121]
	v_mfma_f32_16x16x32_bf16 v[114:117], v[178:181], v[194:197], v[114:117]
	v_mfma_f32_16x16x32_bf16 v[110:113], v[170:173], v[202:205], v[110:113]
	v_mfma_f32_16x16x32_bf16 v[106:109], v[178:181], v[202:205], v[106:109]
	v_mfma_f32_16x16x32_bf16 v[102:105], v[170:173], v[210:213], v[102:105]
	v_mfma_f32_16x16x32_bf16 v[98:101], v[178:181], v[210:213], v[98:101]
	s_barrier
	s_add_i32 s60, s47, s38
	v_lshl_add_u64 v[142:143], s[30:31], 0, v[130:131]
	s_mov_b32 m0, s60
	ds_read_b128 v[182:185], v148 offset:16384
	ds_read_b128 v[186:189], v148 offset:17408
	ds_read_b128 v[190:193], v148 offset:18432
	ds_read_b128 v[194:197], v148 offset:19456
	ds_read_b128 v[198:201], v148 offset:20480
	ds_read_b128 v[202:205], v148 offset:21504
	ds_read_b128 v[206:209], v148 offset:22528
	ds_read_b128 v[210:213], v148 offset:23552
	global_load_lds_dwordx4 v[142:143], off
	s_add_i32 m0, s60, 0x2000
	s_add_u32 s60, s30, 0x80000
	v_lshl_add_u64 v[214:215], s[30:31], 0, v[132:133]
	s_addc_u32 s61, s31, 0
	s_add_i32 s62, s48, s38
	global_load_lds_dwordx4 v[214:215], off
	v_lshl_add_u64 v[216:217], s[60:61], 0, v[130:131]
	s_mov_b32 m0, s62
	v_lshl_add_u64 v[218:219], s[34:35], 0, v[132:133]
	global_load_lds_dwordx4 v[216:217], off
	v_lshl_add_u64 v[216:217], s[60:61], 0, v[132:133]
	s_add_i32 m0, s62, 0x2000
	s_nop 0
	global_load_lds_dwordx4 v[216:217], off
	v_lshl_add_u64 v[216:217], s[34:35], 0, v[130:131]
	s_mov_b32 m0, s39
	s_nop 0
	global_load_lds_dwordx4 v[216:217], off
	s_mov_b32 m0, s40
	s_nop 0
	global_load_lds_dwordx4 v[218:219], off
	s_waitcnt vmcnt(8)
	s_waitcnt lgkmcnt(0)
	s_barrier
	v_mfma_f32_16x16x32_bf16 v[30:33], v[150:153], v[182:185], v[30:33]
	v_mfma_f32_16x16x32_bf16 v[26:29], v[158:161], v[182:185], v[26:29]
	v_mfma_f32_16x16x32_bf16 v[22:25], v[150:153], v[190:193], v[22:25]
	v_mfma_f32_16x16x32_bf16 v[18:21], v[158:161], v[190:193], v[18:21]
	v_mfma_f32_16x16x32_bf16 v[14:17], v[150:153], v[198:201], v[14:17]
	v_mfma_f32_16x16x32_bf16 v[10:13], v[158:161], v[198:201], v[10:13]
	v_mfma_f32_16x16x32_bf16 v[6:9], v[150:153], v[206:209], v[6:9]
	v_mfma_f32_16x16x32_bf16 v[2:5], v[158:161], v[206:209], v[2:5]
	v_mfma_f32_16x16x32_bf16 v[30:33], v[154:157], v[186:189], v[30:33]
	v_mfma_f32_16x16x32_bf16 v[26:29], v[162:165], v[186:189], v[26:29]
	v_mfma_f32_16x16x32_bf16 v[22:25], v[154:157], v[194:197], v[22:25]
	v_mfma_f32_16x16x32_bf16 v[18:21], v[162:165], v[194:197], v[18:21]
	v_mfma_f32_16x16x32_bf16 v[14:17], v[154:157], v[202:205], v[14:17]
	v_mfma_f32_16x16x32_bf16 v[10:13], v[162:165], v[202:205], v[10:13]
	v_mfma_f32_16x16x32_bf16 v[6:9], v[154:157], v[210:213], v[6:9]
	v_mfma_f32_16x16x32_bf16 v[2:5], v[162:165], v[210:213], v[2:5]
	v_mfma_f32_16x16x32_bf16 v[90:93], v[166:169], v[182:185], v[90:93]
	v_mfma_f32_16x16x32_bf16 v[82:85], v[174:177], v[182:185], v[82:85]
	v_mfma_f32_16x16x32_bf16 v[78:81], v[166:169], v[190:193], v[78:81]
	v_mfma_f32_16x16x32_bf16 v[74:77], v[174:177], v[190:193], v[74:77]
	v_mfma_f32_16x16x32_bf16 v[70:73], v[166:169], v[198:201], v[70:73]
	v_mfma_f32_16x16x32_bf16 v[62:65], v[174:177], v[198:201], v[62:65]
	v_mfma_f32_16x16x32_bf16 v[58:61], v[166:169], v[206:209], v[58:61]
	v_mfma_f32_16x16x32_bf16 v[54:57], v[174:177], v[206:209], v[54:57]
	v_mfma_f32_16x16x32_bf16 v[90:93], v[170:173], v[186:189], v[90:93]
	v_mfma_f32_16x16x32_bf16 v[82:85], v[178:181], v[186:189], v[82:85]
	v_mfma_f32_16x16x32_bf16 v[78:81], v[170:173], v[194:197], v[78:81]
	v_mfma_f32_16x16x32_bf16 v[74:77], v[178:181], v[194:197], v[74:77]
	v_mfma_f32_16x16x32_bf16 v[70:73], v[170:173], v[202:205], v[70:73]
	v_mfma_f32_16x16x32_bf16 v[62:65], v[178:181], v[202:205], v[62:65]
	v_mfma_f32_16x16x32_bf16 v[58:61], v[170:173], v[210:213], v[58:61]
	v_mfma_f32_16x16x32_bf16 v[54:57], v[178:181], v[210:213], v[54:57]
	s_barrier
	s_add_i32 s60, 0, 0x18000
	v_add_u32_e32 v134, s60, v144
	s_add_i32 s61, 0, 0x1c000
	ds_read_b128 v[150:153], v134
	ds_read_b128 v[154:157], v134 offset:1024
	ds_read_b128 v[158:161], v134 offset:2048
	ds_read_b128 v[162:165], v134 offset:3072
	v_add_u32_e32 v134, s61, v144
	ds_read_b128 v[166:169], v134
	ds_read_b128 v[170:173], v134 offset:1024
	ds_read_b128 v[174:177], v134 offset:2048
	ds_read_b128 v[178:181], v134 offset:3072
	s_add_u32 s34, s34, 0x80000
	s_addc_u32 s35, s35, 0
	s_mov_b32 m0, s41
	v_lshl_add_u64 v[220:221], s[34:35], 0, v[130:131]
	ds_read_b128 v[182:185], v148 offset:32768
	ds_read_b128 v[186:189], v148 offset:33792
	ds_read_b128 v[190:193], v148 offset:34816
	ds_read_b128 v[194:197], v148 offset:35840
	ds_read_b128 v[198:201], v148 offset:36864
	ds_read_b128 v[202:205], v148 offset:37888
	ds_read_b128 v[206:209], v148 offset:38912
	ds_read_b128 v[210:213], v148 offset:39936
	global_load_lds_dwordx4 v[220:221], off
	v_lshl_add_u64 v[220:221], s[34:35], 0, v[132:133]
	s_mov_b32 m0, s42
	s_nop 0
	global_load_lds_dwordx4 v[220:221], off
	s_waitcnt vmcnt(8)
	s_waitcnt lgkmcnt(0)
	s_barrier
	v_mfma_f32_16x16x32_bf16 v[94:97], v[150:153], v[182:185], v[94:97]
	v_mfma_f32_16x16x32_bf16 v[86:89], v[158:161], v[182:185], v[86:89]
	v_mfma_f32_16x16x32_bf16 v[66:69], v[150:153], v[190:193], v[66:69]
	v_mfma_f32_16x16x32_bf16 v[50:53], v[158:161], v[190:193], v[50:53]
	v_mfma_f32_16x16x32_bf16 v[46:49], v[150:153], v[198:201], v[46:49]
	v_mfma_f32_16x16x32_bf16 v[42:45], v[158:161], v[198:201], v[42:45]
	v_mfma_f32_16x16x32_bf16 v[38:41], v[150:153], v[206:209], v[38:41]
	v_mfma_f32_16x16x32_bf16 v[34:37], v[158:161], v[206:209], v[34:37]
	v_mfma_f32_16x16x32_bf16 v[94:97], v[154:157], v[186:189], v[94:97]
	v_mfma_f32_16x16x32_bf16 v[86:89], v[162:165], v[186:189], v[86:89]
	v_mfma_f32_16x16x32_bf16 v[66:69], v[154:157], v[194:197], v[66:69]
	v_mfma_f32_16x16x32_bf16 v[50:53], v[162:165], v[194:197], v[50:53]
	v_mfma_f32_16x16x32_bf16 v[46:49], v[154:157], v[202:205], v[46:49]
	v_mfma_f32_16x16x32_bf16 v[42:45], v[162:165], v[202:205], v[42:45]
	v_mfma_f32_16x16x32_bf16 v[38:41], v[154:157], v[210:213], v[38:41]
	v_mfma_f32_16x16x32_bf16 v[34:37], v[162:165], v[210:213], v[34:37]
	v_mfma_f32_16x16x32_bf16 v[126:129], v[166:169], v[182:185], v[126:129]
	v_mfma_f32_16x16x32_bf16 v[122:125], v[174:177], v[182:185], v[122:125]
	v_mfma_f32_16x16x32_bf16 v[118:121], v[166:169], v[190:193], v[118:121]
	v_mfma_f32_16x16x32_bf16 v[114:117], v[174:177], v[190:193], v[114:117]
	v_mfma_f32_16x16x32_bf16 v[110:113], v[166:169], v[198:201], v[110:113]
	v_mfma_f32_16x16x32_bf16 v[106:109], v[174:177], v[198:201], v[106:109]
	v_mfma_f32_16x16x32_bf16 v[102:105], v[166:169], v[206:209], v[102:105]
	v_mfma_f32_16x16x32_bf16 v[98:101], v[174:177], v[206:209], v[98:101]
	v_mfma_f32_16x16x32_bf16 v[126:129], v[170:173], v[186:189], v[126:129]
	v_mfma_f32_16x16x32_bf16 v[122:125], v[178:181], v[186:189], v[122:125]
	v_mfma_f32_16x16x32_bf16 v[118:121], v[170:173], v[194:197], v[118:121]
	v_mfma_f32_16x16x32_bf16 v[114:117], v[178:181], v[194:197], v[114:117]
	v_mfma_f32_16x16x32_bf16 v[110:113], v[170:173], v[202:205], v[110:113]
	v_mfma_f32_16x16x32_bf16 v[106:109], v[178:181], v[202:205], v[106:109]
	v_mfma_f32_16x16x32_bf16 v[102:105], v[170:173], v[210:213], v[102:105]
	v_mfma_f32_16x16x32_bf16 v[98:101], v[178:181], v[210:213], v[98:101]
	s_barrier
	s_add_i32 s34, s60, s38
	v_lshl_add_u64 v[142:143], v[142:143], 0, s[6:7]
	s_mov_b32 m0, s34
	ds_read_b128 v[182:185], v148 offset:49152
	ds_read_b128 v[186:189], v148 offset:50176
	ds_read_b128 v[190:193], v148 offset:51200
	ds_read_b128 v[194:197], v148 offset:52224
	ds_read_b128 v[198:201], v148 offset:53248
	ds_read_b128 v[202:205], v148 offset:54272
	ds_read_b128 v[206:209], v148 offset:55296
	ds_read_b128 v[210:213], v148 offset:56320
	global_load_lds_dwordx4 v[142:143], off
	s_add_i32 m0, s34, 0x2000
	s_add_u32 s30, s30, 0x80080
	v_lshl_add_u64 v[142:143], v[214:215], 0, s[6:7]
	s_addc_u32 s31, s31, 0
	s_add_i32 s34, s61, s38
	global_load_lds_dwordx4 v[142:143], off
	v_lshl_add_u64 v[142:143], s[30:31], 0, v[130:131]
	s_mov_b32 m0, s34
	s_nop 0
	global_load_lds_dwordx4 v[142:143], off
	v_lshl_add_u64 v[142:143], s[30:31], 0, v[132:133]
	s_add_i32 m0, s34, 0x2000
	s_nop 0
	global_load_lds_dwordx4 v[142:143], off
	v_lshl_add_u64 v[142:143], v[216:217], 0, s[6:7]
	s_mov_b32 m0, s44
	s_nop 0
	global_load_lds_dwordx4 v[142:143], off
	v_lshl_add_u64 v[142:143], v[218:219], 0, s[6:7]
	s_mov_b32 m0, s45
	s_nop 0
	global_load_lds_dwordx4 v[142:143], off
	s_waitcnt vmcnt(8)
	s_waitcnt lgkmcnt(0)
	s_barrier
	v_mfma_f32_16x16x32_bf16 v[30:33], v[150:153], v[182:185], v[30:33]
	v_mfma_f32_16x16x32_bf16 v[26:29], v[158:161], v[182:185], v[26:29]
	v_mfma_f32_16x16x32_bf16 v[22:25], v[150:153], v[190:193], v[22:25]
	v_mfma_f32_16x16x32_bf16 v[18:21], v[158:161], v[190:193], v[18:21]
	v_mfma_f32_16x16x32_bf16 v[14:17], v[150:153], v[198:201], v[14:17]
	v_mfma_f32_16x16x32_bf16 v[10:13], v[158:161], v[198:201], v[10:13]
	v_mfma_f32_16x16x32_bf16 v[6:9], v[150:153], v[206:209], v[6:9]
	v_mfma_f32_16x16x32_bf16 v[2:5], v[158:161], v[206:209], v[2:5]
	v_mfma_f32_16x16x32_bf16 v[30:33], v[154:157], v[186:189], v[30:33]
	v_mfma_f32_16x16x32_bf16 v[26:29], v[162:165], v[186:189], v[26:29]
	v_mfma_f32_16x16x32_bf16 v[22:25], v[154:157], v[194:197], v[22:25]
	v_mfma_f32_16x16x32_bf16 v[18:21], v[162:165], v[194:197], v[18:21]
	v_mfma_f32_16x16x32_bf16 v[14:17], v[154:157], v[202:205], v[14:17]
	v_mfma_f32_16x16x32_bf16 v[10:13], v[162:165], v[202:205], v[10:13]
	v_mfma_f32_16x16x32_bf16 v[6:9], v[154:157], v[210:213], v[6:9]
	v_mfma_f32_16x16x32_bf16 v[2:5], v[162:165], v[210:213], v[2:5]
	v_mfma_f32_16x16x32_bf16 v[90:93], v[166:169], v[182:185], v[90:93]
	v_mfma_f32_16x16x32_bf16 v[82:85], v[174:177], v[182:185], v[82:85]
	v_mfma_f32_16x16x32_bf16 v[78:81], v[166:169], v[190:193], v[78:81]
	v_mfma_f32_16x16x32_bf16 v[74:77], v[174:177], v[190:193], v[74:77]
	v_mfma_f32_16x16x32_bf16 v[70:73], v[166:169], v[198:201], v[70:73]
	v_mfma_f32_16x16x32_bf16 v[62:65], v[174:177], v[198:201], v[62:65]
	v_mfma_f32_16x16x32_bf16 v[58:61], v[166:169], v[206:209], v[58:61]
	v_mfma_f32_16x16x32_bf16 v[54:57], v[174:177], v[206:209], v[54:57]
	v_mfma_f32_16x16x32_bf16 v[90:93], v[170:173], v[186:189], v[90:93]
	v_mfma_f32_16x16x32_bf16 v[82:85], v[178:181], v[186:189], v[82:85]
	v_mfma_f32_16x16x32_bf16 v[78:81], v[170:173], v[194:197], v[78:81]
	v_mfma_f32_16x16x32_bf16 v[74:77], v[178:181], v[194:197], v[74:77]
	v_mfma_f32_16x16x32_bf16 v[70:73], v[170:173], v[202:205], v[70:73]
	v_mfma_f32_16x16x32_bf16 v[62:65], v[178:181], v[202:205], v[62:65]
	v_mfma_f32_16x16x32_bf16 v[58:61], v[170:173], v[210:213], v[58:61]
	v_mfma_f32_16x16x32_bf16 v[54:57], v[178:181], v[210:213], v[54:57]
	s_barrier
	s_add_i32 s59, s59, 2
	s_add_u32 s0, s0, 0x100
	s_addc_u32 s1, s1, 0
	s_add_u32 s57, s57, 0x100
	s_addc_u32 s58, s58, 0
	s_cmp_gt_u32 s59, 29
	s_cbranch_scc0 .LBB0_428
	v_lshl_add_u32 v142, s54, 8, v1
	s_cmp_lt_i32 s53, 8
	s_mov_b64 s[0:1], -1
	s_cbranch_scc0 .LBB0_431
	s_lshl_b32 s0, s53, 8
	s_and_b32 s0, s0, 0x100
	v_ashrrev_i32_e32 v143, 31, v142
	v_or_b32_e32 v134, s0, v145
	v_lshlrev_b64 v[150:151], 11, v[142:143]
	v_lshl_add_u64 v[150:151], s[4:5], 0, v[150:151]
	v_lshlrev_b32_e32 v134, 2, v134
	v_lshl_add_u64 v[150:151], v[150:151], 0, v[134:135]
	global_store_dwordx4 v[150:151], v[94:97], off
	global_store_dwordx4 v[150:151], v[86:89], off offset:64
	global_store_dwordx4 v[150:151], v[126:129], off offset:512
	global_store_dwordx4 v[150:151], v[122:125], off offset:576
	s_mov_b64 s[0:1], 0
	s_nop 0
	v_or_b32_e32 v122, 16, v142
	v_ashrrev_i32_e32 v123, 31, v122
	v_lshlrev_b64 v[122:123], 11, v[122:123]
	v_lshl_add_u64 v[122:123], s[4:5], 0, v[122:123]
	v_lshl_add_u64 v[122:123], v[122:123], 0, v[134:135]
	global_store_dwordx4 v[122:123], v[66:69], off
	global_store_dwordx4 v[122:123], v[50:53], off offset:64
	global_store_dwordx4 v[122:123], v[118:121], off offset:512
	global_store_dwordx4 v[122:123], v[114:117], off offset:576
	s_nop 1
	v_or_b32_e32 v114, 32, v142
	v_ashrrev_i32_e32 v115, 31, v114
	v_lshlrev_b64 v[114:115], 11, v[114:115]
	v_lshl_add_u64 v[114:115], s[4:5], 0, v[114:115]
	v_lshl_add_u64 v[114:115], v[114:115], 0, v[134:135]
	global_store_dwordx4 v[114:115], v[46:49], off
	global_store_dwordx4 v[114:115], v[42:45], off offset:64
	global_store_dwordx4 v[114:115], v[110:113], off offset:512
	global_store_dwordx4 v[114:115], v[106:109], off offset:576
	s_nop 1
	v_or_b32_e32 v106, 48, v142
	v_ashrrev_i32_e32 v107, 31, v106
	v_lshlrev_b64 v[106:107], 11, v[106:107]
	v_lshl_add_u64 v[106:107], s[4:5], 0, v[106:107]
	v_lshl_add_u64 v[106:107], v[106:107], 0, v[134:135]
	global_store_dwordx4 v[106:107], v[38:41], off
	global_store_dwordx4 v[106:107], v[34:37], off offset:64
	global_store_dwordx4 v[106:107], v[102:105], off offset:512
	global_store_dwordx4 v[106:107], v[98:101], off offset:576
	s_nop 1
	v_add_co_u32_e32 v100, vcc, s49, v150
	v_lshl_add_u64 v[98:99], v[150:151], 0, s[16:17]
	s_nop 0
	v_addc_co_u32_e32 v101, vcc, 0, v151, vcc
	global_store_dwordx4 v[100:101], v[30:33], off
	global_store_dwordx4 v[98:99], v[26:29], off offset:64
	global_store_dwordx4 v[98:99], v[90:93], off offset:512
	global_store_dwordx4 v[98:99], v[82:85], off offset:576
	s_nop 1
	v_add_co_u32_e32 v84, vcc, s50, v150
	v_lshl_add_u64 v[82:83], v[150:151], 0, s[18:19]
	s_nop 0
	v_addc_co_u32_e32 v85, vcc, 0, v151, vcc
	global_store_dwordx4 v[84:85], v[22:25], off
	global_store_dwordx4 v[82:83], v[18:21], off offset:64
	global_store_dwordx4 v[82:83], v[78:81], off offset:512
	global_store_dwordx4 v[82:83], v[74:77], off offset:576
	s_nop 1
	v_add_co_u32_e32 v76, vcc, s51, v150
	v_lshl_add_u64 v[74:75], v[150:151], 0, s[20:21]
	s_nop 0
	v_addc_co_u32_e32 v77, vcc, 0, v151, vcc
	global_store_dwordx4 v[76:77], v[14:17], off
	global_store_dwordx4 v[74:75], v[10:13], off offset:64
	global_store_dwordx4 v[74:75], v[70:73], off offset:512
	global_store_dwordx4 v[74:75], v[62:65], off offset:576
	s_nop 1
	v_add_co_u32_e32 v64, vcc, 0x58000, v150
	v_lshl_add_u64 v[62:63], v[150:151], 0, s[22:23]
	s_nop 0
	v_addc_co_u32_e32 v65, vcc, 0, v151, vcc
	global_store_dwordx4 v[64:65], v[6:9], off
	global_store_dwordx4 v[62:63], v[2:5], off offset:64
	global_store_dwordx4 v[62:63], v[58:61], off offset:512
	global_store_dwordx4 v[62:63], v[54:57], off offset:576

.LBB0_1339:
	s_setprio 0
	v_readlane_b32 s24, v254, 1
	v_readlane_b32 s25, v254, 2
	s_mov_b32 s21, s99
	s_add_i32 s44, s44, 1
	s_mul_i32 s8, s44, s47
	s_waitcnt lgkmcnt(0)
	s_mul_hi_u32 s9, s44, s21
	s_add_i32 s9, s9, s8
	s_mul_i32 s8, s44, s21
	v_readlane_b32 s21, v254, 14
	s_add_u32 s24, s8, s21
	s_addc_u32 s25, s9, s33
	v_cmp_gt_i64_e32 vcc, s[24:25], v[144:145]
	v_cmp_lt_i64_e64 s[8:9], s[24:25], v[142:143]
	s_cbranch_vccnz .LBB0_1345
	s_ashr_i32 s20, s24, 31
	s_lshr_b32 s20, s20, 29
	s_add_i32 s22, s24, s20
	s_and_b32 s20, s22, -8
	s_sub_i32 s23, s24, s20
	s_cmp_gt_i32 s23, -1
	s_mov_b64 s[20:21], -1
	s_cbranch_scc0 .LBB0_1342
	s_lshl_b32 s24, s23, 7
	s_mov_b64 s[20:21], 0

.Lrx_1346_0:
	s_waitcnt vmcnt(24)
	s_waitcnt lgkmcnt(0)
	s_barrier
	v_mfma_f32_16x16x32_bf16 v[126:129], v[154:157], v[186:189], 0
	v_mfma_f32_16x16x32_bf16 v[122:125], v[162:165], v[186:189], 0
	v_mfma_f32_16x16x32_bf16 v[118:121], v[154:157], v[194:197], 0
	v_mfma_f32_16x16x32_bf16 v[110:113], v[162:165], v[194:197], 0
	v_mfma_f32_16x16x32_bf16 v[102:105], v[154:157], v[202:205], 0
	v_mfma_f32_16x16x32_bf16 v[94:97], v[162:165], v[202:205], 0
	v_mfma_f32_16x16x32_bf16 v[86:89], v[154:157], v[210:213], 0
	v_mfma_f32_16x16x32_bf16 v[78:81], v[162:165], v[210:213], 0
	v_mfma_f32_16x16x32_bf16 v[126:129], v[158:161], v[190:193], v[126:129]
	v_mfma_f32_16x16x32_bf16 v[122:125], v[166:169], v[190:193], v[122:125]
	v_mfma_f32_16x16x32_bf16 v[118:121], v[158:161], v[198:201], v[118:121]
	v_mfma_f32_16x16x32_bf16 v[110:113], v[166:169], v[198:201], v[110:113]
	v_mfma_f32_16x16x32_bf16 v[102:105], v[158:161], v[206:209], v[102:105]
	v_mfma_f32_16x16x32_bf16 v[94:97], v[166:169], v[206:209], v[94:97]
	v_mfma_f32_16x16x32_bf16 v[86:89], v[158:161], v[214:217], v[86:89]
	v_mfma_f32_16x16x32_bf16 v[78:81], v[166:169], v[214:217], v[78:81]
	v_mfma_f32_16x16x32_bf16 v[114:117], v[170:173], v[186:189], 0
	v_mfma_f32_16x16x32_bf16 v[106:109], v[178:181], v[186:189], 0
	v_mfma_f32_16x16x32_bf16 v[98:101], v[170:173], v[194:197], 0
	v_mfma_f32_16x16x32_bf16 v[90:93], v[178:181], v[194:197], 0
	v_mfma_f32_16x16x32_bf16 v[82:85], v[170:173], v[202:205], 0
	v_mfma_f32_16x16x32_bf16 v[74:77], v[178:181], v[202:205], 0
	v_mfma_f32_16x16x32_bf16 v[70:73], v[170:173], v[210:213], 0
	v_mfma_f32_16x16x32_bf16 v[66:69], v[178:181], v[210:213], 0
	v_mfma_f32_16x16x32_bf16 v[114:117], v[174:177], v[190:193], v[114:117]
	v_mfma_f32_16x16x32_bf16 v[106:109], v[182:185], v[190:193], v[106:109]
	v_mfma_f32_16x16x32_bf16 v[98:101], v[174:177], v[198:201], v[98:101]
	v_mfma_f32_16x16x32_bf16 v[90:93], v[182:185], v[198:201], v[90:93]
	v_mfma_f32_16x16x32_bf16 v[82:85], v[174:177], v[206:209], v[82:85]
	v_mfma_f32_16x16x32_bf16 v[74:77], v[182:185], v[206:209], v[74:77]
	v_mfma_f32_16x16x32_bf16 v[70:73], v[174:177], v[214:217], v[70:73]
	v_mfma_f32_16x16x32_bf16 v[66:69], v[182:185], v[214:217], v[66:69]
	s_barrier
	s_add_i32 s60, s48, s40
	v_lshl_add_u64 v[146:147], s[34:35], 0, v[132:133]
	s_mov_b32 m0, s60
	ds_read_b128 v[186:189], v152 offset:16384
	ds_read_b128 v[190:193], v152 offset:17408
	ds_read_b128 v[194:197], v152 offset:18432
	ds_read_b128 v[198:201], v152 offset:19456
	ds_read_b128 v[202:205], v152 offset:20480
	ds_read_b128 v[206:209], v152 offset:21504
	ds_read_b128 v[210:213], v152 offset:22528
	ds_read_b128 v[214:217], v152 offset:23552
	global_load_lds_dwordx4 v[146:147], off
	s_add_i32 m0, s60, 0x2000
	s_add_u32 s60, s34, 0x80000
	v_lshl_add_u64 v[218:219], s[34:35], 0, v[136:137]
	s_addc_u32 s61, s35, 0
	s_add_i32 s62, s49, s40
	global_load_lds_dwordx4 v[218:219], off
	v_lshl_add_u64 v[220:221], s[60:61], 0, v[132:133]
	s_mov_b32 m0, s62
	v_lshl_add_u64 v[222:223], s[36:37], 0, v[134:135]
	global_load_lds_dwordx4 v[220:221], off
	v_lshl_add_u64 v[220:221], s[60:61], 0, v[136:137]
	s_add_i32 m0, s62, 0x2000
	s_nop 0
	global_load_lds_dwordx4 v[220:221], off
	v_lshl_add_u64 v[220:221], s[36:37], 0, v[130:131]
	s_mov_b32 m0, s29
	s_nop 0
	global_load_lds_dwordx4 v[220:221], off
	s_mov_b32 m0, s41
	s_nop 0
	global_load_lds_dwordx4 v[222:223], off
	s_cmp_lg_u32 s100, 0
	s_cbranch_scc1 .Lrx_1346_1
	s_waitcnt vmcnt(8)
.Lrx_1346_1:
	s_waitcnt vmcnt(24)
	s_mov_b32 s100, 1
	s_waitcnt lgkmcnt(0)
	s_barrier
	v_mfma_f32_16x16x32_bf16 v[62:65], v[154:157], v[186:189], 0
	v_mfma_f32_16x16x32_bf16 v[58:61], v[162:165], v[186:189], 0
	v_mfma_f32_16x16x32_bf16 v[54:57], v[154:157], v[194:197], 0
	v_mfma_f32_16x16x32_bf16 v[46:49], v[162:165], v[194:197], 0
	v_mfma_f32_16x16x32_bf16 v[38:41], v[154:157], v[202:205], 0
	v_mfma_f32_16x16x32_bf16 v[30:33], v[162:165], v[202:205], 0
	v_mfma_f32_16x16x32_bf16 v[22:25], v[154:157], v[210:213], 0
	v_mfma_f32_16x16x32_bf16 v[14:17], v[162:165], v[210:213], 0
	v_mfma_f32_16x16x32_bf16 v[62:65], v[158:161], v[190:193], v[62:65]
	v_mfma_f32_16x16x32_bf16 v[58:61], v[166:169], v[190:193], v[58:61]
	v_mfma_f32_16x16x32_bf16 v[54:57], v[158:161], v[198:201], v[54:57]
	v_mfma_f32_16x16x32_bf16 v[46:49], v[166:169], v[198:201], v[46:49]
	v_mfma_f32_16x16x32_bf16 v[38:41], v[158:161], v[206:209], v[38:41]
	v_mfma_f32_16x16x32_bf16 v[30:33], v[166:169], v[206:209], v[30:33]
	v_mfma_f32_16x16x32_bf16 v[22:25], v[158:161], v[214:217], v[22:25]
	v_mfma_f32_16x16x32_bf16 v[14:17], v[166:169], v[214:217], v[14:17]
	v_mfma_f32_16x16x32_bf16 v[50:53], v[170:173], v[186:189], 0
	v_mfma_f32_16x16x32_bf16 v[42:45], v[178:181], v[186:189], 0
	v_mfma_f32_16x16x32_bf16 v[34:37], v[170:173], v[194:197], 0
	v_mfma_f32_16x16x32_bf16 v[26:29], v[178:181], v[194:197], 0
	v_mfma_f32_16x16x32_bf16 v[18:21], v[170:173], v[202:205], 0
	v_mfma_f32_16x16x32_bf16 v[10:13], v[178:181], v[202:205], 0
	v_mfma_f32_16x16x32_bf16 v[6:9], v[170:173], v[210:213], 0
	v_mfma_f32_16x16x32_bf16 v[2:5], v[178:181], v[210:213], 0
	v_mfma_f32_16x16x32_bf16 v[50:53], v[174:177], v[190:193], v[50:53]
	v_mfma_f32_16x16x32_bf16 v[42:45], v[182:185], v[190:193], v[42:45]
	v_mfma_f32_16x16x32_bf16 v[34:37], v[174:177], v[198:201], v[34:37]
	v_mfma_f32_16x16x32_bf16 v[26:29], v[182:185], v[198:201], v[26:29]
	v_mfma_f32_16x16x32_bf16 v[18:21], v[174:177], v[206:209], v[18:21]
	v_mfma_f32_16x16x32_bf16 v[10:13], v[182:185], v[206:209], v[10:13]
	v_mfma_f32_16x16x32_bf16 v[6:9], v[174:177], v[214:217], v[6:9]
	v_mfma_f32_16x16x32_bf16 v[2:5], v[182:185], v[214:217], v[2:5]
	s_barrier
	s_add_i32 s60, 0, 0x18000
	v_add_u32_e32 v153, s60, v148
	s_add_i32 s61, 0, 0x1c000
	ds_read_b128 v[154:157], v153
	ds_read_b128 v[158:161], v153 offset:1024
	ds_read_b128 v[162:165], v153 offset:2048
	ds_read_b128 v[166:169], v153 offset:3072
	v_add_u32_e32 v153, s61, v148
	ds_read_b128 v[170:173], v153
	ds_read_b128 v[174:177], v153 offset:1024
	ds_read_b128 v[178:181], v153 offset:2048
	ds_read_b128 v[182:185], v153 offset:3072
	s_add_u32 s36, s36, 0x80000
	s_addc_u32 s37, s37, 0
	s_mov_b32 m0, s42
	v_lshl_add_u64 v[224:225], s[36:37], 0, v[130:131]
	ds_read_b128 v[186:189], v152 offset:32768
	ds_read_b128 v[190:193], v152 offset:33792
	ds_read_b128 v[194:197], v152 offset:34816
	ds_read_b128 v[198:201], v152 offset:35840
	ds_read_b128 v[202:205], v152 offset:36864
	ds_read_b128 v[206:209], v152 offset:37888
	ds_read_b128 v[210:213], v152 offset:38912
	ds_read_b128 v[214:217], v152 offset:39936
	global_load_lds_dwordx4 v[224:225], off
	v_lshl_add_u64 v[224:225], s[36:37], 0, v[134:135]
	s_mov_b32 m0, s43
	s_nop 0
	global_load_lds_dwordx4 v[224:225], off
	s_waitcnt vmcnt(8)
	s_waitcnt lgkmcnt(0)
	s_barrier
	v_mfma_f32_16x16x32_bf16 v[126:129], v[154:157], v[186:189], v[126:129]
	v_mfma_f32_16x16x32_bf16 v[122:125], v[162:165], v[186:189], v[122:125]
	v_mfma_f32_16x16x32_bf16 v[118:121], v[154:157], v[194:197], v[118:121]
	v_mfma_f32_16x16x32_bf16 v[110:113], v[162:165], v[194:197], v[110:113]
	v_mfma_f32_16x16x32_bf16 v[102:105], v[154:157], v[202:205], v[102:105]
	v_mfma_f32_16x16x32_bf16 v[94:97], v[162:165], v[202:205], v[94:97]
	v_mfma_f32_16x16x32_bf16 v[86:89], v[154:157], v[210:213], v[86:89]
	v_mfma_f32_16x16x32_bf16 v[78:81], v[162:165], v[210:213], v[78:81]
	v_mfma_f32_16x16x32_bf16 v[126:129], v[158:161], v[190:193], v[126:129]
	v_mfma_f32_16x16x32_bf16 v[122:125], v[166:169], v[190:193], v[122:125]
	v_mfma_f32_16x16x32_bf16 v[118:121], v[158:161], v[198:201], v[118:121]
	v_mfma_f32_16x16x32_bf16 v[110:113], v[166:169], v[198:201], v[110:113]
	v_mfma_f32_16x16x32_bf16 v[102:105], v[158:161], v[206:209], v[102:105]
	v_mfma_f32_16x16x32_bf16 v[94:97], v[166:169], v[206:209], v[94:97]
	v_mfma_f32_16x16x32_bf16 v[86:89], v[158:161], v[214:217], v[86:89]
	v_mfma_f32_16x16x32_bf16 v[78:81], v[166:169], v[214:217], v[78:81]
	v_mfma_f32_16x16x32_bf16 v[114:117], v[170:173], v[186:189], v[114:117]
	v_mfma_f32_16x16x32_bf16 v[106:109], v[178:181], v[186:189], v[106:109]
	v_mfma_f32_16x16x32_bf16 v[98:101], v[170:173], v[194:197], v[98:101]
	v_mfma_f32_16x16x32_bf16 v[90:93], v[178:181], v[194:197], v[90:93]
	v_mfma_f32_16x16x32_bf16 v[82:85], v[170:173], v[202:205], v[82:85]
	v_mfma_f32_16x16x32_bf16 v[74:77], v[178:181], v[202:205], v[74:77]
	v_mfma_f32_16x16x32_bf16 v[70:73], v[170:173], v[210:213], v[70:73]
	v_mfma_f32_16x16x32_bf16 v[66:69], v[178:181], v[210:213], v[66:69]
	v_mfma_f32_16x16x32_bf16 v[114:117], v[174:177], v[190:193], v[114:117]
	v_mfma_f32_16x16x32_bf16 v[106:109], v[182:185], v[190:193], v[106:109]
	v_mfma_f32_16x16x32_bf16 v[98:101], v[174:177], v[198:201], v[98:101]
	v_mfma_f32_16x16x32_bf16 v[90:93], v[182:185], v[198:201], v[90:93]
	v_mfma_f32_16x16x32_bf16 v[82:85], v[174:177], v[206:209], v[82:85]
	v_mfma_f32_16x16x32_bf16 v[74:77], v[182:185], v[206:209], v[74:77]
	v_mfma_f32_16x16x32_bf16 v[70:73], v[174:177], v[214:217], v[70:73]
	v_mfma_f32_16x16x32_bf16 v[66:69], v[182:185], v[214:217], v[66:69]
	s_barrier
	s_add_i32 s36, s60, s40
	v_lshl_add_u64 v[146:147], v[146:147], 0, s[10:11]
	s_mov_b32 m0, s36
	ds_read_b128 v[186:189], v152 offset:49152
	ds_read_b128 v[190:193], v152 offset:50176
	ds_read_b128 v[194:197], v152 offset:51200
	ds_read_b128 v[198:201], v152 offset:52224
	ds_read_b128 v[202:205], v152 offset:53248
	ds_read_b128 v[206:209], v152 offset:54272
	ds_read_b128 v[210:213], v152 offset:55296
	ds_read_b128 v[214:217], v152 offset:56320
	global_load_lds_dwordx4 v[146:147], off
	s_add_i32 m0, s36, 0x2000
	s_add_u32 s34, s34, 0x80080
	v_lshl_add_u64 v[146:147], v[218:219], 0, s[10:11]
	s_addc_u32 s35, s35, 0
	s_add_i32 s36, s61, s40
	global_load_lds_dwordx4 v[146:147], off
	v_lshl_add_u64 v[146:147], s[34:35], 0, v[132:133]
	s_mov_b32 m0, s36
	s_nop 0
	global_load_lds_dwordx4 v[146:147], off
	v_lshl_add_u64 v[146:147], s[34:35], 0, v[136:137]
	s_add_i32 m0, s36, 0x2000
	s_nop 0
	global_load_lds_dwordx4 v[146:147], off
	v_lshl_add_u64 v[146:147], v[220:221], 0, s[10:11]
	s_mov_b32 m0, s45
	s_nop 0
	global_load_lds_dwordx4 v[146:147], off
	v_lshl_add_u64 v[146:147], v[222:223], 0, s[10:11]
	s_mov_b32 m0, s46
	s_nop 0
	global_load_lds_dwordx4 v[146:147], off
	s_waitcnt vmcnt(8)
	s_waitcnt lgkmcnt(0)
	s_barrier
	v_mfma_f32_16x16x32_bf16 v[62:65], v[154:157], v[186:189], v[62:65]
	v_mfma_f32_16x16x32_bf16 v[58:61], v[162:165], v[186:189], v[58:61]
	v_mfma_f32_16x16x32_bf16 v[54:57], v[154:157], v[194:197], v[54:57]
	v_mfma_f32_16x16x32_bf16 v[46:49], v[162:165], v[194:197], v[46:49]
	v_mfma_f32_16x16x32_bf16 v[38:41], v[154:157], v[202:205], v[38:41]
	v_mfma_f32_16x16x32_bf16 v[30:33], v[162:165], v[202:205], v[30:33]
	v_mfma_f32_16x16x32_bf16 v[22:25], v[154:157], v[210:213], v[22:25]
	v_mfma_f32_16x16x32_bf16 v[14:17], v[162:165], v[210:213], v[14:17]
	v_mfma_f32_16x16x32_bf16 v[62:65], v[158:161], v[190:193], v[62:65]
	v_mfma_f32_16x16x32_bf16 v[58:61], v[166:169], v[190:193], v[58:61]
	v_mfma_f32_16x16x32_bf16 v[54:57], v[158:161], v[198:201], v[54:57]
	v_mfma_f32_16x16x32_bf16 v[46:49], v[166:169], v[198:201], v[46:49]
	v_mfma_f32_16x16x32_bf16 v[38:41], v[158:161], v[206:209], v[38:41]
	v_mfma_f32_16x16x32_bf16 v[30:33], v[166:169], v[206:209], v[30:33]
	v_mfma_f32_16x16x32_bf16 v[22:25], v[158:161], v[214:217], v[22:25]
	v_mfma_f32_16x16x32_bf16 v[14:17], v[166:169], v[214:217], v[14:17]
	v_mfma_f32_16x16x32_bf16 v[50:53], v[170:173], v[186:189], v[50:53]
	v_mfma_f32_16x16x32_bf16 v[42:45], v[178:181], v[186:189], v[42:45]
	v_mfma_f32_16x16x32_bf16 v[34:37], v[170:173], v[194:197], v[34:37]
	v_mfma_f32_16x16x32_bf16 v[26:29], v[178:181], v[194:197], v[26:29]
	v_mfma_f32_16x16x32_bf16 v[18:21], v[170:173], v[202:205], v[18:21]
	v_mfma_f32_16x16x32_bf16 v[10:13], v[178:181], v[202:205], v[10:13]
	v_mfma_f32_16x16x32_bf16 v[6:9], v[170:173], v[210:213], v[6:9]
	v_mfma_f32_16x16x32_bf16 v[2:5], v[178:181], v[210:213], v[2:5]
	v_mfma_f32_16x16x32_bf16 v[50:53], v[174:177], v[190:193], v[50:53]
	v_mfma_f32_16x16x32_bf16 v[42:45], v[182:185], v[190:193], v[42:45]
	v_mfma_f32_16x16x32_bf16 v[34:37], v[174:177], v[198:201], v[34:37]
	v_mfma_f32_16x16x32_bf16 v[26:29], v[182:185], v[198:201], v[26:29]
	v_mfma_f32_16x16x32_bf16 v[18:21], v[174:177], v[206:209], v[18:21]
	v_mfma_f32_16x16x32_bf16 v[10:13], v[182:185], v[206:209], v[10:13]
	v_mfma_f32_16x16x32_bf16 v[6:9], v[174:177], v[214:217], v[6:9]
	v_mfma_f32_16x16x32_bf16 v[2:5], v[182:185], v[214:217], v[2:5]
	s_barrier
	s_add_i32 s59, s59, 2
	s_add_u32 s30, s30, 0x100
	s_addc_u32 s31, s31, 0
	s_add_u32 s57, s57, 0x100
	s_addc_u32 s58, s58, 0
	s_cmp_gt_u32 s59, 29
.LBB0_1346:
	ds_read_b128 v[154:157], v150
	ds_read_b128 v[158:161], v150 offset:1024
	ds_read_b128 v[162:165], v150 offset:2048
	ds_read_b128 v[166:169], v150 offset:3072
	ds_read_b128 v[170:173], v151
	ds_read_b128 v[174:177], v151 offset:1024
	ds_read_b128 v[178:181], v151 offset:2048
	ds_read_b128 v[182:185], v151 offset:3072
	s_add_u32 s34, s30, 0xfff80080
	s_addc_u32 s35, s31, -1
	s_cmp_eq_u32 s59, 28
	s_cselect_b32 s37, s23, s35
	s_cselect_b32 s36, s55, s34
	s_cselect_b32 s35, s21, s58
	s_cselect_b32 s34, s56, s57
	v_lshl_add_u64 v[146:147], s[30:31], 0, v[138:139]
	s_add_i32 m0, s29, 0xc000
	ds_read_b128 v[186:189], v152
	ds_read_b128 v[190:193], v152 offset:1024
	ds_read_b128 v[194:197], v152 offset:2048
	ds_read_b128 v[198:201], v152 offset:3072
	ds_read_b128 v[202:205], v152 offset:4096
	ds_read_b128 v[206:209], v152 offset:5120
	ds_read_b128 v[210:213], v152 offset:6144
	ds_read_b128 v[214:217], v152 offset:7168
	global_load_lds_dwordx4 v[146:147], off
	v_lshl_add_u64 v[146:147], s[30:31], 0, v[140:141]
	s_add_i32 m0, s29, 0xe000
	s_nop 0
	global_load_lds_dwordx4 v[146:147], off
	s_waitcnt vmcnt(8)
	s_waitcnt lgkmcnt(0)
	s_barrier
	v_mfma_f32_16x16x32_bf16 v[126:129], v[154:157], v[186:189], v[126:129]
	v_mfma_f32_16x16x32_bf16 v[122:125], v[162:165], v[186:189], v[122:125]
	v_mfma_f32_16x16x32_bf16 v[118:121], v[154:157], v[194:197], v[118:121]
	v_mfma_f32_16x16x32_bf16 v[110:113], v[162:165], v[194:197], v[110:113]
	v_mfma_f32_16x16x32_bf16 v[102:105], v[154:157], v[202:205], v[102:105]
	v_mfma_f32_16x16x32_bf16 v[94:97], v[162:165], v[202:205], v[94:97]
	v_mfma_f32_16x16x32_bf16 v[86:89], v[154:157], v[210:213], v[86:89]
	v_mfma_f32_16x16x32_bf16 v[78:81], v[162:165], v[210:213], v[78:81]
	v_mfma_f32_16x16x32_bf16 v[126:129], v[158:161], v[190:193], v[126:129]
	v_mfma_f32_16x16x32_bf16 v[122:125], v[166:169], v[190:193], v[122:125]
	v_mfma_f32_16x16x32_bf16 v[118:121], v[158:161], v[198:201], v[118:121]
	v_mfma_f32_16x16x32_bf16 v[110:113], v[166:169], v[198:201], v[110:113]
	v_mfma_f32_16x16x32_bf16 v[102:105], v[158:161], v[206:209], v[102:105]
	v_mfma_f32_16x16x32_bf16 v[94:97], v[166:169], v[206:209], v[94:97]
	v_mfma_f32_16x16x32_bf16 v[86:89], v[158:161], v[214:217], v[86:89]
	v_mfma_f32_16x16x32_bf16 v[78:81], v[166:169], v[214:217], v[78:81]
	v_mfma_f32_16x16x32_bf16 v[114:117], v[170:173], v[186:189], v[114:117]
	v_mfma_f32_16x16x32_bf16 v[106:109], v[178:181], v[186:189], v[106:109]
	v_mfma_f32_16x16x32_bf16 v[98:101], v[170:173], v[194:197], v[98:101]
	v_mfma_f32_16x16x32_bf16 v[90:93], v[178:181], v[194:197], v[90:93]
	v_mfma_f32_16x16x32_bf16 v[82:85], v[170:173], v[202:205], v[82:85]
	v_mfma_f32_16x16x32_bf16 v[74:77], v[178:181], v[202:205], v[74:77]
	v_mfma_f32_16x16x32_bf16 v[70:73], v[170:173], v[210:213], v[70:73]
	v_mfma_f32_16x16x32_bf16 v[66:69], v[178:181], v[210:213], v[66:69]
	v_mfma_f32_16x16x32_bf16 v[114:117], v[174:177], v[190:193], v[114:117]
	v_mfma_f32_16x16x32_bf16 v[106:109], v[182:185], v[190:193], v[106:109]
	v_mfma_f32_16x16x32_bf16 v[98:101], v[174:177], v[198:201], v[98:101]
	v_mfma_f32_16x16x32_bf16 v[90:93], v[182:185], v[198:201], v[90:93]
	v_mfma_f32_16x16x32_bf16 v[82:85], v[174:177], v[206:209], v[82:85]
	v_mfma_f32_16x16x32_bf16 v[74:77], v[182:185], v[206:209], v[74:77]
	v_mfma_f32_16x16x32_bf16 v[70:73], v[174:177], v[214:217], v[70:73]
	v_mfma_f32_16x16x32_bf16 v[66:69], v[182:185], v[214:217], v[66:69]
	s_barrier
	s_add_i32 s60, s48, s40
	v_lshl_add_u64 v[146:147], s[34:35], 0, v[132:133]
	s_mov_b32 m0, s60
	ds_read_b128 v[186:189], v152 offset:16384
	ds_read_b128 v[190:193], v152 offset:17408
	ds_read_b128 v[194:197], v152 offset:18432
	ds_read_b128 v[198:201], v152 offset:19456
	ds_read_b128 v[202:205], v152 offset:20480
	ds_read_b128 v[206:209], v152 offset:21504
	ds_read_b128 v[210:213], v152 offset:22528
	ds_read_b128 v[214:217], v152 offset:23552
	global_load_lds_dwordx4 v[146:147], off
	s_add_i32 m0, s60, 0x2000
	s_add_u32 s60, s34, 0x80000
	v_lshl_add_u64 v[218:219], s[34:35], 0, v[136:137]
	s_addc_u32 s61, s35, 0
	s_add_i32 s62, s49, s40
	global_load_lds_dwordx4 v[218:219], off
	v_lshl_add_u64 v[220:221], s[60:61], 0, v[132:133]
	s_mov_b32 m0, s62
	v_lshl_add_u64 v[222:223], s[36:37], 0, v[134:135]
	global_load_lds_dwordx4 v[220:221], off
	v_lshl_add_u64 v[220:221], s[60:61], 0, v[136:137]
	s_add_i32 m0, s62, 0x2000
	s_nop 0
	global_load_lds_dwordx4 v[220:221], off
	v_lshl_add_u64 v[220:221], s[36:37], 0, v[130:131]
	s_mov_b32 m0, s29
	s_nop 0
	global_load_lds_dwordx4 v[220:221], off
	s_mov_b32 m0, s41
	s_nop 0
	global_load_lds_dwordx4 v[222:223], off
	s_waitcnt vmcnt(8)
	s_waitcnt lgkmcnt(0)
	s_barrier
	v_mfma_f32_16x16x32_bf16 v[62:65], v[154:157], v[186:189], v[62:65]
	v_mfma_f32_16x16x32_bf16 v[58:61], v[162:165], v[186:189], v[58:61]
	v_mfma_f32_16x16x32_bf16 v[54:57], v[154:157], v[194:197], v[54:57]
	v_mfma_f32_16x16x32_bf16 v[46:49], v[162:165], v[194:197], v[46:49]
	v_mfma_f32_16x16x32_bf16 v[38:41], v[154:157], v[202:205], v[38:41]
	v_mfma_f32_16x16x32_bf16 v[30:33], v[162:165], v[202:205], v[30:33]
	v_mfma_f32_16x16x32_bf16 v[22:25], v[154:157], v[210:213], v[22:25]
	v_mfma_f32_16x16x32_bf16 v[14:17], v[162:165], v[210:213], v[14:17]
	v_mfma_f32_16x16x32_bf16 v[62:65], v[158:161], v[190:193], v[62:65]
	v_mfma_f32_16x16x32_bf16 v[58:61], v[166:169], v[190:193], v[58:61]
	v_mfma_f32_16x16x32_bf16 v[54:57], v[158:161], v[198:201], v[54:57]
	v_mfma_f32_16x16x32_bf16 v[46:49], v[166:169], v[198:201], v[46:49]
	v_mfma_f32_16x16x32_bf16 v[38:41], v[158:161], v[206:209], v[38:41]
	v_mfma_f32_16x16x32_bf16 v[30:33], v[166:169], v[206:209], v[30:33]
	v_mfma_f32_16x16x32_bf16 v[22:25], v[158:161], v[214:217], v[22:25]
	v_mfma_f32_16x16x32_bf16 v[14:17], v[166:169], v[214:217], v[14:17]
	v_mfma_f32_16x16x32_bf16 v[50:53], v[170:173], v[186:189], v[50:53]
	v_mfma_f32_16x16x32_bf16 v[42:45], v[178:181], v[186:189], v[42:45]
	v_mfma_f32_16x16x32_bf16 v[34:37], v[170:173], v[194:197], v[34:37]
	v_mfma_f32_16x16x32_bf16 v[26:29], v[178:181], v[194:197], v[26:29]
	v_mfma_f32_16x16x32_bf16 v[18:21], v[170:173], v[202:205], v[18:21]
	v_mfma_f32_16x16x32_bf16 v[10:13], v[178:181], v[202:205], v[10:13]
	v_mfma_f32_16x16x32_bf16 v[6:9], v[170:173], v[210:213], v[6:9]
	v_mfma_f32_16x16x32_bf16 v[2:5], v[178:181], v[210:213], v[2:5]
	v_mfma_f32_16x16x32_bf16 v[50:53], v[174:177], v[190:193], v[50:53]
	v_mfma_f32_16x16x32_bf16 v[42:45], v[182:185], v[190:193], v[42:45]
	v_mfma_f32_16x16x32_bf16 v[34:37], v[174:177], v[198:201], v[34:37]
	v_mfma_f32_16x16x32_bf16 v[26:29], v[182:185], v[198:201], v[26:29]
	v_mfma_f32_16x16x32_bf16 v[18:21], v[174:177], v[206:209], v[18:21]
	v_mfma_f32_16x16x32_bf16 v[10:13], v[182:185], v[206:209], v[10:13]
	v_mfma_f32_16x16x32_bf16 v[6:9], v[174:177], v[214:217], v[6:9]
	v_mfma_f32_16x16x32_bf16 v[2:5], v[182:185], v[214:217], v[2:5]
	s_barrier
	s_add_i32 s60, 0, 0x18000
	v_add_u32_e32 v153, s60, v148
	s_add_i32 s61, 0, 0x1c000
	ds_read_b128 v[154:157], v153
	ds_read_b128 v[158:161], v153 offset:1024
	ds_read_b128 v[162:165], v153 offset:2048
	ds_read_b128 v[166:169], v153 offset:3072
	v_add_u32_e32 v153, s61, v148
	ds_read_b128 v[170:173], v153
	ds_read_b128 v[174:177], v153 offset:1024
	ds_read_b128 v[178:181], v153 offset:2048
	ds_read_b128 v[182:185], v153 offset:3072
	s_add_u32 s36, s36, 0x80000
	s_addc_u32 s37, s37, 0
	s_mov_b32 m0, s42
	v_lshl_add_u64 v[224:225], s[36:37], 0, v[130:131]
	ds_read_b128 v[186:189], v152 offset:32768
	ds_read_b128 v[190:193], v152 offset:33792
	ds_read_b128 v[194:197], v152 offset:34816
	ds_read_b128 v[198:201], v152 offset:35840
	ds_read_b128 v[202:205], v152 offset:36864
	ds_read_b128 v[206:209], v152 offset:37888
	ds_read_b128 v[210:213], v152 offset:38912
	ds_read_b128 v[214:217], v152 offset:39936
	global_load_lds_dwordx4 v[224:225], off
	v_lshl_add_u64 v[224:225], s[36:37], 0, v[134:135]
	s_mov_b32 m0, s43
	s_nop 0
	global_load_lds_dwordx4 v[224:225], off
	s_waitcnt vmcnt(8)
	s_waitcnt lgkmcnt(0)
	s_barrier
	v_mfma_f32_16x16x32_bf16 v[126:129], v[154:157], v[186:189], v[126:129]
	v_mfma_f32_16x16x32_bf16 v[122:125], v[162:165], v[186:189], v[122:125]
	v_mfma_f32_16x16x32_bf16 v[118:121], v[154:157], v[194:197], v[118:121]
	v_mfma_f32_16x16x32_bf16 v[110:113], v[162:165], v[194:197], v[110:113]
	v_mfma_f32_16x16x32_bf16 v[102:105], v[154:157], v[202:205], v[102:105]
	v_mfma_f32_16x16x32_bf16 v[94:97], v[162:165], v[202:205], v[94:97]
	v_mfma_f32_16x16x32_bf16 v[86:89], v[154:157], v[210:213], v[86:89]
	v_mfma_f32_16x16x32_bf16 v[78:81], v[162:165], v[210:213], v[78:81]
	v_mfma_f32_16x16x32_bf16 v[126:129], v[158:161], v[190:193], v[126:129]
	v_mfma_f32_16x16x32_bf16 v[122:125], v[166:169], v[190:193], v[122:125]
	v_mfma_f32_16x16x32_bf16 v[118:121], v[158:161], v[198:201], v[118:121]
	v_mfma_f32_16x16x32_bf16 v[110:113], v[166:169], v[198:201], v[110:113]
	v_mfma_f32_16x16x32_bf16 v[102:105], v[158:161], v[206:209], v[102:105]
	v_mfma_f32_16x16x32_bf16 v[94:97], v[166:169], v[206:209], v[94:97]
	v_mfma_f32_16x16x32_bf16 v[86:89], v[158:161], v[214:217], v[86:89]
	v_mfma_f32_16x16x32_bf16 v[78:81], v[166:169], v[214:217], v[78:81]
	v_mfma_f32_16x16x32_bf16 v[114:117], v[170:173], v[186:189], v[114:117]
	v_mfma_f32_16x16x32_bf16 v[106:109], v[178:181], v[186:189], v[106:109]
	v_mfma_f32_16x16x32_bf16 v[98:101], v[170:173], v[194:197], v[98:101]
	v_mfma_f32_16x16x32_bf16 v[90:93], v[178:181], v[194:197], v[90:93]
	v_mfma_f32_16x16x32_bf16 v[82:85], v[170:173], v[202:205], v[82:85]
	v_mfma_f32_16x16x32_bf16 v[74:77], v[178:181], v[202:205], v[74:77]
	v_mfma_f32_16x16x32_bf16 v[70:73], v[170:173], v[210:213], v[70:73]
	v_mfma_f32_16x16x32_bf16 v[66:69], v[178:181], v[210:213], v[66:69]
	v_mfma_f32_16x16x32_bf16 v[114:117], v[174:177], v[190:193], v[114:117]
	v_mfma_f32_16x16x32_bf16 v[106:109], v[182:185], v[190:193], v[106:109]
	v_mfma_f32_16x16x32_bf16 v[98:101], v[174:177], v[198:201], v[98:101]
	v_mfma_f32_16x16x32_bf16 v[90:93], v[182:185], v[198:201], v[90:93]
	v_mfma_f32_16x16x32_bf16 v[82:85], v[174:177], v[206:209], v[82:85]
	v_mfma_f32_16x16x32_bf16 v[74:77], v[182:185], v[206:209], v[74:77]
	v_mfma_f32_16x16x32_bf16 v[70:73], v[174:177], v[214:217], v[70:73]
	v_mfma_f32_16x16x32_bf16 v[66:69], v[182:185], v[214:217], v[66:69]
	s_barrier
	s_add_i32 s36, s60, s40
	v_lshl_add_u64 v[146:147], v[146:147], 0, s[10:11]
	s_mov_b32 m0, s36
	ds_read_b128 v[186:189], v152 offset:49152
	ds_read_b128 v[190:193], v152 offset:50176
	ds_read_b128 v[194:197], v152 offset:51200
	ds_read_b128 v[198:201], v152 offset:52224
	ds_read_b128 v[202:205], v152 offset:53248
	ds_read_b128 v[206:209], v152 offset:54272
	ds_read_b128 v[210:213], v152 offset:55296
	ds_read_b128 v[214:217], v152 offset:56320
	global_load_lds_dwordx4 v[146:147], off
	s_add_i32 m0, s36, 0x2000
	s_add_u32 s34, s34, 0x80080
	v_lshl_add_u64 v[146:147], v[218:219], 0, s[10:11]
	s_addc_u32 s35, s35, 0
	s_add_i32 s36, s61, s40
	global_load_lds_dwordx4 v[146:147], off
	v_lshl_add_u64 v[146:147], s[34:35], 0, v[132:133]
	s_mov_b32 m0, s36
	s_nop 0
	global_load_lds_dwordx4 v[146:147], off
	v_lshl_add_u64 v[146:147], s[34:35], 0, v[136:137]
	s_add_i32 m0, s36, 0x2000
	s_nop 0
	global_load_lds_dwordx4 v[146:147], off
	v_lshl_add_u64 v[146:147], v[220:221], 0, s[10:11]
	s_mov_b32 m0, s45
	s_nop 0
	global_load_lds_dwordx4 v[146:147], off
	v_lshl_add_u64 v[146:147], v[222:223], 0, s[10:11]
	s_mov_b32 m0, s46
	s_nop 0
	global_load_lds_dwordx4 v[146:147], off
	s_waitcnt vmcnt(8)
	s_waitcnt lgkmcnt(0)
	s_barrier
	v_mfma_f32_16x16x32_bf16 v[62:65], v[154:157], v[186:189], v[62:65]
	v_mfma_f32_16x16x32_bf16 v[58:61], v[162:165], v[186:189], v[58:61]
	v_mfma_f32_16x16x32_bf16 v[54:57], v[154:157], v[194:197], v[54:57]
	v_mfma_f32_16x16x32_bf16 v[46:49], v[162:165], v[194:197], v[46:49]
	v_mfma_f32_16x16x32_bf16 v[38:41], v[154:157], v[202:205], v[38:41]
	v_mfma_f32_16x16x32_bf16 v[30:33], v[162:165], v[202:205], v[30:33]
	v_mfma_f32_16x16x32_bf16 v[22:25], v[154:157], v[210:213], v[22:25]
	v_mfma_f32_16x16x32_bf16 v[14:17], v[162:165], v[210:213], v[14:17]
	v_mfma_f32_16x16x32_bf16 v[62:65], v[158:161], v[190:193], v[62:65]
	v_mfma_f32_16x16x32_bf16 v[58:61], v[166:169], v[190:193], v[58:61]
	v_mfma_f32_16x16x32_bf16 v[54:57], v[158:161], v[198:201], v[54:57]
	v_mfma_f32_16x16x32_bf16 v[46:49], v[166:169], v[198:201], v[46:49]
	v_mfma_f32_16x16x32_bf16 v[38:41], v[158:161], v[206:209], v[38:41]
	v_mfma_f32_16x16x32_bf16 v[30:33], v[166:169], v[206:209], v[30:33]
	v_mfma_f32_16x16x32_bf16 v[22:25], v[158:161], v[214:217], v[22:25]
	v_mfma_f32_16x16x32_bf16 v[14:17], v[166:169], v[214:217], v[14:17]
	v_mfma_f32_16x16x32_bf16 v[50:53], v[170:173], v[186:189], v[50:53]
	v_mfma_f32_16x16x32_bf16 v[42:45], v[178:181], v[186:189], v[42:45]
	v_mfma_f32_16x16x32_bf16 v[34:37], v[170:173], v[194:197], v[34:37]
	v_mfma_f32_16x16x32_bf16 v[26:29], v[178:181], v[194:197], v[26:29]
	v_mfma_f32_16x16x32_bf16 v[18:21], v[170:173], v[202:205], v[18:21]
	v_mfma_f32_16x16x32_bf16 v[10:13], v[178:181], v[202:205], v[10:13]
	v_mfma_f32_16x16x32_bf16 v[6:9], v[170:173], v[210:213], v[6:9]
	v_mfma_f32_16x16x32_bf16 v[2:5], v[178:181], v[210:213], v[2:5]
	v_mfma_f32_16x16x32_bf16 v[50:53], v[174:177], v[190:193], v[50:53]
	v_mfma_f32_16x16x32_bf16 v[42:45], v[182:185], v[190:193], v[42:45]
	v_mfma_f32_16x16x32_bf16 v[34:37], v[174:177], v[198:201], v[34:37]
	v_mfma_f32_16x16x32_bf16 v[26:29], v[182:185], v[198:201], v[26:29]
	v_mfma_f32_16x16x32_bf16 v[18:21], v[174:177], v[206:209], v[18:21]
	v_mfma_f32_16x16x32_bf16 v[10:13], v[182:185], v[206:209], v[10:13]
	v_mfma_f32_16x16x32_bf16 v[6:9], v[174:177], v[214:217], v[6:9]
	v_mfma_f32_16x16x32_bf16 v[2:5], v[182:185], v[214:217], v[2:5]
	s_barrier
	s_add_i32 s59, s59, 2
	s_add_u32 s30, s30, 0x100
	s_addc_u32 s31, s31, 0
	s_add_u32 s57, s57, 0x100
	s_addc_u32 s58, s58, 0
	s_cmp_gt_u32 s59, 29
	s_cbranch_scc0 .LBB0_1346
	s_and_b64 vcc, exec, s[12:13]
	s_cbranch_vccz .LBB0_1349
	s_barrier

.LBB0_1476:
	s_setprio 0
	v_readlane_b32 s22, v254, 1
	v_readlane_b32 s23, v254, 2
	s_mov_b32 s17, s99
	s_add_i32 s43, s43, 1
	s_mul_i32 s8, s43, s46
	s_waitcnt lgkmcnt(0)
	s_mul_hi_u32 s9, s43, s17
	s_add_i32 s9, s9, s8
	s_mul_i32 s8, s43, s17
	v_readlane_b32 s17, v254, 14
	s_add_u32 s22, s8, s17
	s_addc_u32 s23, s9, s37
	v_cmp_gt_i64_e32 vcc, s[22:23], v[146:147]
	v_cmp_lt_i64_e64 s[8:9], s[22:23], v[144:145]
	s_cbranch_vccnz .LBB0_1478
	s_ashr_i32 s16, s22, 31
	s_lshr_b32 s16, s16, 29
	s_add_i32 s16, s22, s16
	s_ashr_i32 s17, s16, 3
	s_and_b32 s16, s16, -8
	s_sub_i32 s16, s22, s16
	s_cmp_lt_i32 s16, 0
	s_cselect_b32 s18, s38, 0x2c0
	s_mul_i32 s16, s16, s18
	s_add_i32 s16, s16, s17
	s_mul_hi_i32 s17, s16, 0x2e8ba2e9
	s_lshr_b32 s18, s17, 31
	s_ashr_i32 s17, s17, 6
	s_add_i32 s17, s17, s18
	s_lshl_b32 s18, s17, 3
	s_sub_i32 s19, 0x80, s18
	s_min_i32 s19, s19, 8
	s_abs_i32 s22, s19
	v_cvt_f32_u32_e32 v2, s22
	s_sub_i32 s24, 0, s22
	s_mulk_i32 s17, 0x160
	s_sub_i32 s17, s16, s17
	v_rcp_iflag_f32_e32 v2, v2
	s_abs_i32 s16, s17
	s_xor_b32 s23, s17, s19
	s_ashr_i32 s23, s23, 31
	v_mul_f32_e32 v2, 0x4f7ffffe, v2
	v_cvt_u32_f32_e32 v2, v2
	s_nop 0
	v_readfirstlane_b32 s25, v2
	s_mul_i32 s24, s24, s25
	s_mul_hi_u32 s24, s25, s24
	s_add_i32 s25, s25, s24
	s_mul_hi_u32 s24, s16, s25
	s_mul_i32 s25, s24, s22
	s_sub_i32 s16, s16, s25
	s_add_i32 s27, s24, 1
	s_sub_i32 s25, s16, s22
	s_cmp_ge_u32 s16, s22
	s_cselect_b32 s24, s27, s24
	s_cselect_b32 s16, s25, s16
	s_add_i32 s25, s24, 1
	s_cmp_ge_u32 s16, s22
	s_cselect_b32 s16, s25, s24
	s_xor_b32 s16, s16, s23
	s_sub_i32 s16, s16, s23
	s_mul_i32 s19, s16, s19
	s_sub_i32 s17, s17, s19
	s_add_i32 s18, s18, s17

.Lrx_1479_0:
	s_waitcnt vmcnt(24)
	s_waitcnt lgkmcnt(0)
	s_barrier
	v_mfma_f32_16x16x32_bf16 v[126:129], v[154:157], v[186:189], 0
	v_mfma_f32_16x16x32_bf16 v[122:125], v[162:165], v[186:189], 0
	v_mfma_f32_16x16x32_bf16 v[118:121], v[154:157], v[194:197], 0
	v_mfma_f32_16x16x32_bf16 v[114:117], v[162:165], v[194:197], 0
	v_mfma_f32_16x16x32_bf16 v[110:113], v[154:157], v[202:205], 0
	v_mfma_f32_16x16x32_bf16 v[102:105], v[162:165], v[202:205], 0
	v_mfma_f32_16x16x32_bf16 v[94:97], v[154:157], v[210:213], 0
	v_mfma_f32_16x16x32_bf16 v[86:89], v[162:165], v[210:213], 0
	v_mfma_f32_16x16x32_bf16 v[126:129], v[158:161], v[190:193], v[126:129]
	v_mfma_f32_16x16x32_bf16 v[122:125], v[166:169], v[190:193], v[122:125]
	v_mfma_f32_16x16x32_bf16 v[118:121], v[158:161], v[198:201], v[118:121]
	v_mfma_f32_16x16x32_bf16 v[114:117], v[166:169], v[198:201], v[114:117]
	v_mfma_f32_16x16x32_bf16 v[110:113], v[158:161], v[206:209], v[110:113]
	v_mfma_f32_16x16x32_bf16 v[102:105], v[166:169], v[206:209], v[102:105]
	v_mfma_f32_16x16x32_bf16 v[94:97], v[158:161], v[214:217], v[94:97]
	v_mfma_f32_16x16x32_bf16 v[86:89], v[166:169], v[214:217], v[86:89]
	v_mfma_f32_16x16x32_bf16 v[106:109], v[170:173], v[186:189], 0
	v_mfma_f32_16x16x32_bf16 v[98:101], v[178:181], v[186:189], 0
	v_mfma_f32_16x16x32_bf16 v[90:93], v[170:173], v[194:197], 0
	v_mfma_f32_16x16x32_bf16 v[82:85], v[178:181], v[194:197], 0
	v_mfma_f32_16x16x32_bf16 v[78:81], v[170:173], v[202:205], 0
	v_mfma_f32_16x16x32_bf16 v[74:77], v[178:181], v[202:205], 0
	v_mfma_f32_16x16x32_bf16 v[70:73], v[170:173], v[210:213], 0
	v_mfma_f32_16x16x32_bf16 v[66:69], v[178:181], v[210:213], 0
	v_mfma_f32_16x16x32_bf16 v[106:109], v[174:177], v[190:193], v[106:109]
	v_mfma_f32_16x16x32_bf16 v[98:101], v[182:185], v[190:193], v[98:101]
	v_mfma_f32_16x16x32_bf16 v[90:93], v[174:177], v[198:201], v[90:93]
	v_mfma_f32_16x16x32_bf16 v[82:85], v[182:185], v[198:201], v[82:85]
	v_mfma_f32_16x16x32_bf16 v[78:81], v[174:177], v[206:209], v[78:81]
	v_mfma_f32_16x16x32_bf16 v[74:77], v[182:185], v[206:209], v[74:77]
	v_mfma_f32_16x16x32_bf16 v[70:73], v[174:177], v[214:217], v[70:73]
	v_mfma_f32_16x16x32_bf16 v[66:69], v[182:185], v[214:217], v[66:69]
	s_barrier
	s_add_i32 s55, s47, s36
	v_lshl_add_u64 v[218:219], s[30:31], 0, v[134:135]
	s_mov_b32 m0, s55
	ds_read_b128 v[186:189], v152 offset:16384
	ds_read_b128 v[190:193], v152 offset:17408
	ds_read_b128 v[194:197], v152 offset:18432
	ds_read_b128 v[198:201], v152 offset:19456
	ds_read_b128 v[202:205], v152 offset:20480
	ds_read_b128 v[206:209], v152 offset:21504
	ds_read_b128 v[210:213], v152 offset:22528
	ds_read_b128 v[214:217], v152 offset:23552
	global_load_lds_dwordx4 v[218:219], off
	s_add_i32 m0, s55, 0x2000
	s_add_u32 s56, s30, 0x80000
	v_lshl_add_u64 v[220:221], s[30:31], 0, v[130:131]
	s_addc_u32 s57, s31, 0
	s_add_i32 s55, s48, s36
	global_load_lds_dwordx4 v[220:221], off
	v_lshl_add_u64 v[222:223], s[56:57], 0, v[134:135]
	s_mov_b32 m0, s55
	v_lshl_add_u64 v[224:225], s[34:35], 0, v[132:133]
	global_load_lds_dwordx4 v[222:223], off
	v_lshl_add_u64 v[222:223], s[56:57], 0, v[130:131]
	s_add_i32 m0, s55, 0x2000
	s_nop 0
	global_load_lds_dwordx4 v[222:223], off
	v_lshl_add_u64 v[222:223], s[34:35], 0, v[136:137]
	s_mov_b32 m0, s39
	s_nop 0
	global_load_lds_dwordx4 v[222:223], off
	s_mov_b32 m0, s40
	s_nop 0
	global_load_lds_dwordx4 v[224:225], off
	s_cmp_lg_u32 s100, 0
	s_cbranch_scc1 .Lrx_1479_1
	s_waitcnt vmcnt(8)
.Lrx_1479_1:
	s_waitcnt vmcnt(24)
	s_mov_b32 s100, 1
	s_waitcnt lgkmcnt(0)
	s_barrier
	v_mfma_f32_16x16x32_bf16 v[62:65], v[154:157], v[186:189], 0
	v_mfma_f32_16x16x32_bf16 v[58:61], v[162:165], v[186:189], 0
	v_mfma_f32_16x16x32_bf16 v[54:57], v[154:157], v[194:197], 0
	v_mfma_f32_16x16x32_bf16 v[50:53], v[162:165], v[194:197], 0
	v_mfma_f32_16x16x32_bf16 v[46:49], v[154:157], v[202:205], 0
	v_mfma_f32_16x16x32_bf16 v[38:41], v[162:165], v[202:205], 0
	v_mfma_f32_16x16x32_bf16 v[30:33], v[154:157], v[210:213], 0
	v_mfma_f32_16x16x32_bf16 v[22:25], v[162:165], v[210:213], 0
	v_mfma_f32_16x16x32_bf16 v[62:65], v[158:161], v[190:193], v[62:65]
	v_mfma_f32_16x16x32_bf16 v[58:61], v[166:169], v[190:193], v[58:61]
	v_mfma_f32_16x16x32_bf16 v[54:57], v[158:161], v[198:201], v[54:57]
	v_mfma_f32_16x16x32_bf16 v[50:53], v[166:169], v[198:201], v[50:53]
	v_mfma_f32_16x16x32_bf16 v[46:49], v[158:161], v[206:209], v[46:49]
	v_mfma_f32_16x16x32_bf16 v[38:41], v[166:169], v[206:209], v[38:41]
	v_mfma_f32_16x16x32_bf16 v[30:33], v[158:161], v[214:217], v[30:33]
	v_mfma_f32_16x16x32_bf16 v[22:25], v[166:169], v[214:217], v[22:25]
	v_mfma_f32_16x16x32_bf16 v[42:45], v[170:173], v[186:189], 0
	v_mfma_f32_16x16x32_bf16 v[34:37], v[178:181], v[186:189], 0
	v_mfma_f32_16x16x32_bf16 v[26:29], v[170:173], v[194:197], 0
	v_mfma_f32_16x16x32_bf16 v[18:21], v[178:181], v[194:197], 0
	v_mfma_f32_16x16x32_bf16 v[14:17], v[170:173], v[202:205], 0
	v_mfma_f32_16x16x32_bf16 v[10:13], v[178:181], v[202:205], 0
	v_mfma_f32_16x16x32_bf16 v[6:9], v[170:173], v[210:213], 0
	v_mfma_f32_16x16x32_bf16 v[2:5], v[178:181], v[210:213], 0
	v_mfma_f32_16x16x32_bf16 v[42:45], v[174:177], v[190:193], v[42:45]
	v_mfma_f32_16x16x32_bf16 v[34:37], v[182:185], v[190:193], v[34:37]
	v_mfma_f32_16x16x32_bf16 v[26:29], v[174:177], v[198:201], v[26:29]
	v_mfma_f32_16x16x32_bf16 v[18:21], v[182:185], v[198:201], v[18:21]
	v_mfma_f32_16x16x32_bf16 v[14:17], v[174:177], v[206:209], v[14:17]
	v_mfma_f32_16x16x32_bf16 v[10:13], v[182:185], v[206:209], v[10:13]
	v_mfma_f32_16x16x32_bf16 v[6:9], v[174:177], v[214:217], v[6:9]
	v_mfma_f32_16x16x32_bf16 v[2:5], v[182:185], v[214:217], v[2:5]
	s_barrier
	s_add_i32 s55, 0, 0x18000
	v_add_u32_e32 v153, s55, v148
	s_add_i32 s56, 0, 0x1c000
	ds_read_b128 v[154:157], v153
	ds_read_b128 v[158:161], v153 offset:1024
	ds_read_b128 v[162:165], v153 offset:2048
	ds_read_b128 v[166:169], v153 offset:3072
	v_add_u32_e32 v153, s56, v148
	ds_read_b128 v[170:173], v153
	ds_read_b128 v[174:177], v153 offset:1024
	ds_read_b128 v[178:181], v153 offset:2048
	ds_read_b128 v[182:185], v153 offset:3072
	s_add_u32 s34, s34, 0x80000
	s_addc_u32 s35, s35, 0
	s_mov_b32 m0, s41
	v_lshl_add_u64 v[226:227], s[34:35], 0, v[136:137]
	ds_read_b128 v[186:189], v152 offset:32768
	ds_read_b128 v[190:193], v152 offset:33792
	ds_read_b128 v[194:197], v152 offset:34816
	ds_read_b128 v[198:201], v152 offset:35840
	ds_read_b128 v[202:205], v152 offset:36864
	ds_read_b128 v[206:209], v152 offset:37888
	ds_read_b128 v[210:213], v152 offset:38912
	ds_read_b128 v[214:217], v152 offset:39936
	global_load_lds_dwordx4 v[226:227], off
	v_lshl_add_u64 v[226:227], s[34:35], 0, v[132:133]
	s_mov_b32 m0, s42
	s_nop 0
	global_load_lds_dwordx4 v[226:227], off
	s_waitcnt vmcnt(8)
	s_waitcnt lgkmcnt(0)
	s_barrier
	v_mfma_f32_16x16x32_bf16 v[126:129], v[154:157], v[186:189], v[126:129]
	v_mfma_f32_16x16x32_bf16 v[122:125], v[162:165], v[186:189], v[122:125]
	v_mfma_f32_16x16x32_bf16 v[118:121], v[154:157], v[194:197], v[118:121]
	v_mfma_f32_16x16x32_bf16 v[114:117], v[162:165], v[194:197], v[114:117]
	v_mfma_f32_16x16x32_bf16 v[110:113], v[154:157], v[202:205], v[110:113]
	v_mfma_f32_16x16x32_bf16 v[102:105], v[162:165], v[202:205], v[102:105]
	v_mfma_f32_16x16x32_bf16 v[94:97], v[154:157], v[210:213], v[94:97]
	v_mfma_f32_16x16x32_bf16 v[86:89], v[162:165], v[210:213], v[86:89]
	v_mfma_f32_16x16x32_bf16 v[126:129], v[158:161], v[190:193], v[126:129]
	v_mfma_f32_16x16x32_bf16 v[122:125], v[166:169], v[190:193], v[122:125]
	v_mfma_f32_16x16x32_bf16 v[118:121], v[158:161], v[198:201], v[118:121]
	v_mfma_f32_16x16x32_bf16 v[114:117], v[166:169], v[198:201], v[114:117]
	v_mfma_f32_16x16x32_bf16 v[110:113], v[158:161], v[206:209], v[110:113]
	v_mfma_f32_16x16x32_bf16 v[102:105], v[166:169], v[206:209], v[102:105]
	v_mfma_f32_16x16x32_bf16 v[94:97], v[158:161], v[214:217], v[94:97]
	v_mfma_f32_16x16x32_bf16 v[86:89], v[166:169], v[214:217], v[86:89]
	v_mfma_f32_16x16x32_bf16 v[106:109], v[170:173], v[186:189], v[106:109]
	v_mfma_f32_16x16x32_bf16 v[98:101], v[178:181], v[186:189], v[98:101]
	v_mfma_f32_16x16x32_bf16 v[90:93], v[170:173], v[194:197], v[90:93]
	v_mfma_f32_16x16x32_bf16 v[82:85], v[178:181], v[194:197], v[82:85]
	v_mfma_f32_16x16x32_bf16 v[78:81], v[170:173], v[202:205], v[78:81]
	v_mfma_f32_16x16x32_bf16 v[74:77], v[178:181], v[202:205], v[74:77]
	v_mfma_f32_16x16x32_bf16 v[70:73], v[170:173], v[210:213], v[70:73]
	v_mfma_f32_16x16x32_bf16 v[66:69], v[178:181], v[210:213], v[66:69]
	v_mfma_f32_16x16x32_bf16 v[106:109], v[174:177], v[190:193], v[106:109]
	v_mfma_f32_16x16x32_bf16 v[98:101], v[182:185], v[190:193], v[98:101]
	v_mfma_f32_16x16x32_bf16 v[90:93], v[174:177], v[198:201], v[90:93]
	v_mfma_f32_16x16x32_bf16 v[82:85], v[182:185], v[198:201], v[82:85]
	v_mfma_f32_16x16x32_bf16 v[78:81], v[174:177], v[206:209], v[78:81]
	v_mfma_f32_16x16x32_bf16 v[74:77], v[182:185], v[206:209], v[74:77]
	v_mfma_f32_16x16x32_bf16 v[70:73], v[174:177], v[214:217], v[70:73]
	v_mfma_f32_16x16x32_bf16 v[66:69], v[182:185], v[214:217], v[66:69]
	s_barrier
	s_add_i32 s34, s55, s36
	v_lshl_add_u64 v[218:219], v[218:219], 0, s[10:11]
	s_mov_b32 m0, s34
	ds_read_b128 v[186:189], v152 offset:49152
	ds_read_b128 v[190:193], v152 offset:50176
	ds_read_b128 v[194:197], v152 offset:51200
	ds_read_b128 v[198:201], v152 offset:52224
	ds_read_b128 v[202:205], v152 offset:53248
	ds_read_b128 v[206:209], v152 offset:54272
	ds_read_b128 v[210:213], v152 offset:55296
	ds_read_b128 v[214:217], v152 offset:56320
	global_load_lds_dwordx4 v[218:219], off
	s_add_i32 m0, s34, 0x2000
	s_add_u32 s30, s30, 0x80080
	v_lshl_add_u64 v[218:219], v[220:221], 0, s[10:11]
	s_addc_u32 s31, s31, 0
	s_add_i32 s34, s56, s36
	global_load_lds_dwordx4 v[218:219], off
	v_lshl_add_u64 v[218:219], s[30:31], 0, v[134:135]
	s_mov_b32 m0, s34
	s_nop 0
	global_load_lds_dwordx4 v[218:219], off
	v_lshl_add_u64 v[218:219], s[30:31], 0, v[130:131]
	s_add_i32 m0, s34, 0x2000
	s_nop 0
	global_load_lds_dwordx4 v[218:219], off
	v_lshl_add_u64 v[218:219], v[222:223], 0, s[10:11]
	s_mov_b32 m0, s44
	s_nop 0
	global_load_lds_dwordx4 v[218:219], off
	v_lshl_add_u64 v[218:219], v[224:225], 0, s[10:11]
	s_mov_b32 m0, s45
	s_nop 0
	global_load_lds_dwordx4 v[218:219], off
	s_waitcnt vmcnt(8)
	s_waitcnt lgkmcnt(0)
	s_barrier
	v_mfma_f32_16x16x32_bf16 v[62:65], v[154:157], v[186:189], v[62:65]
	v_mfma_f32_16x16x32_bf16 v[58:61], v[162:165], v[186:189], v[58:61]
	v_mfma_f32_16x16x32_bf16 v[54:57], v[154:157], v[194:197], v[54:57]
	v_mfma_f32_16x16x32_bf16 v[50:53], v[162:165], v[194:197], v[50:53]
	v_mfma_f32_16x16x32_bf16 v[46:49], v[154:157], v[202:205], v[46:49]
	v_mfma_f32_16x16x32_bf16 v[38:41], v[162:165], v[202:205], v[38:41]
	v_mfma_f32_16x16x32_bf16 v[30:33], v[154:157], v[210:213], v[30:33]
	v_mfma_f32_16x16x32_bf16 v[22:25], v[162:165], v[210:213], v[22:25]
	v_mfma_f32_16x16x32_bf16 v[62:65], v[158:161], v[190:193], v[62:65]
	v_mfma_f32_16x16x32_bf16 v[58:61], v[166:169], v[190:193], v[58:61]
	v_mfma_f32_16x16x32_bf16 v[54:57], v[158:161], v[198:201], v[54:57]
	v_mfma_f32_16x16x32_bf16 v[50:53], v[166:169], v[198:201], v[50:53]
	v_mfma_f32_16x16x32_bf16 v[46:49], v[158:161], v[206:209], v[46:49]
	v_mfma_f32_16x16x32_bf16 v[38:41], v[166:169], v[206:209], v[38:41]
	v_mfma_f32_16x16x32_bf16 v[30:33], v[158:161], v[214:217], v[30:33]
	v_mfma_f32_16x16x32_bf16 v[22:25], v[166:169], v[214:217], v[22:25]
	v_mfma_f32_16x16x32_bf16 v[42:45], v[170:173], v[186:189], v[42:45]
	v_mfma_f32_16x16x32_bf16 v[34:37], v[178:181], v[186:189], v[34:37]
	v_mfma_f32_16x16x32_bf16 v[26:29], v[170:173], v[194:197], v[26:29]
	v_mfma_f32_16x16x32_bf16 v[18:21], v[178:181], v[194:197], v[18:21]
	v_mfma_f32_16x16x32_bf16 v[14:17], v[170:173], v[202:205], v[14:17]
	v_mfma_f32_16x16x32_bf16 v[10:13], v[178:181], v[202:205], v[10:13]
	v_mfma_f32_16x16x32_bf16 v[6:9], v[170:173], v[210:213], v[6:9]
	v_mfma_f32_16x16x32_bf16 v[2:5], v[178:181], v[210:213], v[2:5]
	v_mfma_f32_16x16x32_bf16 v[42:45], v[174:177], v[190:193], v[42:45]
	v_mfma_f32_16x16x32_bf16 v[34:37], v[182:185], v[190:193], v[34:37]
	v_mfma_f32_16x16x32_bf16 v[26:29], v[174:177], v[198:201], v[26:29]
	v_mfma_f32_16x16x32_bf16 v[18:21], v[182:185], v[198:201], v[18:21]
	v_mfma_f32_16x16x32_bf16 v[14:17], v[174:177], v[206:209], v[14:17]
	v_mfma_f32_16x16x32_bf16 v[10:13], v[182:185], v[206:209], v[10:13]
	v_mfma_f32_16x16x32_bf16 v[6:9], v[174:177], v[214:217], v[6:9]
	v_mfma_f32_16x16x32_bf16 v[2:5], v[182:185], v[214:217], v[2:5]
	s_barrier
	s_add_i32 s54, s54, 2
	s_add_u32 s28, s28, 0x100
	s_addc_u32 s29, s29, 0
	s_add_u32 s52, s52, 0x100
	s_addc_u32 s53, s53, 0
	s_cmp_gt_u32 s54, 29
.LBB0_1479:
	ds_read_b128 v[154:157], v150
	ds_read_b128 v[158:161], v150 offset:1024
	ds_read_b128 v[162:165], v150 offset:2048
	ds_read_b128 v[166:169], v150 offset:3072
	ds_read_b128 v[170:173], v151
	ds_read_b128 v[174:177], v151 offset:1024
	ds_read_b128 v[178:181], v151 offset:2048
	ds_read_b128 v[182:185], v151 offset:3072
	s_add_u32 s30, s28, 0xfff80080
	s_addc_u32 s31, s29, -1
	s_cmp_eq_u32 s54, 28
	s_cselect_b32 s35, s19, s31
	s_cselect_b32 s34, s27, s30
	s_cselect_b32 s31, s17, s53
	s_cselect_b32 s30, s51, s52
	v_lshl_add_u64 v[218:219], s[28:29], 0, v[140:141]
	s_add_i32 m0, s39, 0xc000
	ds_read_b128 v[186:189], v152
	ds_read_b128 v[190:193], v152 offset:1024
	ds_read_b128 v[194:197], v152 offset:2048
	ds_read_b128 v[198:201], v152 offset:3072
	ds_read_b128 v[202:205], v152 offset:4096
	ds_read_b128 v[206:209], v152 offset:5120
	ds_read_b128 v[210:213], v152 offset:6144
	ds_read_b128 v[214:217], v152 offset:7168
	global_load_lds_dwordx4 v[218:219], off
	v_lshl_add_u64 v[218:219], s[28:29], 0, v[142:143]
	s_add_i32 m0, s39, 0xe000
	s_nop 0
	global_load_lds_dwordx4 v[218:219], off
	s_waitcnt vmcnt(8)
	s_waitcnt lgkmcnt(0)
	s_barrier
	v_mfma_f32_16x16x32_bf16 v[126:129], v[154:157], v[186:189], v[126:129]
	v_mfma_f32_16x16x32_bf16 v[122:125], v[162:165], v[186:189], v[122:125]
	v_mfma_f32_16x16x32_bf16 v[118:121], v[154:157], v[194:197], v[118:121]
	v_mfma_f32_16x16x32_bf16 v[114:117], v[162:165], v[194:197], v[114:117]
	v_mfma_f32_16x16x32_bf16 v[110:113], v[154:157], v[202:205], v[110:113]
	v_mfma_f32_16x16x32_bf16 v[102:105], v[162:165], v[202:205], v[102:105]
	v_mfma_f32_16x16x32_bf16 v[94:97], v[154:157], v[210:213], v[94:97]
	v_mfma_f32_16x16x32_bf16 v[86:89], v[162:165], v[210:213], v[86:89]
	v_mfma_f32_16x16x32_bf16 v[126:129], v[158:161], v[190:193], v[126:129]
	v_mfma_f32_16x16x32_bf16 v[122:125], v[166:169], v[190:193], v[122:125]
	v_mfma_f32_16x16x32_bf16 v[118:121], v[158:161], v[198:201], v[118:121]
	v_mfma_f32_16x16x32_bf16 v[114:117], v[166:169], v[198:201], v[114:117]
	v_mfma_f32_16x16x32_bf16 v[110:113], v[158:161], v[206:209], v[110:113]
	v_mfma_f32_16x16x32_bf16 v[102:105], v[166:169], v[206:209], v[102:105]
	v_mfma_f32_16x16x32_bf16 v[94:97], v[158:161], v[214:217], v[94:97]
	v_mfma_f32_16x16x32_bf16 v[86:89], v[166:169], v[214:217], v[86:89]
	v_mfma_f32_16x16x32_bf16 v[106:109], v[170:173], v[186:189], v[106:109]
	v_mfma_f32_16x16x32_bf16 v[98:101], v[178:181], v[186:189], v[98:101]
	v_mfma_f32_16x16x32_bf16 v[90:93], v[170:173], v[194:197], v[90:93]
	v_mfma_f32_16x16x32_bf16 v[82:85], v[178:181], v[194:197], v[82:85]
	v_mfma_f32_16x16x32_bf16 v[78:81], v[170:173], v[202:205], v[78:81]
	v_mfma_f32_16x16x32_bf16 v[74:77], v[178:181], v[202:205], v[74:77]
	v_mfma_f32_16x16x32_bf16 v[70:73], v[170:173], v[210:213], v[70:73]
	v_mfma_f32_16x16x32_bf16 v[66:69], v[178:181], v[210:213], v[66:69]
	v_mfma_f32_16x16x32_bf16 v[106:109], v[174:177], v[190:193], v[106:109]
	v_mfma_f32_16x16x32_bf16 v[98:101], v[182:185], v[190:193], v[98:101]
	v_mfma_f32_16x16x32_bf16 v[90:93], v[174:177], v[198:201], v[90:93]
	v_mfma_f32_16x16x32_bf16 v[82:85], v[182:185], v[198:201], v[82:85]
	v_mfma_f32_16x16x32_bf16 v[78:81], v[174:177], v[206:209], v[78:81]
	v_mfma_f32_16x16x32_bf16 v[74:77], v[182:185], v[206:209], v[74:77]
	v_mfma_f32_16x16x32_bf16 v[70:73], v[174:177], v[214:217], v[70:73]
	v_mfma_f32_16x16x32_bf16 v[66:69], v[182:185], v[214:217], v[66:69]
	s_barrier
	s_add_i32 s55, s47, s36
	v_lshl_add_u64 v[218:219], s[30:31], 0, v[134:135]
	s_mov_b32 m0, s55
	ds_read_b128 v[186:189], v152 offset:16384
	ds_read_b128 v[190:193], v152 offset:17408
	ds_read_b128 v[194:197], v152 offset:18432
	ds_read_b128 v[198:201], v152 offset:19456
	ds_read_b128 v[202:205], v152 offset:20480
	ds_read_b128 v[206:209], v152 offset:21504
	ds_read_b128 v[210:213], v152 offset:22528
	ds_read_b128 v[214:217], v152 offset:23552
	global_load_lds_dwordx4 v[218:219], off
	s_add_i32 m0, s55, 0x2000
	s_add_u32 s56, s30, 0x80000
	v_lshl_add_u64 v[220:221], s[30:31], 0, v[130:131]
	s_addc_u32 s57, s31, 0
	s_add_i32 s55, s48, s36
	global_load_lds_dwordx4 v[220:221], off
	v_lshl_add_u64 v[222:223], s[56:57], 0, v[134:135]
	s_mov_b32 m0, s55
	v_lshl_add_u64 v[224:225], s[34:35], 0, v[132:133]
	global_load_lds_dwordx4 v[222:223], off
	v_lshl_add_u64 v[222:223], s[56:57], 0, v[130:131]
	s_add_i32 m0, s55, 0x2000
	s_nop 0
	global_load_lds_dwordx4 v[222:223], off
	v_lshl_add_u64 v[222:223], s[34:35], 0, v[136:137]
	s_mov_b32 m0, s39
	s_nop 0
	global_load_lds_dwordx4 v[222:223], off
	s_mov_b32 m0, s40
	s_nop 0
	global_load_lds_dwordx4 v[224:225], off
	s_waitcnt vmcnt(8)
	s_waitcnt lgkmcnt(0)
	s_barrier
	v_mfma_f32_16x16x32_bf16 v[62:65], v[154:157], v[186:189], v[62:65]
	v_mfma_f32_16x16x32_bf16 v[58:61], v[162:165], v[186:189], v[58:61]
	v_mfma_f32_16x16x32_bf16 v[54:57], v[154:157], v[194:197], v[54:57]
	v_mfma_f32_16x16x32_bf16 v[50:53], v[162:165], v[194:197], v[50:53]
	v_mfma_f32_16x16x32_bf16 v[46:49], v[154:157], v[202:205], v[46:49]
	v_mfma_f32_16x16x32_bf16 v[38:41], v[162:165], v[202:205], v[38:41]
	v_mfma_f32_16x16x32_bf16 v[30:33], v[154:157], v[210:213], v[30:33]
	v_mfma_f32_16x16x32_bf16 v[22:25], v[162:165], v[210:213], v[22:25]
	v_mfma_f32_16x16x32_bf16 v[62:65], v[158:161], v[190:193], v[62:65]
	v_mfma_f32_16x16x32_bf16 v[58:61], v[166:169], v[190:193], v[58:61]
	v_mfma_f32_16x16x32_bf16 v[54:57], v[158:161], v[198:201], v[54:57]
	v_mfma_f32_16x16x32_bf16 v[50:53], v[166:169], v[198:201], v[50:53]
	v_mfma_f32_16x16x32_bf16 v[46:49], v[158:161], v[206:209], v[46:49]
	v_mfma_f32_16x16x32_bf16 v[38:41], v[166:169], v[206:209], v[38:41]
	v_mfma_f32_16x16x32_bf16 v[30:33], v[158:161], v[214:217], v[30:33]
	v_mfma_f32_16x16x32_bf16 v[22:25], v[166:169], v[214:217], v[22:25]
	v_mfma_f32_16x16x32_bf16 v[42:45], v[170:173], v[186:189], v[42:45]
	v_mfma_f32_16x16x32_bf16 v[34:37], v[178:181], v[186:189], v[34:37]
	v_mfma_f32_16x16x32_bf16 v[26:29], v[170:173], v[194:197], v[26:29]
	v_mfma_f32_16x16x32_bf16 v[18:21], v[178:181], v[194:197], v[18:21]
	v_mfma_f32_16x16x32_bf16 v[14:17], v[170:173], v[202:205], v[14:17]
	v_mfma_f32_16x16x32_bf16 v[10:13], v[178:181], v[202:205], v[10:13]
	v_mfma_f32_16x16x32_bf16 v[6:9], v[170:173], v[210:213], v[6:9]
	v_mfma_f32_16x16x32_bf16 v[2:5], v[178:181], v[210:213], v[2:5]
	v_mfma_f32_16x16x32_bf16 v[42:45], v[174:177], v[190:193], v[42:45]
	v_mfma_f32_16x16x32_bf16 v[34:37], v[182:185], v[190:193], v[34:37]
	v_mfma_f32_16x16x32_bf16 v[26:29], v[174:177], v[198:201], v[26:29]
	v_mfma_f32_16x16x32_bf16 v[18:21], v[182:185], v[198:201], v[18:21]
	v_mfma_f32_16x16x32_bf16 v[14:17], v[174:177], v[206:209], v[14:17]
	v_mfma_f32_16x16x32_bf16 v[10:13], v[182:185], v[206:209], v[10:13]
	v_mfma_f32_16x16x32_bf16 v[6:9], v[174:177], v[214:217], v[6:9]
	v_mfma_f32_16x16x32_bf16 v[2:5], v[182:185], v[214:217], v[2:5]
	s_barrier
	s_add_i32 s55, 0, 0x18000
	v_add_u32_e32 v153, s55, v148
	s_add_i32 s56, 0, 0x1c000
	ds_read_b128 v[154:157], v153
	ds_read_b128 v[158:161], v153 offset:1024
	ds_read_b128 v[162:165], v153 offset:2048
	ds_read_b128 v[166:169], v153 offset:3072
	v_add_u32_e32 v153, s56, v148
	ds_read_b128 v[170:173], v153
	ds_read_b128 v[174:177], v153 offset:1024
	ds_read_b128 v[178:181], v153 offset:2048
	ds_read_b128 v[182:185], v153 offset:3072
	s_add_u32 s34, s34, 0x80000
	s_addc_u32 s35, s35, 0
	s_mov_b32 m0, s41
	v_lshl_add_u64 v[226:227], s[34:35], 0, v[136:137]
	ds_read_b128 v[186:189], v152 offset:32768
	ds_read_b128 v[190:193], v152 offset:33792
	ds_read_b128 v[194:197], v152 offset:34816
	ds_read_b128 v[198:201], v152 offset:35840
	ds_read_b128 v[202:205], v152 offset:36864
	ds_read_b128 v[206:209], v152 offset:37888
	ds_read_b128 v[210:213], v152 offset:38912
	ds_read_b128 v[214:217], v152 offset:39936
	global_load_lds_dwordx4 v[226:227], off
	v_lshl_add_u64 v[226:227], s[34:35], 0, v[132:133]
	s_mov_b32 m0, s42
	s_nop 0
	global_load_lds_dwordx4 v[226:227], off
	s_waitcnt vmcnt(8)
	s_waitcnt lgkmcnt(0)
	s_barrier
	v_mfma_f32_16x16x32_bf16 v[126:129], v[154:157], v[186:189], v[126:129]
	v_mfma_f32_16x16x32_bf16 v[122:125], v[162:165], v[186:189], v[122:125]
	v_mfma_f32_16x16x32_bf16 v[118:121], v[154:157], v[194:197], v[118:121]
	v_mfma_f32_16x16x32_bf16 v[114:117], v[162:165], v[194:197], v[114:117]
	v_mfma_f32_16x16x32_bf16 v[110:113], v[154:157], v[202:205], v[110:113]
	v_mfma_f32_16x16x32_bf16 v[102:105], v[162:165], v[202:205], v[102:105]
	v_mfma_f32_16x16x32_bf16 v[94:97], v[154:157], v[210:213], v[94:97]
	v_mfma_f32_16x16x32_bf16 v[86:89], v[162:165], v[210:213], v[86:89]
	v_mfma_f32_16x16x32_bf16 v[126:129], v[158:161], v[190:193], v[126:129]
	v_mfma_f32_16x16x32_bf16 v[122:125], v[166:169], v[190:193], v[122:125]
	v_mfma_f32_16x16x32_bf16 v[118:121], v[158:161], v[198:201], v[118:121]
	v_mfma_f32_16x16x32_bf16 v[114:117], v[166:169], v[198:201], v[114:117]
	v_mfma_f32_16x16x32_bf16 v[110:113], v[158:161], v[206:209], v[110:113]
	v_mfma_f32_16x16x32_bf16 v[102:105], v[166:169], v[206:209], v[102:105]
	v_mfma_f32_16x16x32_bf16 v[94:97], v[158:161], v[214:217], v[94:97]
	v_mfma_f32_16x16x32_bf16 v[86:89], v[166:169], v[214:217], v[86:89]
	v_mfma_f32_16x16x32_bf16 v[106:109], v[170:173], v[186:189], v[106:109]
	v_mfma_f32_16x16x32_bf16 v[98:101], v[178:181], v[186:189], v[98:101]
	v_mfma_f32_16x16x32_bf16 v[90:93], v[170:173], v[194:197], v[90:93]
	v_mfma_f32_16x16x32_bf16 v[82:85], v[178:181], v[194:197], v[82:85]
	v_mfma_f32_16x16x32_bf16 v[78:81], v[170:173], v[202:205], v[78:81]
	v_mfma_f32_16x16x32_bf16 v[74:77], v[178:181], v[202:205], v[74:77]
	v_mfma_f32_16x16x32_bf16 v[70:73], v[170:173], v[210:213], v[70:73]
	v_mfma_f32_16x16x32_bf16 v[66:69], v[178:181], v[210:213], v[66:69]
	v_mfma_f32_16x16x32_bf16 v[106:109], v[174:177], v[190:193], v[106:109]
	v_mfma_f32_16x16x32_bf16 v[98:101], v[182:185], v[190:193], v[98:101]
	v_mfma_f32_16x16x32_bf16 v[90:93], v[174:177], v[198:201], v[90:93]
	v_mfma_f32_16x16x32_bf16 v[82:85], v[182:185], v[198:201], v[82:85]
	v_mfma_f32_16x16x32_bf16 v[78:81], v[174:177], v[206:209], v[78:81]
	v_mfma_f32_16x16x32_bf16 v[74:77], v[182:185], v[206:209], v[74:77]
	v_mfma_f32_16x16x32_bf16 v[70:73], v[174:177], v[214:217], v[70:73]
	v_mfma_f32_16x16x32_bf16 v[66:69], v[182:185], v[214:217], v[66:69]
	s_barrier
	s_add_i32 s34, s55, s36
	v_lshl_add_u64 v[218:219], v[218:219], 0, s[10:11]
	s_mov_b32 m0, s34
	ds_read_b128 v[186:189], v152 offset:49152
	ds_read_b128 v[190:193], v152 offset:50176
	ds_read_b128 v[194:197], v152 offset:51200
	ds_read_b128 v[198:201], v152 offset:52224
	ds_read_b128 v[202:205], v152 offset:53248
	ds_read_b128 v[206:209], v152 offset:54272
	ds_read_b128 v[210:213], v152 offset:55296
	ds_read_b128 v[214:217], v152 offset:56320
	global_load_lds_dwordx4 v[218:219], off
	s_add_i32 m0, s34, 0x2000
	s_add_u32 s30, s30, 0x80080
	v_lshl_add_u64 v[218:219], v[220:221], 0, s[10:11]
	s_addc_u32 s31, s31, 0
	s_add_i32 s34, s56, s36
	global_load_lds_dwordx4 v[218:219], off
	v_lshl_add_u64 v[218:219], s[30:31], 0, v[134:135]
	s_mov_b32 m0, s34
	s_nop 0
	global_load_lds_dwordx4 v[218:219], off
	v_lshl_add_u64 v[218:219], s[30:31], 0, v[130:131]
	s_add_i32 m0, s34, 0x2000
	s_nop 0
	global_load_lds_dwordx4 v[218:219], off
	v_lshl_add_u64 v[218:219], v[222:223], 0, s[10:11]
	s_mov_b32 m0, s44
	s_nop 0
	global_load_lds_dwordx4 v[218:219], off
	v_lshl_add_u64 v[218:219], v[224:225], 0, s[10:11]
	s_mov_b32 m0, s45
	s_nop 0
	global_load_lds_dwordx4 v[218:219], off
	s_waitcnt vmcnt(8)
	s_waitcnt lgkmcnt(0)
	s_barrier
	v_mfma_f32_16x16x32_bf16 v[62:65], v[154:157], v[186:189], v[62:65]
	v_mfma_f32_16x16x32_bf16 v[58:61], v[162:165], v[186:189], v[58:61]
	v_mfma_f32_16x16x32_bf16 v[54:57], v[154:157], v[194:197], v[54:57]
	v_mfma_f32_16x16x32_bf16 v[50:53], v[162:165], v[194:197], v[50:53]
	v_mfma_f32_16x16x32_bf16 v[46:49], v[154:157], v[202:205], v[46:49]
	v_mfma_f32_16x16x32_bf16 v[38:41], v[162:165], v[202:205], v[38:41]
	v_mfma_f32_16x16x32_bf16 v[30:33], v[154:157], v[210:213], v[30:33]
	v_mfma_f32_16x16x32_bf16 v[22:25], v[162:165], v[210:213], v[22:25]
	v_mfma_f32_16x16x32_bf16 v[62:65], v[158:161], v[190:193], v[62:65]
	v_mfma_f32_16x16x32_bf16 v[58:61], v[166:169], v[190:193], v[58:61]
	v_mfma_f32_16x16x32_bf16 v[54:57], v[158:161], v[198:201], v[54:57]
	v_mfma_f32_16x16x32_bf16 v[50:53], v[166:169], v[198:201], v[50:53]
	v_mfma_f32_16x16x32_bf16 v[46:49], v[158:161], v[206:209], v[46:49]
	v_mfma_f32_16x16x32_bf16 v[38:41], v[166:169], v[206:209], v[38:41]
	v_mfma_f32_16x16x32_bf16 v[30:33], v[158:161], v[214:217], v[30:33]
	v_mfma_f32_16x16x32_bf16 v[22:25], v[166:169], v[214:217], v[22:25]
	v_mfma_f32_16x16x32_bf16 v[42:45], v[170:173], v[186:189], v[42:45]
	v_mfma_f32_16x16x32_bf16 v[34:37], v[178:181], v[186:189], v[34:37]
	v_mfma_f32_16x16x32_bf16 v[26:29], v[170:173], v[194:197], v[26:29]
	v_mfma_f32_16x16x32_bf16 v[18:21], v[178:181], v[194:197], v[18:21]
	v_mfma_f32_16x16x32_bf16 v[14:17], v[170:173], v[202:205], v[14:17]
	v_mfma_f32_16x16x32_bf16 v[10:13], v[178:181], v[202:205], v[10:13]
	v_mfma_f32_16x16x32_bf16 v[6:9], v[170:173], v[210:213], v[6:9]
	v_mfma_f32_16x16x32_bf16 v[2:5], v[178:181], v[210:213], v[2:5]
	v_mfma_f32_16x16x32_bf16 v[42:45], v[174:177], v[190:193], v[42:45]
	v_mfma_f32_16x16x32_bf16 v[34:37], v[182:185], v[190:193], v[34:37]
	v_mfma_f32_16x16x32_bf16 v[26:29], v[174:177], v[198:201], v[26:29]
	v_mfma_f32_16x16x32_bf16 v[18:21], v[182:185], v[198:201], v[18:21]
	v_mfma_f32_16x16x32_bf16 v[14:17], v[174:177], v[206:209], v[14:17]
	v_mfma_f32_16x16x32_bf16 v[10:13], v[182:185], v[206:209], v[10:13]
	v_mfma_f32_16x16x32_bf16 v[6:9], v[174:177], v[214:217], v[6:9]
	v_mfma_f32_16x16x32_bf16 v[2:5], v[182:185], v[214:217], v[2:5]
	s_barrier
	s_add_i32 s54, s54, 2
	s_add_u32 s28, s28, 0x100
	s_addc_u32 s29, s29, 0
	s_add_u32 s52, s52, 0x100
	s_addc_u32 s53, s53, 0
	s_cmp_gt_u32 s54, 29
	s_cbranch_scc0 .LBB0_1479
	s_and_b64 vcc, exec, s[12:13]
	s_cbranch_vccz .LBB0_1482
	s_barrier

.LBB0_1551:
	s_setprio 0
	v_readlane_b32 s8, v254, 1
	v_readlane_b32 s9, v254, 2
	s_mov_b32 s8, s99
	s_add_i32 s43, s43, 1
	s_mul_i32 s0, s43, s46
	s_waitcnt lgkmcnt(0)
	s_mul_hi_u32 s1, s43, s8
	s_add_i32 s1, s1, s0
	s_mul_i32 s0, s43, s8
	v_readlane_b32 s8, v254, 14
	s_add_u32 s8, s0, s8
	s_addc_u32 s9, s1, s33
	v_cmp_gt_i64_e32 vcc, s[8:9], v[144:145]
	v_cmp_lt_i64_e64 s[0:1], s[8:9], v[142:143]
	s_cbranch_vccnz .LBB0_1557
	s_ashr_i32 s9, s8, 31
	s_lshr_b32 s9, s9, 29
	s_add_i32 s24, s8, s9
	s_and_b32 s9, s24, -8
	s_sub_i32 s25, s8, s9
	s_cmp_gt_i32 s25, -1
	s_mov_b64 s[8:9], -1
	s_cbranch_scc0 .LBB0_1554
	s_lshl_b32 s30, s25, 7
	s_mov_b64 s[8:9], 0

.Lrx_1562_0:
	s_waitcnt vmcnt(24)
	s_waitcnt lgkmcnt(0)
	s_barrier
	v_mfma_f32_16x16x32_bf16 v[126:129], v[154:157], v[186:189], 0
	v_mfma_f32_16x16x32_bf16 v[122:125], v[162:165], v[186:189], 0
	v_mfma_f32_16x16x32_bf16 v[118:121], v[154:157], v[194:197], 0
	v_mfma_f32_16x16x32_bf16 v[110:113], v[162:165], v[194:197], 0
	v_mfma_f32_16x16x32_bf16 v[102:105], v[154:157], v[202:205], 0
	v_mfma_f32_16x16x32_bf16 v[94:97], v[162:165], v[202:205], 0
	v_mfma_f32_16x16x32_bf16 v[86:89], v[154:157], v[210:213], 0
	v_mfma_f32_16x16x32_bf16 v[78:81], v[162:165], v[210:213], 0
	v_mfma_f32_16x16x32_bf16 v[126:129], v[158:161], v[190:193], v[126:129]
	v_mfma_f32_16x16x32_bf16 v[122:125], v[166:169], v[190:193], v[122:125]
	v_mfma_f32_16x16x32_bf16 v[118:121], v[158:161], v[198:201], v[118:121]
	v_mfma_f32_16x16x32_bf16 v[110:113], v[166:169], v[198:201], v[110:113]
	v_mfma_f32_16x16x32_bf16 v[102:105], v[158:161], v[206:209], v[102:105]
	v_mfma_f32_16x16x32_bf16 v[94:97], v[166:169], v[206:209], v[94:97]
	v_mfma_f32_16x16x32_bf16 v[86:89], v[158:161], v[214:217], v[86:89]
	v_mfma_f32_16x16x32_bf16 v[78:81], v[166:169], v[214:217], v[78:81]
	v_mfma_f32_16x16x32_bf16 v[114:117], v[170:173], v[186:189], 0
	v_mfma_f32_16x16x32_bf16 v[106:109], v[178:181], v[186:189], 0
	v_mfma_f32_16x16x32_bf16 v[98:101], v[170:173], v[194:197], 0
	v_mfma_f32_16x16x32_bf16 v[90:93], v[178:181], v[194:197], 0
	v_mfma_f32_16x16x32_bf16 v[82:85], v[170:173], v[202:205], 0
	v_mfma_f32_16x16x32_bf16 v[74:77], v[178:181], v[202:205], 0
	v_mfma_f32_16x16x32_bf16 v[70:73], v[170:173], v[210:213], 0
	v_mfma_f32_16x16x32_bf16 v[66:69], v[178:181], v[210:213], 0
	v_mfma_f32_16x16x32_bf16 v[114:117], v[174:177], v[190:193], v[114:117]
	v_mfma_f32_16x16x32_bf16 v[106:109], v[182:185], v[190:193], v[106:109]
	v_mfma_f32_16x16x32_bf16 v[98:101], v[174:177], v[198:201], v[98:101]
	v_mfma_f32_16x16x32_bf16 v[90:93], v[182:185], v[198:201], v[90:93]
	v_mfma_f32_16x16x32_bf16 v[82:85], v[174:177], v[206:209], v[82:85]
	v_mfma_f32_16x16x32_bf16 v[74:77], v[182:185], v[206:209], v[74:77]
	v_mfma_f32_16x16x32_bf16 v[70:73], v[174:177], v[214:217], v[70:73]
	v_mfma_f32_16x16x32_bf16 v[66:69], v[182:185], v[214:217], v[66:69]
	s_barrier
	s_add_i32 s60, s47, s38
	v_lshl_add_u64 v[146:147], s[28:29], 0, v[132:133]
	s_mov_b32 m0, s60
	ds_read_b128 v[186:189], v152 offset:16384
	ds_read_b128 v[190:193], v152 offset:17408
	ds_read_b128 v[194:197], v152 offset:18432
	ds_read_b128 v[198:201], v152 offset:19456
	ds_read_b128 v[202:205], v152 offset:20480
	ds_read_b128 v[206:209], v152 offset:21504
	ds_read_b128 v[210:213], v152 offset:22528
	ds_read_b128 v[214:217], v152 offset:23552
	global_load_lds_dwordx4 v[146:147], off
	s_add_i32 m0, s60, 0x2000
	s_add_u32 s60, s28, 0x160000
	v_lshl_add_u64 v[218:219], s[28:29], 0, v[136:137]
	s_addc_u32 s61, s29, 0
	s_add_i32 s62, s48, s38
	global_load_lds_dwordx4 v[218:219], off
	v_lshl_add_u64 v[220:221], s[60:61], 0, v[132:133]
	s_mov_b32 m0, s62
	v_lshl_add_u64 v[222:223], s[30:31], 0, v[134:135]
	global_load_lds_dwordx4 v[220:221], off
	v_lshl_add_u64 v[220:221], s[60:61], 0, v[136:137]
	s_add_i32 m0, s62, 0x2000
	s_nop 0
	global_load_lds_dwordx4 v[220:221], off
	v_lshl_add_u64 v[220:221], s[30:31], 0, v[130:131]
	s_mov_b32 m0, s39
	s_nop 0
	global_load_lds_dwordx4 v[220:221], off
	s_mov_b32 m0, s40
	s_nop 0
	global_load_lds_dwordx4 v[222:223], off
	s_cmp_lg_u32 s100, 0
	s_cbranch_scc1 .Lrx_1562_1
	s_waitcnt vmcnt(8)
.Lrx_1562_1:
	s_waitcnt vmcnt(24)
	s_mov_b32 s100, 1
	s_waitcnt lgkmcnt(0)
	s_barrier
	v_mfma_f32_16x16x32_bf16 v[62:65], v[154:157], v[186:189], 0
	v_mfma_f32_16x16x32_bf16 v[58:61], v[162:165], v[186:189], 0
	v_mfma_f32_16x16x32_bf16 v[54:57], v[154:157], v[194:197], 0
	v_mfma_f32_16x16x32_bf16 v[46:49], v[162:165], v[194:197], 0
	v_mfma_f32_16x16x32_bf16 v[38:41], v[154:157], v[202:205], 0
	v_mfma_f32_16x16x32_bf16 v[30:33], v[162:165], v[202:205], 0
	v_mfma_f32_16x16x32_bf16 v[22:25], v[154:157], v[210:213], 0
	v_mfma_f32_16x16x32_bf16 v[14:17], v[162:165], v[210:213], 0
	v_mfma_f32_16x16x32_bf16 v[62:65], v[158:161], v[190:193], v[62:65]
	v_mfma_f32_16x16x32_bf16 v[58:61], v[166:169], v[190:193], v[58:61]
	v_mfma_f32_16x16x32_bf16 v[54:57], v[158:161], v[198:201], v[54:57]
	v_mfma_f32_16x16x32_bf16 v[46:49], v[166:169], v[198:201], v[46:49]
	v_mfma_f32_16x16x32_bf16 v[38:41], v[158:161], v[206:209], v[38:41]
	v_mfma_f32_16x16x32_bf16 v[30:33], v[166:169], v[206:209], v[30:33]
	v_mfma_f32_16x16x32_bf16 v[22:25], v[158:161], v[214:217], v[22:25]
	v_mfma_f32_16x16x32_bf16 v[14:17], v[166:169], v[214:217], v[14:17]
	v_mfma_f32_16x16x32_bf16 v[50:53], v[170:173], v[186:189], 0
	v_mfma_f32_16x16x32_bf16 v[42:45], v[178:181], v[186:189], 0
	v_mfma_f32_16x16x32_bf16 v[34:37], v[170:173], v[194:197], 0
	v_mfma_f32_16x16x32_bf16 v[26:29], v[178:181], v[194:197], 0
	v_mfma_f32_16x16x32_bf16 v[18:21], v[170:173], v[202:205], 0
	v_mfma_f32_16x16x32_bf16 v[10:13], v[178:181], v[202:205], 0
	v_mfma_f32_16x16x32_bf16 v[6:9], v[170:173], v[210:213], 0
	v_mfma_f32_16x16x32_bf16 v[2:5], v[178:181], v[210:213], 0
	v_mfma_f32_16x16x32_bf16 v[50:53], v[174:177], v[190:193], v[50:53]
	v_mfma_f32_16x16x32_bf16 v[42:45], v[182:185], v[190:193], v[42:45]
	v_mfma_f32_16x16x32_bf16 v[34:37], v[174:177], v[198:201], v[34:37]
	v_mfma_f32_16x16x32_bf16 v[26:29], v[182:185], v[198:201], v[26:29]
	v_mfma_f32_16x16x32_bf16 v[18:21], v[174:177], v[206:209], v[18:21]
	v_mfma_f32_16x16x32_bf16 v[10:13], v[182:185], v[206:209], v[10:13]
	v_mfma_f32_16x16x32_bf16 v[6:9], v[174:177], v[214:217], v[6:9]
	v_mfma_f32_16x16x32_bf16 v[2:5], v[182:185], v[214:217], v[2:5]
	s_barrier
	s_add_i32 s60, 0, 0x18000
	v_add_u32_e32 v153, s60, v148
	s_add_i32 s61, 0, 0x1c000
	ds_read_b128 v[154:157], v153
	ds_read_b128 v[158:161], v153 offset:1024
	ds_read_b128 v[162:165], v153 offset:2048
	ds_read_b128 v[166:169], v153 offset:3072
	v_add_u32_e32 v153, s61, v148
	ds_read_b128 v[170:173], v153
	ds_read_b128 v[174:177], v153 offset:1024
	ds_read_b128 v[178:181], v153 offset:2048
	ds_read_b128 v[182:185], v153 offset:3072
	s_add_u32 s30, s30, 0x160000
	s_addc_u32 s31, s31, 0
	s_mov_b32 m0, s41
	v_lshl_add_u64 v[224:225], s[30:31], 0, v[130:131]
	ds_read_b128 v[186:189], v152 offset:32768
	ds_read_b128 v[190:193], v152 offset:33792
	ds_read_b128 v[194:197], v152 offset:34816
	ds_read_b128 v[198:201], v152 offset:35840
	ds_read_b128 v[202:205], v152 offset:36864
	ds_read_b128 v[206:209], v152 offset:37888
	ds_read_b128 v[210:213], v152 offset:38912
	ds_read_b128 v[214:217], v152 offset:39936
	global_load_lds_dwordx4 v[224:225], off
	v_lshl_add_u64 v[224:225], s[30:31], 0, v[134:135]
	s_mov_b32 m0, s42
	s_nop 0
	global_load_lds_dwordx4 v[224:225], off
	s_waitcnt vmcnt(8)
	s_waitcnt lgkmcnt(0)
	s_barrier
	v_mfma_f32_16x16x32_bf16 v[126:129], v[154:157], v[186:189], v[126:129]
	v_mfma_f32_16x16x32_bf16 v[122:125], v[162:165], v[186:189], v[122:125]
	v_mfma_f32_16x16x32_bf16 v[118:121], v[154:157], v[194:197], v[118:121]
	v_mfma_f32_16x16x32_bf16 v[110:113], v[162:165], v[194:197], v[110:113]
	v_mfma_f32_16x16x32_bf16 v[102:105], v[154:157], v[202:205], v[102:105]
	v_mfma_f32_16x16x32_bf16 v[94:97], v[162:165], v[202:205], v[94:97]
	v_mfma_f32_16x16x32_bf16 v[86:89], v[154:157], v[210:213], v[86:89]
	v_mfma_f32_16x16x32_bf16 v[78:81], v[162:165], v[210:213], v[78:81]
	v_mfma_f32_16x16x32_bf16 v[126:129], v[158:161], v[190:193], v[126:129]
	v_mfma_f32_16x16x32_bf16 v[122:125], v[166:169], v[190:193], v[122:125]
	v_mfma_f32_16x16x32_bf16 v[118:121], v[158:161], v[198:201], v[118:121]
	v_mfma_f32_16x16x32_bf16 v[110:113], v[166:169], v[198:201], v[110:113]
	v_mfma_f32_16x16x32_bf16 v[102:105], v[158:161], v[206:209], v[102:105]
	v_mfma_f32_16x16x32_bf16 v[94:97], v[166:169], v[206:209], v[94:97]
	v_mfma_f32_16x16x32_bf16 v[86:89], v[158:161], v[214:217], v[86:89]
	v_mfma_f32_16x16x32_bf16 v[78:81], v[166:169], v[214:217], v[78:81]
	v_mfma_f32_16x16x32_bf16 v[114:117], v[170:173], v[186:189], v[114:117]
	v_mfma_f32_16x16x32_bf16 v[106:109], v[178:181], v[186:189], v[106:109]
	v_mfma_f32_16x16x32_bf16 v[98:101], v[170:173], v[194:197], v[98:101]
	v_mfma_f32_16x16x32_bf16 v[90:93], v[178:181], v[194:197], v[90:93]
	v_mfma_f32_16x16x32_bf16 v[82:85], v[170:173], v[202:205], v[82:85]
	v_mfma_f32_16x16x32_bf16 v[74:77], v[178:181], v[202:205], v[74:77]
	v_mfma_f32_16x16x32_bf16 v[70:73], v[170:173], v[210:213], v[70:73]
	v_mfma_f32_16x16x32_bf16 v[66:69], v[178:181], v[210:213], v[66:69]
	v_mfma_f32_16x16x32_bf16 v[114:117], v[174:177], v[190:193], v[114:117]
	v_mfma_f32_16x16x32_bf16 v[106:109], v[182:185], v[190:193], v[106:109]
	v_mfma_f32_16x16x32_bf16 v[98:101], v[174:177], v[198:201], v[98:101]
	v_mfma_f32_16x16x32_bf16 v[90:93], v[182:185], v[198:201], v[90:93]
	v_mfma_f32_16x16x32_bf16 v[82:85], v[174:177], v[206:209], v[82:85]
	v_mfma_f32_16x16x32_bf16 v[74:77], v[182:185], v[206:209], v[74:77]
	v_mfma_f32_16x16x32_bf16 v[70:73], v[174:177], v[214:217], v[70:73]
	v_mfma_f32_16x16x32_bf16 v[66:69], v[182:185], v[214:217], v[66:69]
	s_barrier
	s_add_i32 s30, s60, s38
	v_lshl_add_u64 v[146:147], v[146:147], 0, s[10:11]
	s_mov_b32 m0, s30
	ds_read_b128 v[186:189], v152 offset:49152
	ds_read_b128 v[190:193], v152 offset:50176
	ds_read_b128 v[194:197], v152 offset:51200
	ds_read_b128 v[198:201], v152 offset:52224
	ds_read_b128 v[202:205], v152 offset:53248
	ds_read_b128 v[206:209], v152 offset:54272
	ds_read_b128 v[210:213], v152 offset:55296
	ds_read_b128 v[214:217], v152 offset:56320
	global_load_lds_dwordx4 v[146:147], off
	s_add_i32 m0, s30, 0x2000
	s_add_u32 s28, s28, 0x160080
	v_lshl_add_u64 v[146:147], v[218:219], 0, s[10:11]
	s_addc_u32 s29, s29, 0
	s_add_i32 s30, s61, s38
	global_load_lds_dwordx4 v[146:147], off
	v_lshl_add_u64 v[146:147], s[28:29], 0, v[132:133]
	s_mov_b32 m0, s30
	s_nop 0
	global_load_lds_dwordx4 v[146:147], off
	v_lshl_add_u64 v[146:147], s[28:29], 0, v[136:137]
	s_add_i32 m0, s30, 0x2000
	s_nop 0
	global_load_lds_dwordx4 v[146:147], off
	v_lshl_add_u64 v[146:147], v[220:221], 0, s[10:11]
	s_mov_b32 m0, s44
	s_nop 0
	global_load_lds_dwordx4 v[146:147], off
	v_lshl_add_u64 v[146:147], v[222:223], 0, s[10:11]
	s_mov_b32 m0, s45
	s_nop 0
	global_load_lds_dwordx4 v[146:147], off
	s_waitcnt vmcnt(8)
	s_waitcnt lgkmcnt(0)
	s_barrier
	v_mfma_f32_16x16x32_bf16 v[62:65], v[154:157], v[186:189], v[62:65]
	v_mfma_f32_16x16x32_bf16 v[58:61], v[162:165], v[186:189], v[58:61]
	v_mfma_f32_16x16x32_bf16 v[54:57], v[154:157], v[194:197], v[54:57]
	v_mfma_f32_16x16x32_bf16 v[46:49], v[162:165], v[194:197], v[46:49]
	v_mfma_f32_16x16x32_bf16 v[38:41], v[154:157], v[202:205], v[38:41]
	v_mfma_f32_16x16x32_bf16 v[30:33], v[162:165], v[202:205], v[30:33]
	v_mfma_f32_16x16x32_bf16 v[22:25], v[154:157], v[210:213], v[22:25]
	v_mfma_f32_16x16x32_bf16 v[14:17], v[162:165], v[210:213], v[14:17]
	v_mfma_f32_16x16x32_bf16 v[62:65], v[158:161], v[190:193], v[62:65]
	v_mfma_f32_16x16x32_bf16 v[58:61], v[166:169], v[190:193], v[58:61]
	v_mfma_f32_16x16x32_bf16 v[54:57], v[158:161], v[198:201], v[54:57]
	v_mfma_f32_16x16x32_bf16 v[46:49], v[166:169], v[198:201], v[46:49]
	v_mfma_f32_16x16x32_bf16 v[38:41], v[158:161], v[206:209], v[38:41]
	v_mfma_f32_16x16x32_bf16 v[30:33], v[166:169], v[206:209], v[30:33]
	v_mfma_f32_16x16x32_bf16 v[22:25], v[158:161], v[214:217], v[22:25]
	v_mfma_f32_16x16x32_bf16 v[14:17], v[166:169], v[214:217], v[14:17]
	v_mfma_f32_16x16x32_bf16 v[50:53], v[170:173], v[186:189], v[50:53]
	v_mfma_f32_16x16x32_bf16 v[42:45], v[178:181], v[186:189], v[42:45]
	v_mfma_f32_16x16x32_bf16 v[34:37], v[170:173], v[194:197], v[34:37]
	v_mfma_f32_16x16x32_bf16 v[26:29], v[178:181], v[194:197], v[26:29]
	v_mfma_f32_16x16x32_bf16 v[18:21], v[170:173], v[202:205], v[18:21]
	v_mfma_f32_16x16x32_bf16 v[10:13], v[178:181], v[202:205], v[10:13]
	v_mfma_f32_16x16x32_bf16 v[6:9], v[170:173], v[210:213], v[6:9]
	v_mfma_f32_16x16x32_bf16 v[2:5], v[178:181], v[210:213], v[2:5]
	v_mfma_f32_16x16x32_bf16 v[50:53], v[174:177], v[190:193], v[50:53]
	v_mfma_f32_16x16x32_bf16 v[42:45], v[182:185], v[190:193], v[42:45]
	v_mfma_f32_16x16x32_bf16 v[34:37], v[174:177], v[198:201], v[34:37]
	v_mfma_f32_16x16x32_bf16 v[26:29], v[182:185], v[198:201], v[26:29]
	v_mfma_f32_16x16x32_bf16 v[18:21], v[174:177], v[206:209], v[18:21]
	v_mfma_f32_16x16x32_bf16 v[10:13], v[182:185], v[206:209], v[10:13]
	v_mfma_f32_16x16x32_bf16 v[6:9], v[174:177], v[214:217], v[6:9]
	v_mfma_f32_16x16x32_bf16 v[2:5], v[182:185], v[214:217], v[2:5]
	s_barrier
	s_add_i32 s59, s59, 2
	s_add_u32 s26, s26, 0x100
	s_addc_u32 s27, s27, 0
	s_add_u32 s57, s57, 0x100
	s_addc_u32 s58, s58, 0
	s_cmpk_gt_u32 s59, 0x55
.LBB0_1562:
	ds_read_b128 v[154:157], v150
	ds_read_b128 v[158:161], v150 offset:1024
	ds_read_b128 v[162:165], v150 offset:2048
	ds_read_b128 v[166:169], v150 offset:3072
	ds_read_b128 v[170:173], v151
	ds_read_b128 v[174:177], v151 offset:1024
	ds_read_b128 v[178:181], v151 offset:2048
	ds_read_b128 v[182:185], v151 offset:3072
	s_add_u32 s28, s26, 0xffea0080
	s_addc_u32 s29, s27, -1
	s_cmpk_eq_i32 s59, 0x54
	s_cselect_b32 s31, s1, s29
	s_cselect_b32 s30, s0, s28
	s_cselect_b32 s29, s25, s58
	s_cselect_b32 s28, s24, s57
	v_lshl_add_u64 v[146:147], s[26:27], 0, v[138:139]
	s_add_i32 m0, s39, 0xc000
	ds_read_b128 v[186:189], v152
	ds_read_b128 v[190:193], v152 offset:1024
	ds_read_b128 v[194:197], v152 offset:2048
	ds_read_b128 v[198:201], v152 offset:3072
	ds_read_b128 v[202:205], v152 offset:4096
	ds_read_b128 v[206:209], v152 offset:5120
	ds_read_b128 v[210:213], v152 offset:6144
	ds_read_b128 v[214:217], v152 offset:7168
	global_load_lds_dwordx4 v[146:147], off
	v_lshl_add_u64 v[146:147], s[26:27], 0, v[140:141]
	s_add_i32 m0, s39, 0xe000
	s_nop 0
	global_load_lds_dwordx4 v[146:147], off
	s_waitcnt vmcnt(8)
	s_waitcnt lgkmcnt(0)
	s_barrier
	v_mfma_f32_16x16x32_bf16 v[126:129], v[154:157], v[186:189], v[126:129]
	v_mfma_f32_16x16x32_bf16 v[122:125], v[162:165], v[186:189], v[122:125]
	v_mfma_f32_16x16x32_bf16 v[118:121], v[154:157], v[194:197], v[118:121]
	v_mfma_f32_16x16x32_bf16 v[110:113], v[162:165], v[194:197], v[110:113]
	v_mfma_f32_16x16x32_bf16 v[102:105], v[154:157], v[202:205], v[102:105]
	v_mfma_f32_16x16x32_bf16 v[94:97], v[162:165], v[202:205], v[94:97]
	v_mfma_f32_16x16x32_bf16 v[86:89], v[154:157], v[210:213], v[86:89]
	v_mfma_f32_16x16x32_bf16 v[78:81], v[162:165], v[210:213], v[78:81]
	v_mfma_f32_16x16x32_bf16 v[126:129], v[158:161], v[190:193], v[126:129]
	v_mfma_f32_16x16x32_bf16 v[122:125], v[166:169], v[190:193], v[122:125]
	v_mfma_f32_16x16x32_bf16 v[118:121], v[158:161], v[198:201], v[118:121]
	v_mfma_f32_16x16x32_bf16 v[110:113], v[166:169], v[198:201], v[110:113]
	v_mfma_f32_16x16x32_bf16 v[102:105], v[158:161], v[206:209], v[102:105]
	v_mfma_f32_16x16x32_bf16 v[94:97], v[166:169], v[206:209], v[94:97]
	v_mfma_f32_16x16x32_bf16 v[86:89], v[158:161], v[214:217], v[86:89]
	v_mfma_f32_16x16x32_bf16 v[78:81], v[166:169], v[214:217], v[78:81]
	v_mfma_f32_16x16x32_bf16 v[114:117], v[170:173], v[186:189], v[114:117]
	v_mfma_f32_16x16x32_bf16 v[106:109], v[178:181], v[186:189], v[106:109]
	v_mfma_f32_16x16x32_bf16 v[98:101], v[170:173], v[194:197], v[98:101]
	v_mfma_f32_16x16x32_bf16 v[90:93], v[178:181], v[194:197], v[90:93]
	v_mfma_f32_16x16x32_bf16 v[82:85], v[170:173], v[202:205], v[82:85]
	v_mfma_f32_16x16x32_bf16 v[74:77], v[178:181], v[202:205], v[74:77]
	v_mfma_f32_16x16x32_bf16 v[70:73], v[170:173], v[210:213], v[70:73]
	v_mfma_f32_16x16x32_bf16 v[66:69], v[178:181], v[210:213], v[66:69]
	v_mfma_f32_16x16x32_bf16 v[114:117], v[174:177], v[190:193], v[114:117]
	v_mfma_f32_16x16x32_bf16 v[106:109], v[182:185], v[190:193], v[106:109]
	v_mfma_f32_16x16x32_bf16 v[98:101], v[174:177], v[198:201], v[98:101]
	v_mfma_f32_16x16x32_bf16 v[90:93], v[182:185], v[198:201], v[90:93]
	v_mfma_f32_16x16x32_bf16 v[82:85], v[174:177], v[206:209], v[82:85]
	v_mfma_f32_16x16x32_bf16 v[74:77], v[182:185], v[206:209], v[74:77]
	v_mfma_f32_16x16x32_bf16 v[70:73], v[174:177], v[214:217], v[70:73]
	v_mfma_f32_16x16x32_bf16 v[66:69], v[182:185], v[214:217], v[66:69]
	s_barrier
	s_add_i32 s60, s47, s38
	v_lshl_add_u64 v[146:147], s[28:29], 0, v[132:133]
	s_mov_b32 m0, s60
	ds_read_b128 v[186:189], v152 offset:16384
	ds_read_b128 v[190:193], v152 offset:17408
	ds_read_b128 v[194:197], v152 offset:18432
	ds_read_b128 v[198:201], v152 offset:19456
	ds_read_b128 v[202:205], v152 offset:20480
	ds_read_b128 v[206:209], v152 offset:21504
	ds_read_b128 v[210:213], v152 offset:22528
	ds_read_b128 v[214:217], v152 offset:23552
	global_load_lds_dwordx4 v[146:147], off
	s_add_i32 m0, s60, 0x2000
	s_add_u32 s60, s28, 0x160000
	v_lshl_add_u64 v[218:219], s[28:29], 0, v[136:137]
	s_addc_u32 s61, s29, 0
	s_add_i32 s62, s48, s38
	global_load_lds_dwordx4 v[218:219], off
	v_lshl_add_u64 v[220:221], s[60:61], 0, v[132:133]
	s_mov_b32 m0, s62
	v_lshl_add_u64 v[222:223], s[30:31], 0, v[134:135]
	global_load_lds_dwordx4 v[220:221], off
	v_lshl_add_u64 v[220:221], s[60:61], 0, v[136:137]
	s_add_i32 m0, s62, 0x2000
	s_nop 0
	global_load_lds_dwordx4 v[220:221], off
	v_lshl_add_u64 v[220:221], s[30:31], 0, v[130:131]
	s_mov_b32 m0, s39
	s_nop 0
	global_load_lds_dwordx4 v[220:221], off
	s_mov_b32 m0, s40
	s_nop 0
	global_load_lds_dwordx4 v[222:223], off
	s_waitcnt vmcnt(8)
	s_waitcnt lgkmcnt(0)
	s_barrier
	v_mfma_f32_16x16x32_bf16 v[62:65], v[154:157], v[186:189], v[62:65]
	v_mfma_f32_16x16x32_bf16 v[58:61], v[162:165], v[186:189], v[58:61]
	v_mfma_f32_16x16x32_bf16 v[54:57], v[154:157], v[194:197], v[54:57]
	v_mfma_f32_16x16x32_bf16 v[46:49], v[162:165], v[194:197], v[46:49]
	v_mfma_f32_16x16x32_bf16 v[38:41], v[154:157], v[202:205], v[38:41]
	v_mfma_f32_16x16x32_bf16 v[30:33], v[162:165], v[202:205], v[30:33]
	v_mfma_f32_16x16x32_bf16 v[22:25], v[154:157], v[210:213], v[22:25]
	v_mfma_f32_16x16x32_bf16 v[14:17], v[162:165], v[210:213], v[14:17]
	v_mfma_f32_16x16x32_bf16 v[62:65], v[158:161], v[190:193], v[62:65]
	v_mfma_f32_16x16x32_bf16 v[58:61], v[166:169], v[190:193], v[58:61]
	v_mfma_f32_16x16x32_bf16 v[54:57], v[158:161], v[198:201], v[54:57]
	v_mfma_f32_16x16x32_bf16 v[46:49], v[166:169], v[198:201], v[46:49]
	v_mfma_f32_16x16x32_bf16 v[38:41], v[158:161], v[206:209], v[38:41]
	v_mfma_f32_16x16x32_bf16 v[30:33], v[166:169], v[206:209], v[30:33]
	v_mfma_f32_16x16x32_bf16 v[22:25], v[158:161], v[214:217], v[22:25]
	v_mfma_f32_16x16x32_bf16 v[14:17], v[166:169], v[214:217], v[14:17]
	v_mfma_f32_16x16x32_bf16 v[50:53], v[170:173], v[186:189], v[50:53]
	v_mfma_f32_16x16x32_bf16 v[42:45], v[178:181], v[186:189], v[42:45]
	v_mfma_f32_16x16x32_bf16 v[34:37], v[170:173], v[194:197], v[34:37]
	v_mfma_f32_16x16x32_bf16 v[26:29], v[178:181], v[194:197], v[26:29]
	v_mfma_f32_16x16x32_bf16 v[18:21], v[170:173], v[202:205], v[18:21]
	v_mfma_f32_16x16x32_bf16 v[10:13], v[178:181], v[202:205], v[10:13]
	v_mfma_f32_16x16x32_bf16 v[6:9], v[170:173], v[210:213], v[6:9]
	v_mfma_f32_16x16x32_bf16 v[2:5], v[178:181], v[210:213], v[2:5]
	v_mfma_f32_16x16x32_bf16 v[50:53], v[174:177], v[190:193], v[50:53]
	v_mfma_f32_16x16x32_bf16 v[42:45], v[182:185], v[190:193], v[42:45]
	v_mfma_f32_16x16x32_bf16 v[34:37], v[174:177], v[198:201], v[34:37]
	v_mfma_f32_16x16x32_bf16 v[26:29], v[182:185], v[198:201], v[26:29]
	v_mfma_f32_16x16x32_bf16 v[18:21], v[174:177], v[206:209], v[18:21]
	v_mfma_f32_16x16x32_bf16 v[10:13], v[182:185], v[206:209], v[10:13]
	v_mfma_f32_16x16x32_bf16 v[6:9], v[174:177], v[214:217], v[6:9]
	v_mfma_f32_16x16x32_bf16 v[2:5], v[182:185], v[214:217], v[2:5]
	s_barrier
	s_add_i32 s60, 0, 0x18000
	v_add_u32_e32 v153, s60, v148
	s_add_i32 s61, 0, 0x1c000
	ds_read_b128 v[154:157], v153
	ds_read_b128 v[158:161], v153 offset:1024
	ds_read_b128 v[162:165], v153 offset:2048
	ds_read_b128 v[166:169], v153 offset:3072
	v_add_u32_e32 v153, s61, v148
	ds_read_b128 v[170:173], v153
	ds_read_b128 v[174:177], v153 offset:1024
	ds_read_b128 v[178:181], v153 offset:2048
	ds_read_b128 v[182:185], v153 offset:3072
	s_add_u32 s30, s30, 0x160000
	s_addc_u32 s31, s31, 0
	s_mov_b32 m0, s41
	v_lshl_add_u64 v[224:225], s[30:31], 0, v[130:131]
	ds_read_b128 v[186:189], v152 offset:32768
	ds_read_b128 v[190:193], v152 offset:33792
	ds_read_b128 v[194:197], v152 offset:34816
	ds_read_b128 v[198:201], v152 offset:35840
	ds_read_b128 v[202:205], v152 offset:36864
	ds_read_b128 v[206:209], v152 offset:37888
	ds_read_b128 v[210:213], v152 offset:38912
	ds_read_b128 v[214:217], v152 offset:39936
	global_load_lds_dwordx4 v[224:225], off
	v_lshl_add_u64 v[224:225], s[30:31], 0, v[134:135]
	s_mov_b32 m0, s42
	s_nop 0
	global_load_lds_dwordx4 v[224:225], off
	s_waitcnt vmcnt(8)
	s_waitcnt lgkmcnt(0)
	s_barrier
	v_mfma_f32_16x16x32_bf16 v[126:129], v[154:157], v[186:189], v[126:129]
	v_mfma_f32_16x16x32_bf16 v[122:125], v[162:165], v[186:189], v[122:125]
	v_mfma_f32_16x16x32_bf16 v[118:121], v[154:157], v[194:197], v[118:121]
	v_mfma_f32_16x16x32_bf16 v[110:113], v[162:165], v[194:197], v[110:113]
	v_mfma_f32_16x16x32_bf16 v[102:105], v[154:157], v[202:205], v[102:105]
	v_mfma_f32_16x16x32_bf16 v[94:97], v[162:165], v[202:205], v[94:97]
	v_mfma_f32_16x16x32_bf16 v[86:89], v[154:157], v[210:213], v[86:89]
	v_mfma_f32_16x16x32_bf16 v[78:81], v[162:165], v[210:213], v[78:81]
	v_mfma_f32_16x16x32_bf16 v[126:129], v[158:161], v[190:193], v[126:129]
	v_mfma_f32_16x16x32_bf16 v[122:125], v[166:169], v[190:193], v[122:125]
	v_mfma_f32_16x16x32_bf16 v[118:121], v[158:161], v[198:201], v[118:121]
	v_mfma_f32_16x16x32_bf16 v[110:113], v[166:169], v[198:201], v[110:113]
	v_mfma_f32_16x16x32_bf16 v[102:105], v[158:161], v[206:209], v[102:105]
	v_mfma_f32_16x16x32_bf16 v[94:97], v[166:169], v[206:209], v[94:97]
	v_mfma_f32_16x16x32_bf16 v[86:89], v[158:161], v[214:217], v[86:89]
	v_mfma_f32_16x16x32_bf16 v[78:81], v[166:169], v[214:217], v[78:81]
	v_mfma_f32_16x16x32_bf16 v[114:117], v[170:173], v[186:189], v[114:117]
	v_mfma_f32_16x16x32_bf16 v[106:109], v[178:181], v[186:189], v[106:109]
	v_mfma_f32_16x16x32_bf16 v[98:101], v[170:173], v[194:197], v[98:101]
	v_mfma_f32_16x16x32_bf16 v[90:93], v[178:181], v[194:197], v[90:93]
	v_mfma_f32_16x16x32_bf16 v[82:85], v[170:173], v[202:205], v[82:85]
	v_mfma_f32_16x16x32_bf16 v[74:77], v[178:181], v[202:205], v[74:77]
	v_mfma_f32_16x16x32_bf16 v[70:73], v[170:173], v[210:213], v[70:73]
	v_mfma_f32_16x16x32_bf16 v[66:69], v[178:181], v[210:213], v[66:69]
	v_mfma_f32_16x16x32_bf16 v[114:117], v[174:177], v[190:193], v[114:117]
	v_mfma_f32_16x16x32_bf16 v[106:109], v[182:185], v[190:193], v[106:109]
	v_mfma_f32_16x16x32_bf16 v[98:101], v[174:177], v[198:201], v[98:101]
	v_mfma_f32_16x16x32_bf16 v[90:93], v[182:185], v[198:201], v[90:93]
	v_mfma_f32_16x16x32_bf16 v[82:85], v[174:177], v[206:209], v[82:85]
	v_mfma_f32_16x16x32_bf16 v[74:77], v[182:185], v[206:209], v[74:77]
	v_mfma_f32_16x16x32_bf16 v[70:73], v[174:177], v[214:217], v[70:73]
	v_mfma_f32_16x16x32_bf16 v[66:69], v[182:185], v[214:217], v[66:69]
	s_barrier
	s_add_i32 s30, s60, s38
	v_lshl_add_u64 v[146:147], v[146:147], 0, s[10:11]
	s_mov_b32 m0, s30
	ds_read_b128 v[186:189], v152 offset:49152
	ds_read_b128 v[190:193], v152 offset:50176
	ds_read_b128 v[194:197], v152 offset:51200
	ds_read_b128 v[198:201], v152 offset:52224
	ds_read_b128 v[202:205], v152 offset:53248
	ds_read_b128 v[206:209], v152 offset:54272
	ds_read_b128 v[210:213], v152 offset:55296
	ds_read_b128 v[214:217], v152 offset:56320
	global_load_lds_dwordx4 v[146:147], off
	s_add_i32 m0, s30, 0x2000
	s_add_u32 s28, s28, 0x160080
	v_lshl_add_u64 v[146:147], v[218:219], 0, s[10:11]
	s_addc_u32 s29, s29, 0
	s_add_i32 s30, s61, s38
	global_load_lds_dwordx4 v[146:147], off
	v_lshl_add_u64 v[146:147], s[28:29], 0, v[132:133]
	s_mov_b32 m0, s30
	s_nop 0
	global_load_lds_dwordx4 v[146:147], off
	v_lshl_add_u64 v[146:147], s[28:29], 0, v[136:137]
	s_add_i32 m0, s30, 0x2000
	s_nop 0
	global_load_lds_dwordx4 v[146:147], off
	v_lshl_add_u64 v[146:147], v[220:221], 0, s[10:11]
	s_mov_b32 m0, s44
	s_nop 0
	global_load_lds_dwordx4 v[146:147], off
	v_lshl_add_u64 v[146:147], v[222:223], 0, s[10:11]
	s_mov_b32 m0, s45
	s_nop 0
	global_load_lds_dwordx4 v[146:147], off
	s_waitcnt vmcnt(8)
	s_waitcnt lgkmcnt(0)
	s_barrier
	v_mfma_f32_16x16x32_bf16 v[62:65], v[154:157], v[186:189], v[62:65]
	v_mfma_f32_16x16x32_bf16 v[58:61], v[162:165], v[186:189], v[58:61]
	v_mfma_f32_16x16x32_bf16 v[54:57], v[154:157], v[194:197], v[54:57]
	v_mfma_f32_16x16x32_bf16 v[46:49], v[162:165], v[194:197], v[46:49]
	v_mfma_f32_16x16x32_bf16 v[38:41], v[154:157], v[202:205], v[38:41]
	v_mfma_f32_16x16x32_bf16 v[30:33], v[162:165], v[202:205], v[30:33]
	v_mfma_f32_16x16x32_bf16 v[22:25], v[154:157], v[210:213], v[22:25]
	v_mfma_f32_16x16x32_bf16 v[14:17], v[162:165], v[210:213], v[14:17]
	v_mfma_f32_16x16x32_bf16 v[62:65], v[158:161], v[190:193], v[62:65]
	v_mfma_f32_16x16x32_bf16 v[58:61], v[166:169], v[190:193], v[58:61]
	v_mfma_f32_16x16x32_bf16 v[54:57], v[158:161], v[198:201], v[54:57]
	v_mfma_f32_16x16x32_bf16 v[46:49], v[166:169], v[198:201], v[46:49]
	v_mfma_f32_16x16x32_bf16 v[38:41], v[158:161], v[206:209], v[38:41]
	v_mfma_f32_16x16x32_bf16 v[30:33], v[166:169], v[206:209], v[30:33]
	v_mfma_f32_16x16x32_bf16 v[22:25], v[158:161], v[214:217], v[22:25]
	v_mfma_f32_16x16x32_bf16 v[14:17], v[166:169], v[214:217], v[14:17]
	v_mfma_f32_16x16x32_bf16 v[50:53], v[170:173], v[186:189], v[50:53]
	v_mfma_f32_16x16x32_bf16 v[42:45], v[178:181], v[186:189], v[42:45]
	v_mfma_f32_16x16x32_bf16 v[34:37], v[170:173], v[194:197], v[34:37]
	v_mfma_f32_16x16x32_bf16 v[26:29], v[178:181], v[194:197], v[26:29]
	v_mfma_f32_16x16x32_bf16 v[18:21], v[170:173], v[202:205], v[18:21]
	v_mfma_f32_16x16x32_bf16 v[10:13], v[178:181], v[202:205], v[10:13]
	v_mfma_f32_16x16x32_bf16 v[6:9], v[170:173], v[210:213], v[6:9]
	v_mfma_f32_16x16x32_bf16 v[2:5], v[178:181], v[210:213], v[2:5]
	v_mfma_f32_16x16x32_bf16 v[50:53], v[174:177], v[190:193], v[50:53]
	v_mfma_f32_16x16x32_bf16 v[42:45], v[182:185], v[190:193], v[42:45]
	v_mfma_f32_16x16x32_bf16 v[34:37], v[174:177], v[198:201], v[34:37]
	v_mfma_f32_16x16x32_bf16 v[26:29], v[182:185], v[198:201], v[26:29]
	v_mfma_f32_16x16x32_bf16 v[18:21], v[174:177], v[206:209], v[18:21]
	v_mfma_f32_16x16x32_bf16 v[10:13], v[182:185], v[206:209], v[10:13]
	v_mfma_f32_16x16x32_bf16 v[6:9], v[174:177], v[214:217], v[6:9]
	v_mfma_f32_16x16x32_bf16 v[2:5], v[182:185], v[214:217], v[2:5]
	s_barrier
	s_add_i32 s59, s59, 2
	s_add_u32 s26, s26, 0x100
	s_addc_u32 s27, s27, 0
	s_add_u32 s57, s57, 0x100
	s_addc_u32 s58, s58, 0
	s_cmpk_gt_u32 s59, 0x55
	s_cbranch_scc0 .LBB0_1562
	s_and_b64 vcc, exec, s[12:13]
	s_cbranch_vccz .LBB0_1565
	s_barrier

.LBB0_1694:
	s_setprio 0
	v_readlane_b32 s38, v254, 1
	v_readlane_b32 s39, v254, 2
	s_mov_b32 s35, s99
	s_add_i32 s57, s57, 1
	s_mul_i32 s10, s57, s63
	s_waitcnt lgkmcnt(0)
	s_mul_hi_u32 s11, s57, s35
	s_add_i32 s11, s11, s10
	s_mul_i32 s10, s57, s35
	v_readlane_b32 s35, v254, 14
	s_add_u32 s38, s10, s35
	s_addc_u32 s39, s11, s64
	v_cmp_gt_i64_e32 vcc, s[38:39], v[154:155]
	v_cmp_lt_i64_e64 s[10:11], s[38:39], v[152:153]
	s_cbranch_vccnz .LBB0_1696
	s_ashr_i32 s34, s38, 31
	s_lshr_b32 s34, s34, 29
	s_add_i32 s34, s38, s34
	s_ashr_i32 s35, s34, 3
	s_and_b32 s34, s34, -8
	s_sub_i32 s34, s38, s34
	s_cmp_lt_i32 s34, 0
	s_movk_i32 s36, 0x191
	s_cselect_b32 s36, s36, 0x190
	s_mul_i32 s34, s34, s36
	s_add_i32 s34, s34, s35
	s_mul_hi_i32 s35, s34, 0x51eb851f
	s_lshr_b32 s36, s35, 31
	s_ashr_i32 s35, s35, 6
	s_add_i32 s35, s35, s36
	s_lshl_b32 s36, s35, 3
	s_sub_i32 s37, 0x80, s36
	s_min_i32 s37, s37, 8
	s_abs_i32 s38, s37
	v_cvt_f32_u32_e32 v2, s38
	s_sub_i32 s40, 0, s38
	s_mulk_i32 s35, 0xc8
	s_sub_i32 s35, s34, s35
	v_rcp_iflag_f32_e32 v2, v2
	s_abs_i32 s34, s35
	s_xor_b32 s39, s35, s37
	s_ashr_i32 s39, s39, 31
	v_mul_f32_e32 v2, 0x4f7ffffe, v2
	v_cvt_u32_f32_e32 v2, v2
	s_nop 0
	v_readfirstlane_b32 s41, v2
	s_mul_i32 s40, s40, s41
	s_mul_hi_u32 s40, s41, s40
	s_add_i32 s41, s41, s40
	s_mul_hi_u32 s40, s34, s41
	s_mul_i32 s41, s40, s38
	s_sub_i32 s34, s34, s41
	s_add_i32 s43, s40, 1
	s_sub_i32 s41, s34, s38
	s_cmp_ge_u32 s34, s38
	s_cselect_b32 s40, s43, s40
	s_cselect_b32 s34, s41, s34
	s_add_i32 s41, s40, 1
	s_cmp_ge_u32 s34, s38
	s_cselect_b32 s34, s41, s40
	s_xor_b32 s34, s34, s39
	s_sub_i32 s34, s34, s39
	s_mul_i32 s37, s34, s37
	s_sub_i32 s35, s35, s37
	s_add_i32 s36, s36, s35
.LBB0_1696:
	s_ashr_i32 s37, s36, 31
	s_lshl_b64 s[38:39], s[36:37], 20
	s_add_u32 s38, s20, s38
	s_addc_u32 s39, s21, s39
	s_and_b64 s[40:41], s[10:11], exec
	s_cselect_b32 s37, s39, s47
	s_cselect_b32 s43, s38, s46
	s_ashr_i32 s35, s34, 31
	s_lshl_b64 s[40:41], s[34:35], 20
	s_add_u32 s40, s23, s40
	s_addc_u32 s41, s33, s41
	s_and_b64 s[50:51], s[10:11], exec
	s_cselect_b32 s35, s41, s49
	s_cselect_b32 s45, s40, s48
	s_lshl_b32 s50, s44, 8
	s_ashr_i32 s51, s50, 31
	v_lshl_add_u64 v[238:239], s[50:51], 2, v[140:141]
	global_load_dword v240, v[238:239], off
	global_load_dword v242, v[238:239], off offset:64
	global_load_dword v244, v[238:239], off offset:128
	global_load_dword v246, v[238:239], off offset:192
	global_load_dword v248, v[238:239], off offset:512
	global_load_dword v250, v[238:239], off offset:576
	global_load_dword v252, v[238:239], off offset:640
	global_load_dword v238, v[238:239], off offset:704
	s_add_u32 s46, s46, 0x80080
	s_addc_u32 s47, s47, 0
	s_add_u32 s69, s48, 0x100
	s_addc_u32 s70, s49, 0
	s_mov_b32 s71, -2
	s_waitcnt vmcnt(0)
	ds_read_b128 v[156:159], v176
	ds_read_b128 v[160:163], v176 offset:1024
	ds_read_b128 v[164:167], v176 offset:2048
	ds_read_b128 v[168:171], v176 offset:3072
	ds_read_b128 v[180:183], v177
	ds_read_b128 v[184:187], v177 offset:1024
	ds_read_b128 v[188:191], v177 offset:2048
	ds_read_b128 v[192:195], v177 offset:3072
	s_add_u32 s48, s46, 0xfff80080
	s_addc_u32 s49, s47, -1
	s_cmp_eq_u32 s71, 28
	s_cselect_b32 s51, s37, s49
	s_cselect_b32 s50, s43, s48
	s_cselect_b32 s49, s35, s70
	s_cselect_b32 s48, s45, s69
	v_lshl_add_u64 v[172:173], s[46:47], 0, v[148:149]
	s_add_i32 m0, s53, 0xc000
	ds_read_b128 v[196:199], v178
	ds_read_b128 v[200:203], v178 offset:1024
	ds_read_b128 v[204:207], v178 offset:2048
	ds_read_b128 v[208:211], v178 offset:3072
	ds_read_b128 v[212:215], v178 offset:4096
	ds_read_b128 v[216:219], v178 offset:5120
	ds_read_b128 v[220:223], v178 offset:6144
	ds_read_b128 v[224:227], v178 offset:7168
	global_load_lds_dwordx4 v[172:173], off
	v_lshl_add_u64 v[172:173], s[46:47], 0, v[150:151]
	s_add_i32 m0, s53, 0xe000
	s_nop 0
	global_load_lds_dwordx4 v[172:173], off
	s_waitcnt vmcnt(8)
	s_waitcnt lgkmcnt(0)
	s_barrier
	v_mfma_f32_16x16x32_bf16 v[126:129], v[156:159], v[196:199], 0
	v_mfma_f32_16x16x32_bf16 v[122:125], v[164:167], v[196:199], 0
	v_mfma_f32_16x16x32_bf16 v[118:121], v[156:159], v[204:207], 0
	v_mfma_f32_16x16x32_bf16 v[114:117], v[164:167], v[204:207], 0
	v_mfma_f32_16x16x32_bf16 v[110:113], v[156:159], v[212:215], 0
	v_mfma_f32_16x16x32_bf16 v[106:109], v[164:167], v[212:215], 0
	v_mfma_f32_16x16x32_bf16 v[102:105], v[156:159], v[220:223], 0
	v_mfma_f32_16x16x32_bf16 v[98:101], v[164:167], v[220:223], 0
	v_mfma_f32_16x16x32_bf16 v[126:129], v[160:163], v[200:203], v[126:129]
	v_mfma_f32_16x16x32_bf16 v[122:125], v[168:171], v[200:203], v[122:125]
	v_mfma_f32_16x16x32_bf16 v[118:121], v[160:163], v[208:211], v[118:121]
	v_mfma_f32_16x16x32_bf16 v[114:117], v[168:171], v[208:211], v[114:117]
	v_mfma_f32_16x16x32_bf16 v[110:113], v[160:163], v[216:219], v[110:113]
	v_mfma_f32_16x16x32_bf16 v[106:109], v[168:171], v[216:219], v[106:109]
	v_mfma_f32_16x16x32_bf16 v[102:105], v[160:163], v[224:227], v[102:105]
	v_mfma_f32_16x16x32_bf16 v[98:101], v[168:171], v[224:227], v[98:101]
	v_mfma_f32_16x16x32_bf16 v[38:41], v[180:183], v[196:199], 0
	v_mfma_f32_16x16x32_bf16 v[34:37], v[188:191], v[196:199], 0
	v_mfma_f32_16x16x32_bf16 v[46:49], v[180:183], v[204:207], 0
	v_mfma_f32_16x16x32_bf16 v[42:45], v[188:191], v[204:207], 0
	v_mfma_f32_16x16x32_bf16 v[54:57], v[180:183], v[212:215], 0
	v_mfma_f32_16x16x32_bf16 v[50:53], v[188:191], v[212:215], 0
	v_mfma_f32_16x16x32_bf16 v[62:65], v[180:183], v[220:223], 0
	v_mfma_f32_16x16x32_bf16 v[58:61], v[188:191], v[220:223], 0
	v_mfma_f32_16x16x32_bf16 v[38:41], v[184:187], v[200:203], v[38:41]
	v_mfma_f32_16x16x32_bf16 v[34:37], v[192:195], v[200:203], v[34:37]
	v_mfma_f32_16x16x32_bf16 v[46:49], v[184:187], v[208:211], v[46:49]
	v_mfma_f32_16x16x32_bf16 v[42:45], v[192:195], v[208:211], v[42:45]
	v_mfma_f32_16x16x32_bf16 v[54:57], v[184:187], v[216:219], v[54:57]
	v_mfma_f32_16x16x32_bf16 v[50:53], v[192:195], v[216:219], v[50:53]
	v_mfma_f32_16x16x32_bf16 v[62:65], v[184:187], v[224:227], v[62:65]
	v_mfma_f32_16x16x32_bf16 v[58:61], v[192:195], v[224:227], v[58:61]
	s_barrier
	s_add_i32 s72, s65, s52
	v_lshl_add_u64 v[172:173], s[48:49], 0, v[132:133]
	s_mov_b32 m0, s72
	ds_read_b128 v[196:199], v178 offset:16384
	ds_read_b128 v[200:203], v178 offset:17408
	ds_read_b128 v[204:207], v178 offset:18432
	ds_read_b128 v[208:211], v178 offset:19456
	ds_read_b128 v[212:215], v178 offset:20480
	ds_read_b128 v[216:219], v178 offset:21504
	ds_read_b128 v[220:223], v178 offset:22528
	ds_read_b128 v[224:227], v178 offset:23552
	global_load_lds_dwordx4 v[172:173], off
	s_add_i32 m0, s72, 0x2000
	s_add_u32 s72, s48, 0x80000
	v_lshl_add_u64 v[228:229], s[48:49], 0, v[136:137]
	s_addc_u32 s73, s49, 0
	s_add_i32 s74, s66, s52
	global_load_lds_dwordx4 v[228:229], off
	v_lshl_add_u64 v[230:231], s[72:73], 0, v[132:133]
	s_mov_b32 m0, s74
	v_lshl_add_u64 v[232:233], s[50:51], 0, v[134:135]
	global_load_lds_dwordx4 v[230:231], off
	v_lshl_add_u64 v[230:231], s[72:73], 0, v[136:137]
	s_add_i32 m0, s74, 0x2000
	s_nop 0
	global_load_lds_dwordx4 v[230:231], off
	v_lshl_add_u64 v[230:231], s[50:51], 0, v[130:131]
	s_mov_b32 m0, s53
	s_nop 0
	global_load_lds_dwordx4 v[230:231], off
	s_mov_b32 m0, s54
	s_nop 0
	global_load_lds_dwordx4 v[232:233], off
	s_waitcnt vmcnt(8)
	s_waitcnt lgkmcnt(0)
	s_barrier
	v_mfma_f32_16x16x32_bf16 v[94:97], v[156:159], v[196:199], 0
	v_mfma_f32_16x16x32_bf16 v[90:93], v[164:167], v[196:199], 0
	v_mfma_f32_16x16x32_bf16 v[86:89], v[156:159], v[204:207], 0
	v_mfma_f32_16x16x32_bf16 v[82:85], v[164:167], v[204:207], 0
	v_mfma_f32_16x16x32_bf16 v[78:81], v[156:159], v[212:215], 0
	v_mfma_f32_16x16x32_bf16 v[74:77], v[164:167], v[212:215], 0
	v_mfma_f32_16x16x32_bf16 v[70:73], v[156:159], v[220:223], 0
	v_mfma_f32_16x16x32_bf16 v[66:69], v[164:167], v[220:223], 0
	v_mfma_f32_16x16x32_bf16 v[94:97], v[160:163], v[200:203], v[94:97]
	v_mfma_f32_16x16x32_bf16 v[90:93], v[168:171], v[200:203], v[90:93]
	v_mfma_f32_16x16x32_bf16 v[86:89], v[160:163], v[208:211], v[86:89]
	v_mfma_f32_16x16x32_bf16 v[82:85], v[168:171], v[208:211], v[82:85]
	v_mfma_f32_16x16x32_bf16 v[78:81], v[160:163], v[216:219], v[78:81]
	v_mfma_f32_16x16x32_bf16 v[74:77], v[168:171], v[216:219], v[74:77]
	v_mfma_f32_16x16x32_bf16 v[70:73], v[160:163], v[224:227], v[70:73]
	v_mfma_f32_16x16x32_bf16 v[66:69], v[168:171], v[224:227], v[66:69]
	v_mfma_f32_16x16x32_bf16 v[6:9], v[180:183], v[196:199], 0
	v_mfma_f32_16x16x32_bf16 v[2:5], v[188:191], v[196:199], 0
	v_mfma_f32_16x16x32_bf16 v[18:21], v[180:183], v[204:207], 0
	v_mfma_f32_16x16x32_bf16 v[14:17], v[188:191], v[204:207], 0
	v_mfma_f32_16x16x32_bf16 v[26:29], v[180:183], v[212:215], 0
	v_mfma_f32_16x16x32_bf16 v[22:25], v[188:191], v[212:215], 0
	v_mfma_f32_16x16x32_bf16 v[30:33], v[180:183], v[220:223], 0
	v_mfma_f32_16x16x32_bf16 v[10:13], v[188:191], v[220:223], 0
	v_mfma_f32_16x16x32_bf16 v[6:9], v[184:187], v[200:203], v[6:9]
	v_mfma_f32_16x16x32_bf16 v[2:5], v[192:195], v[200:203], v[2:5]
	v_mfma_f32_16x16x32_bf16 v[18:21], v[184:187], v[208:211], v[18:21]
	v_mfma_f32_16x16x32_bf16 v[14:17], v[192:195], v[208:211], v[14:17]
	v_mfma_f32_16x16x32_bf16 v[26:29], v[184:187], v[216:219], v[26:29]
	v_mfma_f32_16x16x32_bf16 v[22:25], v[192:195], v[216:219], v[22:25]
	v_mfma_f32_16x16x32_bf16 v[30:33], v[184:187], v[224:227], v[30:33]
	v_mfma_f32_16x16x32_bf16 v[10:13], v[192:195], v[224:227], v[10:13]
	s_barrier
	s_add_i32 s72, 0, 0x18000
	v_add_u32_e32 v138, s72, v174
	s_add_i32 s73, 0, 0x1c000
	ds_read_b128 v[156:159], v138
	ds_read_b128 v[160:163], v138 offset:1024
	ds_read_b128 v[164:167], v138 offset:2048
	ds_read_b128 v[168:171], v138 offset:3072
	v_add_u32_e32 v138, s73, v174
	ds_read_b128 v[180:183], v138
	ds_read_b128 v[184:187], v138 offset:1024
	ds_read_b128 v[188:191], v138 offset:2048
	ds_read_b128 v[192:195], v138 offset:3072
	s_add_u32 s50, s50, 0x80000
	s_addc_u32 s51, s51, 0
	s_mov_b32 m0, s55
	v_lshl_add_u64 v[234:235], s[50:51], 0, v[130:131]
	ds_read_b128 v[196:199], v178 offset:32768
	ds_read_b128 v[200:203], v178 offset:33792
	ds_read_b128 v[204:207], v178 offset:34816
	ds_read_b128 v[208:211], v178 offset:35840
	ds_read_b128 v[212:215], v178 offset:36864
	ds_read_b128 v[216:219], v178 offset:37888
	ds_read_b128 v[220:223], v178 offset:38912
	ds_read_b128 v[224:227], v178 offset:39936
	global_load_lds_dwordx4 v[234:235], off
	v_lshl_add_u64 v[234:235], s[50:51], 0, v[134:135]
	s_mov_b32 m0, s56
	s_nop 0
	global_load_lds_dwordx4 v[234:235], off
	s_waitcnt vmcnt(8)
	s_waitcnt lgkmcnt(0)
	s_barrier
	v_mfma_f32_16x16x32_bf16 v[126:129], v[156:159], v[196:199], v[126:129]
	v_mfma_f32_16x16x32_bf16 v[122:125], v[164:167], v[196:199], v[122:125]
	v_mfma_f32_16x16x32_bf16 v[118:121], v[156:159], v[204:207], v[118:121]
	v_mfma_f32_16x16x32_bf16 v[114:117], v[164:167], v[204:207], v[114:117]
	v_mfma_f32_16x16x32_bf16 v[110:113], v[156:159], v[212:215], v[110:113]
	v_mfma_f32_16x16x32_bf16 v[106:109], v[164:167], v[212:215], v[106:109]
	v_mfma_f32_16x16x32_bf16 v[102:105], v[156:159], v[220:223], v[102:105]
	v_mfma_f32_16x16x32_bf16 v[98:101], v[164:167], v[220:223], v[98:101]
	v_mfma_f32_16x16x32_bf16 v[126:129], v[160:163], v[200:203], v[126:129]
	v_mfma_f32_16x16x32_bf16 v[122:125], v[168:171], v[200:203], v[122:125]
	v_mfma_f32_16x16x32_bf16 v[118:121], v[160:163], v[208:211], v[118:121]
	v_mfma_f32_16x16x32_bf16 v[114:117], v[168:171], v[208:211], v[114:117]
	v_mfma_f32_16x16x32_bf16 v[110:113], v[160:163], v[216:219], v[110:113]
	v_mfma_f32_16x16x32_bf16 v[106:109], v[168:171], v[216:219], v[106:109]
	v_mfma_f32_16x16x32_bf16 v[102:105], v[160:163], v[224:227], v[102:105]
	v_mfma_f32_16x16x32_bf16 v[98:101], v[168:171], v[224:227], v[98:101]
	v_mfma_f32_16x16x32_bf16 v[38:41], v[180:183], v[196:199], v[38:41]
	v_mfma_f32_16x16x32_bf16 v[34:37], v[188:191], v[196:199], v[34:37]
	v_mfma_f32_16x16x32_bf16 v[46:49], v[180:183], v[204:207], v[46:49]
	v_mfma_f32_16x16x32_bf16 v[42:45], v[188:191], v[204:207], v[42:45]
	v_mfma_f32_16x16x32_bf16 v[54:57], v[180:183], v[212:215], v[54:57]
	v_mfma_f32_16x16x32_bf16 v[50:53], v[188:191], v[212:215], v[50:53]
	v_mfma_f32_16x16x32_bf16 v[62:65], v[180:183], v[220:223], v[62:65]
	v_mfma_f32_16x16x32_bf16 v[58:61], v[188:191], v[220:223], v[58:61]
	v_mfma_f32_16x16x32_bf16 v[38:41], v[184:187], v[200:203], v[38:41]
	v_mfma_f32_16x16x32_bf16 v[34:37], v[192:195], v[200:203], v[34:37]
	v_mfma_f32_16x16x32_bf16 v[46:49], v[184:187], v[208:211], v[46:49]
	v_mfma_f32_16x16x32_bf16 v[42:45], v[192:195], v[208:211], v[42:45]
	v_mfma_f32_16x16x32_bf16 v[54:57], v[184:187], v[216:219], v[54:57]
	v_mfma_f32_16x16x32_bf16 v[50:53], v[192:195], v[216:219], v[50:53]
	v_mfma_f32_16x16x32_bf16 v[62:65], v[184:187], v[224:227], v[62:65]
	v_mfma_f32_16x16x32_bf16 v[58:61], v[192:195], v[224:227], v[58:61]
	s_barrier
	s_add_i32 s50, s72, s52
	v_lshl_add_u64 v[172:173], v[172:173], 0, s[6:7]
	s_mov_b32 m0, s50
	ds_read_b128 v[196:199], v178 offset:49152
	ds_read_b128 v[200:203], v178 offset:50176
	ds_read_b128 v[204:207], v178 offset:51200
	ds_read_b128 v[208:211], v178 offset:52224
	ds_read_b128 v[212:215], v178 offset:53248
	ds_read_b128 v[216:219], v178 offset:54272
	ds_read_b128 v[220:223], v178 offset:55296
	ds_read_b128 v[224:227], v178 offset:56320
	global_load_lds_dwordx4 v[172:173], off
	s_add_i32 m0, s50, 0x2000
	s_add_u32 s48, s48, 0x80080
	v_lshl_add_u64 v[172:173], v[228:229], 0, s[6:7]
	s_addc_u32 s49, s49, 0
	s_add_i32 s50, s73, s52
	global_load_lds_dwordx4 v[172:173], off
	v_lshl_add_u64 v[172:173], s[48:49], 0, v[132:133]
	s_mov_b32 m0, s50
	s_nop 0
	global_load_lds_dwordx4 v[172:173], off
	v_lshl_add_u64 v[172:173], s[48:49], 0, v[136:137]
	s_add_i32 m0, s50, 0x2000
	s_nop 0
	global_load_lds_dwordx4 v[172:173], off
	v_lshl_add_u64 v[172:173], v[230:231], 0, s[6:7]
	s_mov_b32 m0, s61
	s_nop 0
	global_load_lds_dwordx4 v[172:173], off
	v_lshl_add_u64 v[172:173], v[232:233], 0, s[6:7]
	s_mov_b32 m0, s62
	s_nop 0
	global_load_lds_dwordx4 v[172:173], off
	s_waitcnt vmcnt(8)
	s_waitcnt lgkmcnt(0)
	s_barrier
	v_mfma_f32_16x16x32_bf16 v[94:97], v[156:159], v[196:199], v[94:97]
	v_mfma_f32_16x16x32_bf16 v[90:93], v[164:167], v[196:199], v[90:93]
	v_mfma_f32_16x16x32_bf16 v[86:89], v[156:159], v[204:207], v[86:89]
	v_mfma_f32_16x16x32_bf16 v[82:85], v[164:167], v[204:207], v[82:85]
	v_mfma_f32_16x16x32_bf16 v[78:81], v[156:159], v[212:215], v[78:81]
	v_mfma_f32_16x16x32_bf16 v[74:77], v[164:167], v[212:215], v[74:77]
	v_mfma_f32_16x16x32_bf16 v[70:73], v[156:159], v[220:223], v[70:73]
	v_mfma_f32_16x16x32_bf16 v[66:69], v[164:167], v[220:223], v[66:69]
	v_mfma_f32_16x16x32_bf16 v[94:97], v[160:163], v[200:203], v[94:97]
	v_mfma_f32_16x16x32_bf16 v[90:93], v[168:171], v[200:203], v[90:93]
	v_mfma_f32_16x16x32_bf16 v[86:89], v[160:163], v[208:211], v[86:89]
	v_mfma_f32_16x16x32_bf16 v[82:85], v[168:171], v[208:211], v[82:85]
	v_mfma_f32_16x16x32_bf16 v[78:81], v[160:163], v[216:219], v[78:81]
	v_mfma_f32_16x16x32_bf16 v[74:77], v[168:171], v[216:219], v[74:77]
	v_mfma_f32_16x16x32_bf16 v[70:73], v[160:163], v[224:227], v[70:73]
	v_mfma_f32_16x16x32_bf16 v[66:69], v[168:171], v[224:227], v[66:69]
	v_mfma_f32_16x16x32_bf16 v[6:9], v[180:183], v[196:199], v[6:9]
	v_mfma_f32_16x16x32_bf16 v[2:5], v[188:191], v[196:199], v[2:5]
	v_mfma_f32_16x16x32_bf16 v[18:21], v[180:183], v[204:207], v[18:21]
	v_mfma_f32_16x16x32_bf16 v[14:17], v[188:191], v[204:207], v[14:17]
	v_mfma_f32_16x16x32_bf16 v[26:29], v[180:183], v[212:215], v[26:29]
	v_mfma_f32_16x16x32_bf16 v[22:25], v[188:191], v[212:215], v[22:25]
	v_mfma_f32_16x16x32_bf16 v[30:33], v[180:183], v[220:223], v[30:33]
	v_mfma_f32_16x16x32_bf16 v[10:13], v[188:191], v[220:223], v[10:13]
	v_mfma_f32_16x16x32_bf16 v[6:9], v[184:187], v[200:203], v[6:9]
	v_mfma_f32_16x16x32_bf16 v[2:5], v[192:195], v[200:203], v[2:5]
	v_mfma_f32_16x16x32_bf16 v[18:21], v[184:187], v[208:211], v[18:21]
	v_mfma_f32_16x16x32_bf16 v[14:17], v[192:195], v[208:211], v[14:17]
	v_mfma_f32_16x16x32_bf16 v[26:29], v[184:187], v[216:219], v[26:29]
	v_mfma_f32_16x16x32_bf16 v[22:25], v[192:195], v[216:219], v[22:25]
	v_mfma_f32_16x16x32_bf16 v[30:33], v[184:187], v[224:227], v[30:33]
	v_mfma_f32_16x16x32_bf16 v[10:13], v[192:195], v[224:227], v[10:13]
	s_barrier
	s_add_i32 s71, s71, 2
	s_add_u32 s46, s46, 0x100
	s_addc_u32 s47, s47, 0
	s_add_u32 s69, s69, 0x100
	s_addc_u32 s70, s70, 0
	s_cmp_gt_u32 s71, 29
.LBB0_1697:
	ds_read_b128 v[156:159], v176
	ds_read_b128 v[160:163], v176 offset:1024
	ds_read_b128 v[164:167], v176 offset:2048
	ds_read_b128 v[168:171], v176 offset:3072
	ds_read_b128 v[180:183], v177
	ds_read_b128 v[184:187], v177 offset:1024
	ds_read_b128 v[188:191], v177 offset:2048
	ds_read_b128 v[192:195], v177 offset:3072
	s_add_u32 s48, s46, 0xfff80080
	s_addc_u32 s49, s47, -1
	s_cmp_eq_u32 s71, 28
	s_cselect_b32 s51, s37, s49
	s_cselect_b32 s50, s43, s48
	s_cselect_b32 s49, s35, s70
	s_cselect_b32 s48, s45, s69
	v_lshl_add_u64 v[172:173], s[46:47], 0, v[148:149]
	s_add_i32 m0, s53, 0xc000
	ds_read_b128 v[196:199], v178
	ds_read_b128 v[200:203], v178 offset:1024
	ds_read_b128 v[204:207], v178 offset:2048
	ds_read_b128 v[208:211], v178 offset:3072
	ds_read_b128 v[212:215], v178 offset:4096
	ds_read_b128 v[216:219], v178 offset:5120
	ds_read_b128 v[220:223], v178 offset:6144
	ds_read_b128 v[224:227], v178 offset:7168
	global_load_lds_dwordx4 v[172:173], off
	v_lshl_add_u64 v[172:173], s[46:47], 0, v[150:151]
	s_add_i32 m0, s53, 0xe000
	s_nop 0
	global_load_lds_dwordx4 v[172:173], off
	s_waitcnt vmcnt(8)
	s_waitcnt lgkmcnt(0)
	s_barrier
	v_mfma_f32_16x16x32_bf16 v[126:129], v[156:159], v[196:199], v[126:129]
	v_mfma_f32_16x16x32_bf16 v[122:125], v[164:167], v[196:199], v[122:125]
	v_mfma_f32_16x16x32_bf16 v[118:121], v[156:159], v[204:207], v[118:121]
	v_mfma_f32_16x16x32_bf16 v[114:117], v[164:167], v[204:207], v[114:117]
	v_mfma_f32_16x16x32_bf16 v[110:113], v[156:159], v[212:215], v[110:113]
	v_mfma_f32_16x16x32_bf16 v[106:109], v[164:167], v[212:215], v[106:109]
	v_mfma_f32_16x16x32_bf16 v[102:105], v[156:159], v[220:223], v[102:105]
	v_mfma_f32_16x16x32_bf16 v[98:101], v[164:167], v[220:223], v[98:101]
	v_mfma_f32_16x16x32_bf16 v[126:129], v[160:163], v[200:203], v[126:129]
	v_mfma_f32_16x16x32_bf16 v[122:125], v[168:171], v[200:203], v[122:125]
	v_mfma_f32_16x16x32_bf16 v[118:121], v[160:163], v[208:211], v[118:121]
	v_mfma_f32_16x16x32_bf16 v[114:117], v[168:171], v[208:211], v[114:117]
	v_mfma_f32_16x16x32_bf16 v[110:113], v[160:163], v[216:219], v[110:113]
	v_mfma_f32_16x16x32_bf16 v[106:109], v[168:171], v[216:219], v[106:109]
	v_mfma_f32_16x16x32_bf16 v[102:105], v[160:163], v[224:227], v[102:105]
	v_mfma_f32_16x16x32_bf16 v[98:101], v[168:171], v[224:227], v[98:101]
	v_mfma_f32_16x16x32_bf16 v[38:41], v[180:183], v[196:199], v[38:41]
	v_mfma_f32_16x16x32_bf16 v[34:37], v[188:191], v[196:199], v[34:37]
	v_mfma_f32_16x16x32_bf16 v[46:49], v[180:183], v[204:207], v[46:49]
	v_mfma_f32_16x16x32_bf16 v[42:45], v[188:191], v[204:207], v[42:45]
	v_mfma_f32_16x16x32_bf16 v[54:57], v[180:183], v[212:215], v[54:57]
	v_mfma_f32_16x16x32_bf16 v[50:53], v[188:191], v[212:215], v[50:53]
	v_mfma_f32_16x16x32_bf16 v[62:65], v[180:183], v[220:223], v[62:65]
	v_mfma_f32_16x16x32_bf16 v[58:61], v[188:191], v[220:223], v[58:61]
	v_mfma_f32_16x16x32_bf16 v[38:41], v[184:187], v[200:203], v[38:41]
	v_mfma_f32_16x16x32_bf16 v[34:37], v[192:195], v[200:203], v[34:37]
	v_mfma_f32_16x16x32_bf16 v[46:49], v[184:187], v[208:211], v[46:49]
	v_mfma_f32_16x16x32_bf16 v[42:45], v[192:195], v[208:211], v[42:45]
	v_mfma_f32_16x16x32_bf16 v[54:57], v[184:187], v[216:219], v[54:57]
	v_mfma_f32_16x16x32_bf16 v[50:53], v[192:195], v[216:219], v[50:53]
	v_mfma_f32_16x16x32_bf16 v[62:65], v[184:187], v[224:227], v[62:65]
	v_mfma_f32_16x16x32_bf16 v[58:61], v[192:195], v[224:227], v[58:61]
	s_barrier
	s_add_i32 s72, s65, s52
	v_lshl_add_u64 v[172:173], s[48:49], 0, v[132:133]
	s_mov_b32 m0, s72
	ds_read_b128 v[196:199], v178 offset:16384
	ds_read_b128 v[200:203], v178 offset:17408
	ds_read_b128 v[204:207], v178 offset:18432
	ds_read_b128 v[208:211], v178 offset:19456
	ds_read_b128 v[212:215], v178 offset:20480
	ds_read_b128 v[216:219], v178 offset:21504
	ds_read_b128 v[220:223], v178 offset:22528
	ds_read_b128 v[224:227], v178 offset:23552
	global_load_lds_dwordx4 v[172:173], off
	s_add_i32 m0, s72, 0x2000
	s_add_u32 s72, s48, 0x80000
	v_lshl_add_u64 v[228:229], s[48:49], 0, v[136:137]
	s_addc_u32 s73, s49, 0
	s_add_i32 s74, s66, s52
	global_load_lds_dwordx4 v[228:229], off
	v_lshl_add_u64 v[230:231], s[72:73], 0, v[132:133]
	s_mov_b32 m0, s74
	v_lshl_add_u64 v[232:233], s[50:51], 0, v[134:135]
	global_load_lds_dwordx4 v[230:231], off
	v_lshl_add_u64 v[230:231], s[72:73], 0, v[136:137]
	s_add_i32 m0, s74, 0x2000
	s_nop 0
	global_load_lds_dwordx4 v[230:231], off
	v_lshl_add_u64 v[230:231], s[50:51], 0, v[130:131]
	s_mov_b32 m0, s53
	s_nop 0
	global_load_lds_dwordx4 v[230:231], off
	s_mov_b32 m0, s54
	s_nop 0
	global_load_lds_dwordx4 v[232:233], off
	s_waitcnt vmcnt(8)
	s_waitcnt lgkmcnt(0)
	s_barrier
	v_mfma_f32_16x16x32_bf16 v[94:97], v[156:159], v[196:199], v[94:97]
	v_mfma_f32_16x16x32_bf16 v[90:93], v[164:167], v[196:199], v[90:93]
	v_mfma_f32_16x16x32_bf16 v[86:89], v[156:159], v[204:207], v[86:89]
	v_mfma_f32_16x16x32_bf16 v[82:85], v[164:167], v[204:207], v[82:85]
	v_mfma_f32_16x16x32_bf16 v[78:81], v[156:159], v[212:215], v[78:81]
	v_mfma_f32_16x16x32_bf16 v[74:77], v[164:167], v[212:215], v[74:77]
	v_mfma_f32_16x16x32_bf16 v[70:73], v[156:159], v[220:223], v[70:73]
	v_mfma_f32_16x16x32_bf16 v[66:69], v[164:167], v[220:223], v[66:69]
	v_mfma_f32_16x16x32_bf16 v[94:97], v[160:163], v[200:203], v[94:97]
	v_mfma_f32_16x16x32_bf16 v[90:93], v[168:171], v[200:203], v[90:93]
	v_mfma_f32_16x16x32_bf16 v[86:89], v[160:163], v[208:211], v[86:89]
	v_mfma_f32_16x16x32_bf16 v[82:85], v[168:171], v[208:211], v[82:85]
	v_mfma_f32_16x16x32_bf16 v[78:81], v[160:163], v[216:219], v[78:81]
	v_mfma_f32_16x16x32_bf16 v[74:77], v[168:171], v[216:219], v[74:77]
	v_mfma_f32_16x16x32_bf16 v[70:73], v[160:163], v[224:227], v[70:73]
	v_mfma_f32_16x16x32_bf16 v[66:69], v[168:171], v[224:227], v[66:69]
	v_mfma_f32_16x16x32_bf16 v[6:9], v[180:183], v[196:199], v[6:9]
	v_mfma_f32_16x16x32_bf16 v[2:5], v[188:191], v[196:199], v[2:5]
	v_mfma_f32_16x16x32_bf16 v[18:21], v[180:183], v[204:207], v[18:21]
	v_mfma_f32_16x16x32_bf16 v[14:17], v[188:191], v[204:207], v[14:17]
	v_mfma_f32_16x16x32_bf16 v[26:29], v[180:183], v[212:215], v[26:29]
	v_mfma_f32_16x16x32_bf16 v[22:25], v[188:191], v[212:215], v[22:25]
	v_mfma_f32_16x16x32_bf16 v[30:33], v[180:183], v[220:223], v[30:33]
	v_mfma_f32_16x16x32_bf16 v[10:13], v[188:191], v[220:223], v[10:13]
	v_mfma_f32_16x16x32_bf16 v[6:9], v[184:187], v[200:203], v[6:9]
	v_mfma_f32_16x16x32_bf16 v[2:5], v[192:195], v[200:203], v[2:5]
	v_mfma_f32_16x16x32_bf16 v[18:21], v[184:187], v[208:211], v[18:21]
	v_mfma_f32_16x16x32_bf16 v[14:17], v[192:195], v[208:211], v[14:17]
	v_mfma_f32_16x16x32_bf16 v[26:29], v[184:187], v[216:219], v[26:29]
	v_mfma_f32_16x16x32_bf16 v[22:25], v[192:195], v[216:219], v[22:25]
	v_mfma_f32_16x16x32_bf16 v[30:33], v[184:187], v[224:227], v[30:33]
	v_mfma_f32_16x16x32_bf16 v[10:13], v[192:195], v[224:227], v[10:13]
	s_barrier
	s_add_i32 s72, 0, 0x18000
	v_add_u32_e32 v138, s72, v174
	s_add_i32 s73, 0, 0x1c000
	ds_read_b128 v[156:159], v138
	ds_read_b128 v[160:163], v138 offset:1024
	ds_read_b128 v[164:167], v138 offset:2048
	ds_read_b128 v[168:171], v138 offset:3072
	v_add_u32_e32 v138, s73, v174
	ds_read_b128 v[180:183], v138
	ds_read_b128 v[184:187], v138 offset:1024
	ds_read_b128 v[188:191], v138 offset:2048
	ds_read_b128 v[192:195], v138 offset:3072
	s_add_u32 s50, s50, 0x80000
	s_addc_u32 s51, s51, 0
	s_mov_b32 m0, s55
	v_lshl_add_u64 v[234:235], s[50:51], 0, v[130:131]
	ds_read_b128 v[196:199], v178 offset:32768
	ds_read_b128 v[200:203], v178 offset:33792
	ds_read_b128 v[204:207], v178 offset:34816
	ds_read_b128 v[208:211], v178 offset:35840
	ds_read_b128 v[212:215], v178 offset:36864
	ds_read_b128 v[216:219], v178 offset:37888
	ds_read_b128 v[220:223], v178 offset:38912
	ds_read_b128 v[224:227], v178 offset:39936
	global_load_lds_dwordx4 v[234:235], off
	v_lshl_add_u64 v[234:235], s[50:51], 0, v[134:135]
	s_mov_b32 m0, s56
	s_nop 0
	global_load_lds_dwordx4 v[234:235], off
	s_waitcnt vmcnt(8)
	s_waitcnt lgkmcnt(0)
	s_barrier
	v_mfma_f32_16x16x32_bf16 v[126:129], v[156:159], v[196:199], v[126:129]
	v_mfma_f32_16x16x32_bf16 v[122:125], v[164:167], v[196:199], v[122:125]
	v_mfma_f32_16x16x32_bf16 v[118:121], v[156:159], v[204:207], v[118:121]
	v_mfma_f32_16x16x32_bf16 v[114:117], v[164:167], v[204:207], v[114:117]
	v_mfma_f32_16x16x32_bf16 v[110:113], v[156:159], v[212:215], v[110:113]
	v_mfma_f32_16x16x32_bf16 v[106:109], v[164:167], v[212:215], v[106:109]
	v_mfma_f32_16x16x32_bf16 v[102:105], v[156:159], v[220:223], v[102:105]
	v_mfma_f32_16x16x32_bf16 v[98:101], v[164:167], v[220:223], v[98:101]
	v_mfma_f32_16x16x32_bf16 v[126:129], v[160:163], v[200:203], v[126:129]
	v_mfma_f32_16x16x32_bf16 v[122:125], v[168:171], v[200:203], v[122:125]
	v_mfma_f32_16x16x32_bf16 v[118:121], v[160:163], v[208:211], v[118:121]
	v_mfma_f32_16x16x32_bf16 v[114:117], v[168:171], v[208:211], v[114:117]
	v_mfma_f32_16x16x32_bf16 v[110:113], v[160:163], v[216:219], v[110:113]
	v_mfma_f32_16x16x32_bf16 v[106:109], v[168:171], v[216:219], v[106:109]
	v_mfma_f32_16x16x32_bf16 v[102:105], v[160:163], v[224:227], v[102:105]
	v_mfma_f32_16x16x32_bf16 v[98:101], v[168:171], v[224:227], v[98:101]
	v_mfma_f32_16x16x32_bf16 v[38:41], v[180:183], v[196:199], v[38:41]
	v_mfma_f32_16x16x32_bf16 v[34:37], v[188:191], v[196:199], v[34:37]
	v_mfma_f32_16x16x32_bf16 v[46:49], v[180:183], v[204:207], v[46:49]
	v_mfma_f32_16x16x32_bf16 v[42:45], v[188:191], v[204:207], v[42:45]
	v_mfma_f32_16x16x32_bf16 v[54:57], v[180:183], v[212:215], v[54:57]
	v_mfma_f32_16x16x32_bf16 v[50:53], v[188:191], v[212:215], v[50:53]
	v_mfma_f32_16x16x32_bf16 v[62:65], v[180:183], v[220:223], v[62:65]
	v_mfma_f32_16x16x32_bf16 v[58:61], v[188:191], v[220:223], v[58:61]
	v_mfma_f32_16x16x32_bf16 v[38:41], v[184:187], v[200:203], v[38:41]
	v_mfma_f32_16x16x32_bf16 v[34:37], v[192:195], v[200:203], v[34:37]
	v_mfma_f32_16x16x32_bf16 v[46:49], v[184:187], v[208:211], v[46:49]
	v_mfma_f32_16x16x32_bf16 v[42:45], v[192:195], v[208:211], v[42:45]
	v_mfma_f32_16x16x32_bf16 v[54:57], v[184:187], v[216:219], v[54:57]
	v_mfma_f32_16x16x32_bf16 v[50:53], v[192:195], v[216:219], v[50:53]
	v_mfma_f32_16x16x32_bf16 v[62:65], v[184:187], v[224:227], v[62:65]
	v_mfma_f32_16x16x32_bf16 v[58:61], v[192:195], v[224:227], v[58:61]
	s_barrier
	s_add_i32 s50, s72, s52
	v_lshl_add_u64 v[172:173], v[172:173], 0, s[6:7]
	s_mov_b32 m0, s50
	ds_read_b128 v[196:199], v178 offset:49152
	ds_read_b128 v[200:203], v178 offset:50176
	ds_read_b128 v[204:207], v178 offset:51200
	ds_read_b128 v[208:211], v178 offset:52224
	ds_read_b128 v[212:215], v178 offset:53248
	ds_read_b128 v[216:219], v178 offset:54272
	ds_read_b128 v[220:223], v178 offset:55296
	ds_read_b128 v[224:227], v178 offset:56320
	global_load_lds_dwordx4 v[172:173], off
	s_add_i32 m0, s50, 0x2000
	s_add_u32 s48, s48, 0x80080
	v_lshl_add_u64 v[172:173], v[228:229], 0, s[6:7]
	s_addc_u32 s49, s49, 0
	s_add_i32 s50, s73, s52
	global_load_lds_dwordx4 v[172:173], off
	v_lshl_add_u64 v[172:173], s[48:49], 0, v[132:133]
	s_mov_b32 m0, s50
	s_nop 0
	global_load_lds_dwordx4 v[172:173], off
	v_lshl_add_u64 v[172:173], s[48:49], 0, v[136:137]
	s_add_i32 m0, s50, 0x2000
	s_nop 0
	global_load_lds_dwordx4 v[172:173], off
	v_lshl_add_u64 v[172:173], v[230:231], 0, s[6:7]
	s_mov_b32 m0, s61
	s_nop 0
	global_load_lds_dwordx4 v[172:173], off
	v_lshl_add_u64 v[172:173], v[232:233], 0, s[6:7]
	s_mov_b32 m0, s62
	s_nop 0
	global_load_lds_dwordx4 v[172:173], off
	s_waitcnt vmcnt(8)
	s_waitcnt lgkmcnt(0)
	s_barrier
	v_mfma_f32_16x16x32_bf16 v[94:97], v[156:159], v[196:199], v[94:97]
	v_mfma_f32_16x16x32_bf16 v[90:93], v[164:167], v[196:199], v[90:93]
	v_mfma_f32_16x16x32_bf16 v[86:89], v[156:159], v[204:207], v[86:89]
	v_mfma_f32_16x16x32_bf16 v[82:85], v[164:167], v[204:207], v[82:85]
	v_mfma_f32_16x16x32_bf16 v[78:81], v[156:159], v[212:215], v[78:81]
	v_mfma_f32_16x16x32_bf16 v[74:77], v[164:167], v[212:215], v[74:77]
	v_mfma_f32_16x16x32_bf16 v[70:73], v[156:159], v[220:223], v[70:73]
	v_mfma_f32_16x16x32_bf16 v[66:69], v[164:167], v[220:223], v[66:69]
	v_mfma_f32_16x16x32_bf16 v[94:97], v[160:163], v[200:203], v[94:97]
	v_mfma_f32_16x16x32_bf16 v[90:93], v[168:171], v[200:203], v[90:93]
	v_mfma_f32_16x16x32_bf16 v[86:89], v[160:163], v[208:211], v[86:89]
	v_mfma_f32_16x16x32_bf16 v[82:85], v[168:171], v[208:211], v[82:85]
	v_mfma_f32_16x16x32_bf16 v[78:81], v[160:163], v[216:219], v[78:81]
	v_mfma_f32_16x16x32_bf16 v[74:77], v[168:171], v[216:219], v[74:77]
	v_mfma_f32_16x16x32_bf16 v[70:73], v[160:163], v[224:227], v[70:73]
	v_mfma_f32_16x16x32_bf16 v[66:69], v[168:171], v[224:227], v[66:69]
	v_mfma_f32_16x16x32_bf16 v[6:9], v[180:183], v[196:199], v[6:9]
	v_mfma_f32_16x16x32_bf16 v[2:5], v[188:191], v[196:199], v[2:5]
	v_mfma_f32_16x16x32_bf16 v[18:21], v[180:183], v[204:207], v[18:21]
	v_mfma_f32_16x16x32_bf16 v[14:17], v[188:191], v[204:207], v[14:17]
	v_mfma_f32_16x16x32_bf16 v[26:29], v[180:183], v[212:215], v[26:29]
	v_mfma_f32_16x16x32_bf16 v[22:25], v[188:191], v[212:215], v[22:25]
	v_mfma_f32_16x16x32_bf16 v[30:33], v[180:183], v[220:223], v[30:33]
	v_mfma_f32_16x16x32_bf16 v[10:13], v[188:191], v[220:223], v[10:13]
	v_mfma_f32_16x16x32_bf16 v[6:9], v[184:187], v[200:203], v[6:9]
	v_mfma_f32_16x16x32_bf16 v[2:5], v[192:195], v[200:203], v[2:5]
	v_mfma_f32_16x16x32_bf16 v[18:21], v[184:187], v[208:211], v[18:21]
	v_mfma_f32_16x16x32_bf16 v[14:17], v[192:195], v[208:211], v[14:17]
	v_mfma_f32_16x16x32_bf16 v[26:29], v[184:187], v[216:219], v[26:29]
	v_mfma_f32_16x16x32_bf16 v[22:25], v[192:195], v[216:219], v[22:25]
	v_mfma_f32_16x16x32_bf16 v[30:33], v[184:187], v[224:227], v[30:33]
	v_mfma_f32_16x16x32_bf16 v[10:13], v[192:195], v[224:227], v[10:13]
	s_barrier
	s_add_i32 s71, s71, 2
	s_add_u32 s46, s46, 0x100
	s_addc_u32 s47, s47, 0
	s_add_u32 s69, s69, 0x100
	s_addc_u32 s70, s70, 0
	s_cmp_gt_u32 s71, 29
	s_cbranch_scc0 .LBB0_1697
	s_and_b64 vcc, exec, s[12:13]
	s_cbranch_vccz .LBB0_1700
	s_barrier

.LBB0_2107:
	s_setprio 0
	v_readlane_b32 s26, v254, 1
	v_readlane_b32 s27, v254, 2
	s_mov_b32 s23, s99
	s_add_i32 s46, s46, 1
	s_mul_i32 s4, s46, s49
	s_waitcnt lgkmcnt(0)
	s_mul_hi_u32 s5, s46, s23
	s_add_i32 s5, s5, s4
	s_mul_i32 s4, s46, s23
	v_readlane_b32 s23, v254, 14
	s_add_u32 s26, s4, s23
	s_addc_u32 s27, s5, s33
	v_cmp_gt_i64_e32 vcc, s[26:27], v[144:145]
	v_cmp_lt_i64_e64 s[4:5], s[26:27], v[142:143]
	s_cbranch_vccnz .LBB0_2113
	s_ashr_i32 s22, s26, 31
	s_lshr_b32 s22, s22, 29
	s_add_i32 s24, s26, s22
	s_and_b32 s22, s24, -8
	s_sub_i32 s25, s26, s22
	s_cmp_gt_i32 s25, -1
	s_mov_b64 s[22:23], -1
	s_cbranch_scc0 .LBB0_2110
	s_lshl_b32 s26, s25, 7
	s_mov_b64 s[22:23], 0

.Lrx_2114_0:
	s_waitcnt vmcnt(24)
	s_waitcnt lgkmcnt(0)
	s_barrier
	v_mfma_f32_16x16x32_bf16 v[126:129], v[154:157], v[186:189], 0
	v_mfma_f32_16x16x32_bf16 v[122:125], v[162:165], v[186:189], 0
	v_mfma_f32_16x16x32_bf16 v[118:121], v[154:157], v[194:197], 0
	v_mfma_f32_16x16x32_bf16 v[110:113], v[162:165], v[194:197], 0
	v_mfma_f32_16x16x32_bf16 v[102:105], v[154:157], v[202:205], 0
	v_mfma_f32_16x16x32_bf16 v[94:97], v[162:165], v[202:205], 0
	v_mfma_f32_16x16x32_bf16 v[86:89], v[154:157], v[210:213], 0
	v_mfma_f32_16x16x32_bf16 v[78:81], v[162:165], v[210:213], 0
	v_mfma_f32_16x16x32_bf16 v[126:129], v[158:161], v[190:193], v[126:129]
	v_mfma_f32_16x16x32_bf16 v[122:125], v[166:169], v[190:193], v[122:125]
	v_mfma_f32_16x16x32_bf16 v[118:121], v[158:161], v[198:201], v[118:121]
	v_mfma_f32_16x16x32_bf16 v[110:113], v[166:169], v[198:201], v[110:113]
	v_mfma_f32_16x16x32_bf16 v[102:105], v[158:161], v[206:209], v[102:105]
	v_mfma_f32_16x16x32_bf16 v[94:97], v[166:169], v[206:209], v[94:97]
	v_mfma_f32_16x16x32_bf16 v[86:89], v[158:161], v[214:217], v[86:89]
	v_mfma_f32_16x16x32_bf16 v[78:81], v[166:169], v[214:217], v[78:81]
	v_mfma_f32_16x16x32_bf16 v[114:117], v[170:173], v[186:189], 0
	v_mfma_f32_16x16x32_bf16 v[106:109], v[178:181], v[186:189], 0
	v_mfma_f32_16x16x32_bf16 v[98:101], v[170:173], v[194:197], 0
	v_mfma_f32_16x16x32_bf16 v[90:93], v[178:181], v[194:197], 0
	v_mfma_f32_16x16x32_bf16 v[82:85], v[170:173], v[202:205], 0
	v_mfma_f32_16x16x32_bf16 v[74:77], v[178:181], v[202:205], 0
	v_mfma_f32_16x16x32_bf16 v[70:73], v[170:173], v[210:213], 0
	v_mfma_f32_16x16x32_bf16 v[66:69], v[178:181], v[210:213], 0
	v_mfma_f32_16x16x32_bf16 v[114:117], v[174:177], v[190:193], v[114:117]
	v_mfma_f32_16x16x32_bf16 v[106:109], v[182:185], v[190:193], v[106:109]
	v_mfma_f32_16x16x32_bf16 v[98:101], v[174:177], v[198:201], v[98:101]
	v_mfma_f32_16x16x32_bf16 v[90:93], v[182:185], v[198:201], v[90:93]
	v_mfma_f32_16x16x32_bf16 v[82:85], v[174:177], v[206:209], v[82:85]
	v_mfma_f32_16x16x32_bf16 v[74:77], v[182:185], v[206:209], v[74:77]
	v_mfma_f32_16x16x32_bf16 v[70:73], v[174:177], v[214:217], v[70:73]
	v_mfma_f32_16x16x32_bf16 v[66:69], v[182:185], v[214:217], v[66:69]
	s_barrier
	s_add_i32 s62, s50, s42
	v_lshl_add_u64 v[146:147], s[36:37], 0, v[132:133]
	s_mov_b32 m0, s62
	ds_read_b128 v[186:189], v152 offset:16384
	ds_read_b128 v[190:193], v152 offset:17408
	ds_read_b128 v[194:197], v152 offset:18432
	ds_read_b128 v[198:201], v152 offset:19456
	ds_read_b128 v[202:205], v152 offset:20480
	ds_read_b128 v[206:209], v152 offset:21504
	ds_read_b128 v[210:213], v152 offset:22528
	ds_read_b128 v[214:217], v152 offset:23552
	global_load_lds_dwordx4 v[146:147], off
	s_add_i32 m0, s62, 0x2000
	s_add_u32 s62, s36, 0x80000
	v_lshl_add_u64 v[218:219], s[36:37], 0, v[136:137]
	s_addc_u32 s63, s37, 0
	s_add_i32 s64, s51, s42
	global_load_lds_dwordx4 v[218:219], off
	v_lshl_add_u64 v[220:221], s[62:63], 0, v[132:133]
	s_mov_b32 m0, s64
	v_lshl_add_u64 v[222:223], s[38:39], 0, v[134:135]
	global_load_lds_dwordx4 v[220:221], off
	v_lshl_add_u64 v[220:221], s[62:63], 0, v[136:137]
	s_add_i32 m0, s64, 0x2000
	s_nop 0
	global_load_lds_dwordx4 v[220:221], off
	v_lshl_add_u64 v[220:221], s[38:39], 0, v[130:131]
	s_mov_b32 m0, s31
	s_nop 0
	global_load_lds_dwordx4 v[220:221], off
	s_mov_b32 m0, s43
	s_nop 0
	global_load_lds_dwordx4 v[222:223], off
	s_cmp_lg_u32 s100, 0
	s_cbranch_scc1 .Lrx_2114_1
	s_waitcnt vmcnt(8)
.Lrx_2114_1:
	s_waitcnt vmcnt(24)
	s_mov_b32 s100, 1
	s_waitcnt lgkmcnt(0)
	s_barrier
	v_mfma_f32_16x16x32_bf16 v[62:65], v[154:157], v[186:189], 0
	v_mfma_f32_16x16x32_bf16 v[58:61], v[162:165], v[186:189], 0
	v_mfma_f32_16x16x32_bf16 v[54:57], v[154:157], v[194:197], 0
	v_mfma_f32_16x16x32_bf16 v[46:49], v[162:165], v[194:197], 0
	v_mfma_f32_16x16x32_bf16 v[38:41], v[154:157], v[202:205], 0
	v_mfma_f32_16x16x32_bf16 v[30:33], v[162:165], v[202:205], 0
	v_mfma_f32_16x16x32_bf16 v[22:25], v[154:157], v[210:213], 0
	v_mfma_f32_16x16x32_bf16 v[14:17], v[162:165], v[210:213], 0
	v_mfma_f32_16x16x32_bf16 v[62:65], v[158:161], v[190:193], v[62:65]
	v_mfma_f32_16x16x32_bf16 v[58:61], v[166:169], v[190:193], v[58:61]
	v_mfma_f32_16x16x32_bf16 v[54:57], v[158:161], v[198:201], v[54:57]
	v_mfma_f32_16x16x32_bf16 v[46:49], v[166:169], v[198:201], v[46:49]
	v_mfma_f32_16x16x32_bf16 v[38:41], v[158:161], v[206:209], v[38:41]
	v_mfma_f32_16x16x32_bf16 v[30:33], v[166:169], v[206:209], v[30:33]
	v_mfma_f32_16x16x32_bf16 v[22:25], v[158:161], v[214:217], v[22:25]
	v_mfma_f32_16x16x32_bf16 v[14:17], v[166:169], v[214:217], v[14:17]
	v_mfma_f32_16x16x32_bf16 v[50:53], v[170:173], v[186:189], 0
	v_mfma_f32_16x16x32_bf16 v[42:45], v[178:181], v[186:189], 0
	v_mfma_f32_16x16x32_bf16 v[34:37], v[170:173], v[194:197], 0
	v_mfma_f32_16x16x32_bf16 v[26:29], v[178:181], v[194:197], 0
	v_mfma_f32_16x16x32_bf16 v[18:21], v[170:173], v[202:205], 0
	v_mfma_f32_16x16x32_bf16 v[10:13], v[178:181], v[202:205], 0
	v_mfma_f32_16x16x32_bf16 v[6:9], v[170:173], v[210:213], 0
	v_mfma_f32_16x16x32_bf16 v[2:5], v[178:181], v[210:213], 0
	v_mfma_f32_16x16x32_bf16 v[50:53], v[174:177], v[190:193], v[50:53]
	v_mfma_f32_16x16x32_bf16 v[42:45], v[182:185], v[190:193], v[42:45]
	v_mfma_f32_16x16x32_bf16 v[34:37], v[174:177], v[198:201], v[34:37]
	v_mfma_f32_16x16x32_bf16 v[26:29], v[182:185], v[198:201], v[26:29]
	v_mfma_f32_16x16x32_bf16 v[18:21], v[174:177], v[206:209], v[18:21]
	v_mfma_f32_16x16x32_bf16 v[10:13], v[182:185], v[206:209], v[10:13]
	v_mfma_f32_16x16x32_bf16 v[6:9], v[174:177], v[214:217], v[6:9]
	v_mfma_f32_16x16x32_bf16 v[2:5], v[182:185], v[214:217], v[2:5]
	s_barrier
	s_add_i32 s62, 0, 0x18000
	v_add_u32_e32 v153, s62, v148
	s_add_i32 s63, 0, 0x1c000
	ds_read_b128 v[154:157], v153
	ds_read_b128 v[158:161], v153 offset:1024
	ds_read_b128 v[162:165], v153 offset:2048
	ds_read_b128 v[166:169], v153 offset:3072
	v_add_u32_e32 v153, s63, v148
	ds_read_b128 v[170:173], v153
	ds_read_b128 v[174:177], v153 offset:1024
	ds_read_b128 v[178:181], v153 offset:2048
	ds_read_b128 v[182:185], v153 offset:3072
	s_add_u32 s38, s38, 0x80000
	s_addc_u32 s39, s39, 0
	s_mov_b32 m0, s44
	v_lshl_add_u64 v[224:225], s[38:39], 0, v[130:131]
	ds_read_b128 v[186:189], v152 offset:32768
	ds_read_b128 v[190:193], v152 offset:33792
	ds_read_b128 v[194:197], v152 offset:34816
	ds_read_b128 v[198:201], v152 offset:35840
	ds_read_b128 v[202:205], v152 offset:36864
	ds_read_b128 v[206:209], v152 offset:37888
	ds_read_b128 v[210:213], v152 offset:38912
	ds_read_b128 v[214:217], v152 offset:39936
	global_load_lds_dwordx4 v[224:225], off
	v_lshl_add_u64 v[224:225], s[38:39], 0, v[134:135]
	s_mov_b32 m0, s45
	s_nop 0
	global_load_lds_dwordx4 v[224:225], off
	s_waitcnt vmcnt(8)
	s_waitcnt lgkmcnt(0)
	s_barrier
	v_mfma_f32_16x16x32_bf16 v[126:129], v[154:157], v[186:189], v[126:129]
	v_mfma_f32_16x16x32_bf16 v[122:125], v[162:165], v[186:189], v[122:125]
	v_mfma_f32_16x16x32_bf16 v[118:121], v[154:157], v[194:197], v[118:121]
	v_mfma_f32_16x16x32_bf16 v[110:113], v[162:165], v[194:197], v[110:113]
	v_mfma_f32_16x16x32_bf16 v[102:105], v[154:157], v[202:205], v[102:105]
	v_mfma_f32_16x16x32_bf16 v[94:97], v[162:165], v[202:205], v[94:97]
	v_mfma_f32_16x16x32_bf16 v[86:89], v[154:157], v[210:213], v[86:89]
	v_mfma_f32_16x16x32_bf16 v[78:81], v[162:165], v[210:213], v[78:81]
	v_mfma_f32_16x16x32_bf16 v[126:129], v[158:161], v[190:193], v[126:129]
	v_mfma_f32_16x16x32_bf16 v[122:125], v[166:169], v[190:193], v[122:125]
	v_mfma_f32_16x16x32_bf16 v[118:121], v[158:161], v[198:201], v[118:121]
	v_mfma_f32_16x16x32_bf16 v[110:113], v[166:169], v[198:201], v[110:113]
	v_mfma_f32_16x16x32_bf16 v[102:105], v[158:161], v[206:209], v[102:105]
	v_mfma_f32_16x16x32_bf16 v[94:97], v[166:169], v[206:209], v[94:97]
	v_mfma_f32_16x16x32_bf16 v[86:89], v[158:161], v[214:217], v[86:89]
	v_mfma_f32_16x16x32_bf16 v[78:81], v[166:169], v[214:217], v[78:81]
	v_mfma_f32_16x16x32_bf16 v[114:117], v[170:173], v[186:189], v[114:117]
	v_mfma_f32_16x16x32_bf16 v[106:109], v[178:181], v[186:189], v[106:109]
	v_mfma_f32_16x16x32_bf16 v[98:101], v[170:173], v[194:197], v[98:101]
	v_mfma_f32_16x16x32_bf16 v[90:93], v[178:181], v[194:197], v[90:93]
	v_mfma_f32_16x16x32_bf16 v[82:85], v[170:173], v[202:205], v[82:85]
	v_mfma_f32_16x16x32_bf16 v[74:77], v[178:181], v[202:205], v[74:77]
	v_mfma_f32_16x16x32_bf16 v[70:73], v[170:173], v[210:213], v[70:73]
	v_mfma_f32_16x16x32_bf16 v[66:69], v[178:181], v[210:213], v[66:69]
	v_mfma_f32_16x16x32_bf16 v[114:117], v[174:177], v[190:193], v[114:117]
	v_mfma_f32_16x16x32_bf16 v[106:109], v[182:185], v[190:193], v[106:109]
	v_mfma_f32_16x16x32_bf16 v[98:101], v[174:177], v[198:201], v[98:101]
	v_mfma_f32_16x16x32_bf16 v[90:93], v[182:185], v[198:201], v[90:93]
	v_mfma_f32_16x16x32_bf16 v[82:85], v[174:177], v[206:209], v[82:85]
	v_mfma_f32_16x16x32_bf16 v[74:77], v[182:185], v[206:209], v[74:77]
	v_mfma_f32_16x16x32_bf16 v[70:73], v[174:177], v[214:217], v[70:73]
	v_mfma_f32_16x16x32_bf16 v[66:69], v[182:185], v[214:217], v[66:69]
	s_barrier
	s_add_i32 s38, s62, s42
	v_lshl_add_u64 v[146:147], v[146:147], 0, s[10:11]
	s_mov_b32 m0, s38
	ds_read_b128 v[186:189], v152 offset:49152
	ds_read_b128 v[190:193], v152 offset:50176
	ds_read_b128 v[194:197], v152 offset:51200
	ds_read_b128 v[198:201], v152 offset:52224
	ds_read_b128 v[202:205], v152 offset:53248
	ds_read_b128 v[206:209], v152 offset:54272
	ds_read_b128 v[210:213], v152 offset:55296
	ds_read_b128 v[214:217], v152 offset:56320
	global_load_lds_dwordx4 v[146:147], off
	s_add_i32 m0, s38, 0x2000
	s_add_u32 s36, s36, 0x80080
	v_lshl_add_u64 v[146:147], v[218:219], 0, s[10:11]
	s_addc_u32 s37, s37, 0
	s_add_i32 s38, s63, s42
	global_load_lds_dwordx4 v[146:147], off
	v_lshl_add_u64 v[146:147], s[36:37], 0, v[132:133]
	s_mov_b32 m0, s38
	s_nop 0
	global_load_lds_dwordx4 v[146:147], off
	v_lshl_add_u64 v[146:147], s[36:37], 0, v[136:137]
	s_add_i32 m0, s38, 0x2000
	s_nop 0
	global_load_lds_dwordx4 v[146:147], off
	v_lshl_add_u64 v[146:147], v[220:221], 0, s[10:11]
	s_mov_b32 m0, s47
	s_nop 0
	global_load_lds_dwordx4 v[146:147], off
	v_lshl_add_u64 v[146:147], v[222:223], 0, s[10:11]
	s_mov_b32 m0, s48
	s_nop 0
	global_load_lds_dwordx4 v[146:147], off
	s_waitcnt vmcnt(8)
	s_waitcnt lgkmcnt(0)
	s_barrier
	v_mfma_f32_16x16x32_bf16 v[62:65], v[154:157], v[186:189], v[62:65]
	v_mfma_f32_16x16x32_bf16 v[58:61], v[162:165], v[186:189], v[58:61]
	v_mfma_f32_16x16x32_bf16 v[54:57], v[154:157], v[194:197], v[54:57]
	v_mfma_f32_16x16x32_bf16 v[46:49], v[162:165], v[194:197], v[46:49]
	v_mfma_f32_16x16x32_bf16 v[38:41], v[154:157], v[202:205], v[38:41]
	v_mfma_f32_16x16x32_bf16 v[30:33], v[162:165], v[202:205], v[30:33]
	v_mfma_f32_16x16x32_bf16 v[22:25], v[154:157], v[210:213], v[22:25]
	v_mfma_f32_16x16x32_bf16 v[14:17], v[162:165], v[210:213], v[14:17]
	v_mfma_f32_16x16x32_bf16 v[62:65], v[158:161], v[190:193], v[62:65]
	v_mfma_f32_16x16x32_bf16 v[58:61], v[166:169], v[190:193], v[58:61]
	v_mfma_f32_16x16x32_bf16 v[54:57], v[158:161], v[198:201], v[54:57]
	v_mfma_f32_16x16x32_bf16 v[46:49], v[166:169], v[198:201], v[46:49]
	v_mfma_f32_16x16x32_bf16 v[38:41], v[158:161], v[206:209], v[38:41]
	v_mfma_f32_16x16x32_bf16 v[30:33], v[166:169], v[206:209], v[30:33]
	v_mfma_f32_16x16x32_bf16 v[22:25], v[158:161], v[214:217], v[22:25]
	v_mfma_f32_16x16x32_bf16 v[14:17], v[166:169], v[214:217], v[14:17]
	v_mfma_f32_16x16x32_bf16 v[50:53], v[170:173], v[186:189], v[50:53]
	v_mfma_f32_16x16x32_bf16 v[42:45], v[178:181], v[186:189], v[42:45]
	v_mfma_f32_16x16x32_bf16 v[34:37], v[170:173], v[194:197], v[34:37]
	v_mfma_f32_16x16x32_bf16 v[26:29], v[178:181], v[194:197], v[26:29]
	v_mfma_f32_16x16x32_bf16 v[18:21], v[170:173], v[202:205], v[18:21]
	v_mfma_f32_16x16x32_bf16 v[10:13], v[178:181], v[202:205], v[10:13]
	v_mfma_f32_16x16x32_bf16 v[6:9], v[170:173], v[210:213], v[6:9]
	v_mfma_f32_16x16x32_bf16 v[2:5], v[178:181], v[210:213], v[2:5]
	v_mfma_f32_16x16x32_bf16 v[50:53], v[174:177], v[190:193], v[50:53]
	v_mfma_f32_16x16x32_bf16 v[42:45], v[182:185], v[190:193], v[42:45]
	v_mfma_f32_16x16x32_bf16 v[34:37], v[174:177], v[198:201], v[34:37]
	v_mfma_f32_16x16x32_bf16 v[26:29], v[182:185], v[198:201], v[26:29]
	v_mfma_f32_16x16x32_bf16 v[18:21], v[174:177], v[206:209], v[18:21]
	v_mfma_f32_16x16x32_bf16 v[10:13], v[182:185], v[206:209], v[10:13]
	v_mfma_f32_16x16x32_bf16 v[6:9], v[174:177], v[214:217], v[6:9]
	v_mfma_f32_16x16x32_bf16 v[2:5], v[182:185], v[214:217], v[2:5]
	s_barrier
	s_add_i32 s61, s61, 2
	s_add_u32 s34, s34, 0x100
	s_addc_u32 s35, s35, 0
	s_add_u32 s59, s59, 0x100
	s_addc_u32 s60, s60, 0
	s_cmp_gt_u32 s61, 29
.LBB0_2114:
	ds_read_b128 v[154:157], v150
	ds_read_b128 v[158:161], v150 offset:1024
	ds_read_b128 v[162:165], v150 offset:2048
	ds_read_b128 v[166:169], v150 offset:3072
	ds_read_b128 v[170:173], v151
	ds_read_b128 v[174:177], v151 offset:1024
	ds_read_b128 v[178:181], v151 offset:2048
	ds_read_b128 v[182:185], v151 offset:3072
	s_add_u32 s36, s34, 0xfff80080
	s_addc_u32 s37, s35, -1
	s_cmp_eq_u32 s61, 28
	s_cselect_b32 s39, s25, s37
	s_cselect_b32 s38, s57, s36
	s_cselect_b32 s37, s23, s60
	s_cselect_b32 s36, s58, s59
	v_lshl_add_u64 v[146:147], s[34:35], 0, v[138:139]
	s_add_i32 m0, s31, 0xc000
	ds_read_b128 v[186:189], v152
	ds_read_b128 v[190:193], v152 offset:1024
	ds_read_b128 v[194:197], v152 offset:2048
	ds_read_b128 v[198:201], v152 offset:3072
	ds_read_b128 v[202:205], v152 offset:4096
	ds_read_b128 v[206:209], v152 offset:5120
	ds_read_b128 v[210:213], v152 offset:6144
	ds_read_b128 v[214:217], v152 offset:7168
	global_load_lds_dwordx4 v[146:147], off
	v_lshl_add_u64 v[146:147], s[34:35], 0, v[140:141]
	s_add_i32 m0, s31, 0xe000
	s_nop 0
	global_load_lds_dwordx4 v[146:147], off
	s_waitcnt vmcnt(8)
	s_waitcnt lgkmcnt(0)
	s_barrier
	v_mfma_f32_16x16x32_bf16 v[126:129], v[154:157], v[186:189], v[126:129]
	v_mfma_f32_16x16x32_bf16 v[122:125], v[162:165], v[186:189], v[122:125]
	v_mfma_f32_16x16x32_bf16 v[118:121], v[154:157], v[194:197], v[118:121]
	v_mfma_f32_16x16x32_bf16 v[110:113], v[162:165], v[194:197], v[110:113]
	v_mfma_f32_16x16x32_bf16 v[102:105], v[154:157], v[202:205], v[102:105]
	v_mfma_f32_16x16x32_bf16 v[94:97], v[162:165], v[202:205], v[94:97]
	v_mfma_f32_16x16x32_bf16 v[86:89], v[154:157], v[210:213], v[86:89]
	v_mfma_f32_16x16x32_bf16 v[78:81], v[162:165], v[210:213], v[78:81]
	v_mfma_f32_16x16x32_bf16 v[126:129], v[158:161], v[190:193], v[126:129]
	v_mfma_f32_16x16x32_bf16 v[122:125], v[166:169], v[190:193], v[122:125]
	v_mfma_f32_16x16x32_bf16 v[118:121], v[158:161], v[198:201], v[118:121]
	v_mfma_f32_16x16x32_bf16 v[110:113], v[166:169], v[198:201], v[110:113]
	v_mfma_f32_16x16x32_bf16 v[102:105], v[158:161], v[206:209], v[102:105]
	v_mfma_f32_16x16x32_bf16 v[94:97], v[166:169], v[206:209], v[94:97]
	v_mfma_f32_16x16x32_bf16 v[86:89], v[158:161], v[214:217], v[86:89]
	v_mfma_f32_16x16x32_bf16 v[78:81], v[166:169], v[214:217], v[78:81]
	v_mfma_f32_16x16x32_bf16 v[114:117], v[170:173], v[186:189], v[114:117]
	v_mfma_f32_16x16x32_bf16 v[106:109], v[178:181], v[186:189], v[106:109]
	v_mfma_f32_16x16x32_bf16 v[98:101], v[170:173], v[194:197], v[98:101]
	v_mfma_f32_16x16x32_bf16 v[90:93], v[178:181], v[194:197], v[90:93]
	v_mfma_f32_16x16x32_bf16 v[82:85], v[170:173], v[202:205], v[82:85]
	v_mfma_f32_16x16x32_bf16 v[74:77], v[178:181], v[202:205], v[74:77]
	v_mfma_f32_16x16x32_bf16 v[70:73], v[170:173], v[210:213], v[70:73]
	v_mfma_f32_16x16x32_bf16 v[66:69], v[178:181], v[210:213], v[66:69]
	v_mfma_f32_16x16x32_bf16 v[114:117], v[174:177], v[190:193], v[114:117]
	v_mfma_f32_16x16x32_bf16 v[106:109], v[182:185], v[190:193], v[106:109]
	v_mfma_f32_16x16x32_bf16 v[98:101], v[174:177], v[198:201], v[98:101]
	v_mfma_f32_16x16x32_bf16 v[90:93], v[182:185], v[198:201], v[90:93]
	v_mfma_f32_16x16x32_bf16 v[82:85], v[174:177], v[206:209], v[82:85]
	v_mfma_f32_16x16x32_bf16 v[74:77], v[182:185], v[206:209], v[74:77]
	v_mfma_f32_16x16x32_bf16 v[70:73], v[174:177], v[214:217], v[70:73]
	v_mfma_f32_16x16x32_bf16 v[66:69], v[182:185], v[214:217], v[66:69]
	s_barrier
	s_add_i32 s62, s50, s42
	v_lshl_add_u64 v[146:147], s[36:37], 0, v[132:133]
	s_mov_b32 m0, s62
	ds_read_b128 v[186:189], v152 offset:16384
	ds_read_b128 v[190:193], v152 offset:17408
	ds_read_b128 v[194:197], v152 offset:18432
	ds_read_b128 v[198:201], v152 offset:19456
	ds_read_b128 v[202:205], v152 offset:20480
	ds_read_b128 v[206:209], v152 offset:21504
	ds_read_b128 v[210:213], v152 offset:22528
	ds_read_b128 v[214:217], v152 offset:23552
	global_load_lds_dwordx4 v[146:147], off
	s_add_i32 m0, s62, 0x2000
	s_add_u32 s62, s36, 0x80000
	v_lshl_add_u64 v[218:219], s[36:37], 0, v[136:137]
	s_addc_u32 s63, s37, 0
	s_add_i32 s64, s51, s42
	global_load_lds_dwordx4 v[218:219], off
	v_lshl_add_u64 v[220:221], s[62:63], 0, v[132:133]
	s_mov_b32 m0, s64
	v_lshl_add_u64 v[222:223], s[38:39], 0, v[134:135]
	global_load_lds_dwordx4 v[220:221], off
	v_lshl_add_u64 v[220:221], s[62:63], 0, v[136:137]
	s_add_i32 m0, s64, 0x2000
	s_nop 0
	global_load_lds_dwordx4 v[220:221], off
	v_lshl_add_u64 v[220:221], s[38:39], 0, v[130:131]
	s_mov_b32 m0, s31
	s_nop 0
	global_load_lds_dwordx4 v[220:221], off
	s_mov_b32 m0, s43
	s_nop 0
	global_load_lds_dwordx4 v[222:223], off
	s_waitcnt vmcnt(8)
	s_waitcnt lgkmcnt(0)
	s_barrier
	v_mfma_f32_16x16x32_bf16 v[62:65], v[154:157], v[186:189], v[62:65]
	v_mfma_f32_16x16x32_bf16 v[58:61], v[162:165], v[186:189], v[58:61]
	v_mfma_f32_16x16x32_bf16 v[54:57], v[154:157], v[194:197], v[54:57]
	v_mfma_f32_16x16x32_bf16 v[46:49], v[162:165], v[194:197], v[46:49]
	v_mfma_f32_16x16x32_bf16 v[38:41], v[154:157], v[202:205], v[38:41]
	v_mfma_f32_16x16x32_bf16 v[30:33], v[162:165], v[202:205], v[30:33]
	v_mfma_f32_16x16x32_bf16 v[22:25], v[154:157], v[210:213], v[22:25]
	v_mfma_f32_16x16x32_bf16 v[14:17], v[162:165], v[210:213], v[14:17]
	v_mfma_f32_16x16x32_bf16 v[62:65], v[158:161], v[190:193], v[62:65]
	v_mfma_f32_16x16x32_bf16 v[58:61], v[166:169], v[190:193], v[58:61]
	v_mfma_f32_16x16x32_bf16 v[54:57], v[158:161], v[198:201], v[54:57]
	v_mfma_f32_16x16x32_bf16 v[46:49], v[166:169], v[198:201], v[46:49]
	v_mfma_f32_16x16x32_bf16 v[38:41], v[158:161], v[206:209], v[38:41]
	v_mfma_f32_16x16x32_bf16 v[30:33], v[166:169], v[206:209], v[30:33]
	v_mfma_f32_16x16x32_bf16 v[22:25], v[158:161], v[214:217], v[22:25]
	v_mfma_f32_16x16x32_bf16 v[14:17], v[166:169], v[214:217], v[14:17]
	v_mfma_f32_16x16x32_bf16 v[50:53], v[170:173], v[186:189], v[50:53]
	v_mfma_f32_16x16x32_bf16 v[42:45], v[178:181], v[186:189], v[42:45]
	v_mfma_f32_16x16x32_bf16 v[34:37], v[170:173], v[194:197], v[34:37]
	v_mfma_f32_16x16x32_bf16 v[26:29], v[178:181], v[194:197], v[26:29]
	v_mfma_f32_16x16x32_bf16 v[18:21], v[170:173], v[202:205], v[18:21]
	v_mfma_f32_16x16x32_bf16 v[10:13], v[178:181], v[202:205], v[10:13]
	v_mfma_f32_16x16x32_bf16 v[6:9], v[170:173], v[210:213], v[6:9]
	v_mfma_f32_16x16x32_bf16 v[2:5], v[178:181], v[210:213], v[2:5]
	v_mfma_f32_16x16x32_bf16 v[50:53], v[174:177], v[190:193], v[50:53]
	v_mfma_f32_16x16x32_bf16 v[42:45], v[182:185], v[190:193], v[42:45]
	v_mfma_f32_16x16x32_bf16 v[34:37], v[174:177], v[198:201], v[34:37]
	v_mfma_f32_16x16x32_bf16 v[26:29], v[182:185], v[198:201], v[26:29]
	v_mfma_f32_16x16x32_bf16 v[18:21], v[174:177], v[206:209], v[18:21]
	v_mfma_f32_16x16x32_bf16 v[10:13], v[182:185], v[206:209], v[10:13]
	v_mfma_f32_16x16x32_bf16 v[6:9], v[174:177], v[214:217], v[6:9]
	v_mfma_f32_16x16x32_bf16 v[2:5], v[182:185], v[214:217], v[2:5]
	s_barrier
	s_add_i32 s62, 0, 0x18000
	v_add_u32_e32 v153, s62, v148
	s_add_i32 s63, 0, 0x1c000
	ds_read_b128 v[154:157], v153
	ds_read_b128 v[158:161], v153 offset:1024
	ds_read_b128 v[162:165], v153 offset:2048
	ds_read_b128 v[166:169], v153 offset:3072
	v_add_u32_e32 v153, s63, v148
	ds_read_b128 v[170:173], v153
	ds_read_b128 v[174:177], v153 offset:1024
	ds_read_b128 v[178:181], v153 offset:2048
	ds_read_b128 v[182:185], v153 offset:3072
	s_add_u32 s38, s38, 0x80000
	s_addc_u32 s39, s39, 0
	s_mov_b32 m0, s44
	v_lshl_add_u64 v[224:225], s[38:39], 0, v[130:131]
	ds_read_b128 v[186:189], v152 offset:32768
	ds_read_b128 v[190:193], v152 offset:33792
	ds_read_b128 v[194:197], v152 offset:34816
	ds_read_b128 v[198:201], v152 offset:35840
	ds_read_b128 v[202:205], v152 offset:36864
	ds_read_b128 v[206:209], v152 offset:37888
	ds_read_b128 v[210:213], v152 offset:38912
	ds_read_b128 v[214:217], v152 offset:39936
	global_load_lds_dwordx4 v[224:225], off
	v_lshl_add_u64 v[224:225], s[38:39], 0, v[134:135]
	s_mov_b32 m0, s45
	s_nop 0
	global_load_lds_dwordx4 v[224:225], off
	s_waitcnt vmcnt(8)
	s_waitcnt lgkmcnt(0)
	s_barrier
	v_mfma_f32_16x16x32_bf16 v[126:129], v[154:157], v[186:189], v[126:129]
	v_mfma_f32_16x16x32_bf16 v[122:125], v[162:165], v[186:189], v[122:125]
	v_mfma_f32_16x16x32_bf16 v[118:121], v[154:157], v[194:197], v[118:121]
	v_mfma_f32_16x16x32_bf16 v[110:113], v[162:165], v[194:197], v[110:113]
	v_mfma_f32_16x16x32_bf16 v[102:105], v[154:157], v[202:205], v[102:105]
	v_mfma_f32_16x16x32_bf16 v[94:97], v[162:165], v[202:205], v[94:97]
	v_mfma_f32_16x16x32_bf16 v[86:89], v[154:157], v[210:213], v[86:89]
	v_mfma_f32_16x16x32_bf16 v[78:81], v[162:165], v[210:213], v[78:81]
	v_mfma_f32_16x16x32_bf16 v[126:129], v[158:161], v[190:193], v[126:129]
	v_mfma_f32_16x16x32_bf16 v[122:125], v[166:169], v[190:193], v[122:125]
	v_mfma_f32_16x16x32_bf16 v[118:121], v[158:161], v[198:201], v[118:121]
	v_mfma_f32_16x16x32_bf16 v[110:113], v[166:169], v[198:201], v[110:113]
	v_mfma_f32_16x16x32_bf16 v[102:105], v[158:161], v[206:209], v[102:105]
	v_mfma_f32_16x16x32_bf16 v[94:97], v[166:169], v[206:209], v[94:97]
	v_mfma_f32_16x16x32_bf16 v[86:89], v[158:161], v[214:217], v[86:89]
	v_mfma_f32_16x16x32_bf16 v[78:81], v[166:169], v[214:217], v[78:81]
	v_mfma_f32_16x16x32_bf16 v[114:117], v[170:173], v[186:189], v[114:117]
	v_mfma_f32_16x16x32_bf16 v[106:109], v[178:181], v[186:189], v[106:109]
	v_mfma_f32_16x16x32_bf16 v[98:101], v[170:173], v[194:197], v[98:101]
	v_mfma_f32_16x16x32_bf16 v[90:93], v[178:181], v[194:197], v[90:93]
	v_mfma_f32_16x16x32_bf16 v[82:85], v[170:173], v[202:205], v[82:85]
	v_mfma_f32_16x16x32_bf16 v[74:77], v[178:181], v[202:205], v[74:77]
	v_mfma_f32_16x16x32_bf16 v[70:73], v[170:173], v[210:213], v[70:73]
	v_mfma_f32_16x16x32_bf16 v[66:69], v[178:181], v[210:213], v[66:69]
	v_mfma_f32_16x16x32_bf16 v[114:117], v[174:177], v[190:193], v[114:117]
	v_mfma_f32_16x16x32_bf16 v[106:109], v[182:185], v[190:193], v[106:109]
	v_mfma_f32_16x16x32_bf16 v[98:101], v[174:177], v[198:201], v[98:101]
	v_mfma_f32_16x16x32_bf16 v[90:93], v[182:185], v[198:201], v[90:93]
	v_mfma_f32_16x16x32_bf16 v[82:85], v[174:177], v[206:209], v[82:85]
	v_mfma_f32_16x16x32_bf16 v[74:77], v[182:185], v[206:209], v[74:77]
	v_mfma_f32_16x16x32_bf16 v[70:73], v[174:177], v[214:217], v[70:73]
	v_mfma_f32_16x16x32_bf16 v[66:69], v[182:185], v[214:217], v[66:69]
	s_barrier
	s_add_i32 s38, s62, s42
	v_lshl_add_u64 v[146:147], v[146:147], 0, s[10:11]
	s_mov_b32 m0, s38
	ds_read_b128 v[186:189], v152 offset:49152
	ds_read_b128 v[190:193], v152 offset:50176
	ds_read_b128 v[194:197], v152 offset:51200
	ds_read_b128 v[198:201], v152 offset:52224
	ds_read_b128 v[202:205], v152 offset:53248
	ds_read_b128 v[206:209], v152 offset:54272
	ds_read_b128 v[210:213], v152 offset:55296
	ds_read_b128 v[214:217], v152 offset:56320
	global_load_lds_dwordx4 v[146:147], off
	s_add_i32 m0, s38, 0x2000
	s_add_u32 s36, s36, 0x80080
	v_lshl_add_u64 v[146:147], v[218:219], 0, s[10:11]
	s_addc_u32 s37, s37, 0
	s_add_i32 s38, s63, s42
	global_load_lds_dwordx4 v[146:147], off
	v_lshl_add_u64 v[146:147], s[36:37], 0, v[132:133]
	s_mov_b32 m0, s38
	s_nop 0
	global_load_lds_dwordx4 v[146:147], off
	v_lshl_add_u64 v[146:147], s[36:37], 0, v[136:137]
	s_add_i32 m0, s38, 0x2000
	s_nop 0
	global_load_lds_dwordx4 v[146:147], off
	v_lshl_add_u64 v[146:147], v[220:221], 0, s[10:11]
	s_mov_b32 m0, s47
	s_nop 0
	global_load_lds_dwordx4 v[146:147], off
	v_lshl_add_u64 v[146:147], v[222:223], 0, s[10:11]
	s_mov_b32 m0, s48
	s_nop 0
	global_load_lds_dwordx4 v[146:147], off
	s_waitcnt vmcnt(8)
	s_waitcnt lgkmcnt(0)
	s_barrier
	v_mfma_f32_16x16x32_bf16 v[62:65], v[154:157], v[186:189], v[62:65]
	v_mfma_f32_16x16x32_bf16 v[58:61], v[162:165], v[186:189], v[58:61]
	v_mfma_f32_16x16x32_bf16 v[54:57], v[154:157], v[194:197], v[54:57]
	v_mfma_f32_16x16x32_bf16 v[46:49], v[162:165], v[194:197], v[46:49]
	v_mfma_f32_16x16x32_bf16 v[38:41], v[154:157], v[202:205], v[38:41]
	v_mfma_f32_16x16x32_bf16 v[30:33], v[162:165], v[202:205], v[30:33]
	v_mfma_f32_16x16x32_bf16 v[22:25], v[154:157], v[210:213], v[22:25]
	v_mfma_f32_16x16x32_bf16 v[14:17], v[162:165], v[210:213], v[14:17]
	v_mfma_f32_16x16x32_bf16 v[62:65], v[158:161], v[190:193], v[62:65]
	v_mfma_f32_16x16x32_bf16 v[58:61], v[166:169], v[190:193], v[58:61]
	v_mfma_f32_16x16x32_bf16 v[54:57], v[158:161], v[198:201], v[54:57]
	v_mfma_f32_16x16x32_bf16 v[46:49], v[166:169], v[198:201], v[46:49]
	v_mfma_f32_16x16x32_bf16 v[38:41], v[158:161], v[206:209], v[38:41]
	v_mfma_f32_16x16x32_bf16 v[30:33], v[166:169], v[206:209], v[30:33]
	v_mfma_f32_16x16x32_bf16 v[22:25], v[158:161], v[214:217], v[22:25]
	v_mfma_f32_16x16x32_bf16 v[14:17], v[166:169], v[214:217], v[14:17]
	v_mfma_f32_16x16x32_bf16 v[50:53], v[170:173], v[186:189], v[50:53]
	v_mfma_f32_16x16x32_bf16 v[42:45], v[178:181], v[186:189], v[42:45]
	v_mfma_f32_16x16x32_bf16 v[34:37], v[170:173], v[194:197], v[34:37]
	v_mfma_f32_16x16x32_bf16 v[26:29], v[178:181], v[194:197], v[26:29]
	v_mfma_f32_16x16x32_bf16 v[18:21], v[170:173], v[202:205], v[18:21]
	v_mfma_f32_16x16x32_bf16 v[10:13], v[178:181], v[202:205], v[10:13]
	v_mfma_f32_16x16x32_bf16 v[6:9], v[170:173], v[210:213], v[6:9]
	v_mfma_f32_16x16x32_bf16 v[2:5], v[178:181], v[210:213], v[2:5]
	v_mfma_f32_16x16x32_bf16 v[50:53], v[174:177], v[190:193], v[50:53]
	v_mfma_f32_16x16x32_bf16 v[42:45], v[182:185], v[190:193], v[42:45]
	v_mfma_f32_16x16x32_bf16 v[34:37], v[174:177], v[198:201], v[34:37]
	v_mfma_f32_16x16x32_bf16 v[26:29], v[182:185], v[198:201], v[26:29]
	v_mfma_f32_16x16x32_bf16 v[18:21], v[174:177], v[206:209], v[18:21]
	v_mfma_f32_16x16x32_bf16 v[10:13], v[182:185], v[206:209], v[10:13]
	v_mfma_f32_16x16x32_bf16 v[6:9], v[174:177], v[214:217], v[6:9]
	v_mfma_f32_16x16x32_bf16 v[2:5], v[182:185], v[214:217], v[2:5]
	s_barrier
	s_add_i32 s61, s61, 2
	s_add_u32 s34, s34, 0x100
	s_addc_u32 s35, s35, 0
	s_add_u32 s59, s59, 0x100
	s_addc_u32 s60, s60, 0
	s_cmp_gt_u32 s61, 29
	s_cbranch_scc0 .LBB0_2114
	s_and_b64 vcc, exec, s[12:13]
	s_cbranch_vccz .LBB0_2117
	s_barrier

.LBB0_2363:
	s_setprio 0
	v_readlane_b32 s26, v254, 1
	v_readlane_b32 s27, v254, 2
	s_mov_b32 s23, s99
	s_add_i32 s7, s7, 1
	s_mul_i32 s4, s7, s59
	s_waitcnt lgkmcnt(0)
	s_mul_hi_u32 s5, s7, s23
	s_add_i32 s5, s5, s4
	s_mul_i32 s4, s7, s23
	v_readlane_b32 s23, v254, 14
	s_add_u32 s26, s4, s23
	s_addc_u32 s27, s5, s45
	v_cmp_ge_i64_e32 vcc, s[26:27], v[174:175]
	v_cmp_lt_i64_e64 s[4:5], s[26:27], v[174:175]
	s_cbranch_vccnz .LBB0_2365
	s_ashr_i32 s22, s26, 31
	s_lshr_b32 s22, s22, 29
	s_add_i32 s22, s26, s22
	s_ashr_i32 s23, s22, 3
	s_and_b32 s22, s22, -8
	s_sub_i32 s22, s26, s22
	s_cmp_lt_i32 s22, 0
	s_cselect_b32 s24, s46, s44
	s_mul_i32 s22, s24, s22
	s_add_i32 s22, s22, s23
	s_mul_hi_i32 s23, s22, 0x92492493
	s_add_i32 s23, s23, s22
	s_lshr_b32 s24, s23, 31
	s_ashr_i32 s23, s23, 8
	s_add_i32 s23, s23, s24
	s_lshl_b32 s24, s23, 3
	s_sub_i32 s25, s58, s24
	s_min_i32 s25, s25, 8
	s_abs_i32 s26, s25
	v_cvt_f32_u32_e32 v2, s26
	s_sub_i32 s28, 0, s26
	s_mulk_i32 s23, 0x1c0
	s_sub_i32 s22, s22, s23
	v_rcp_iflag_f32_e32 v2, v2
	s_abs_i32 s23, s22
	s_xor_b32 s27, s22, s25
	s_ashr_i32 s27, s27, 31
	v_mul_f32_e32 v2, 0x4f7ffffe, v2
	v_cvt_u32_f32_e32 v2, v2
	s_nop 0
	v_readfirstlane_b32 s29, v2
	s_mul_i32 s28, s28, s29
	s_mul_hi_u32 s28, s29, s28
	s_add_i32 s29, s29, s28
	s_mul_hi_u32 s28, s23, s29
	s_mul_i32 s29, s28, s26
	s_sub_i32 s23, s23, s29
	s_add_i32 s38, s28, 1
	s_sub_i32 s29, s23, s26
	s_cmp_ge_u32 s23, s26
	s_cselect_b32 s28, s38, s28
	s_cselect_b32 s23, s29, s23
	s_add_i32 s29, s28, 1
	s_cmp_ge_u32 s23, s26
	s_cselect_b32 s23, s29, s28
	s_xor_b32 s23, s23, s27
	s_sub_i32 s64, s23, s27
	s_mul_i32 s23, s64, s25
	s_sub_i32 s22, s22, s23
	s_add_i32 s22, s22, s24
	s_cmp_ge_i32 s22, s57
	s_cselect_b64 s[24:25], -1, 0
	s_cmp_ge_i32 s22, s33
	v_cndmask_b32_e64 v2, 0, 1, s[24:25]
	s_cselect_b64 s[24:25], -1, 0
	s_cmp_ge_i32 s22, s52
	v_cndmask_b32_e64 v3, 0, 1, s[24:25]
	s_cselect_b64 s[24:25], -1, 0
	v_readfirstlane_b32 s23, v3
	v_readfirstlane_b32 s26, v2
	s_cmp_lg_u64 s[24:25], 0
	s_addc_u32 s23, s23, s26
	s_cmp_ge_i32 s22, s53
	s_cselect_b64 s[24:25], -1, 0
	s_cmp_ge_i32 s22, s54
	v_cndmask_b32_e64 v2, 0, 1, s[24:25]
	s_cselect_b64 s[24:25], -1, 0
	v_readfirstlane_b32 s26, v2
	s_cmp_lg_u64 s[24:25], 0
	s_addc_u32 s23, s23, s26
	s_cmp_ge_i32 s22, s55
	s_cselect_b64 s[24:25], -1, 0
	s_cmp_ge_i32 s22, s56
	v_cndmask_b32_e64 v2, 0, 1, s[24:25]
	s_cselect_b64 s[24:25], -1, 0
	v_readfirstlane_b32 s26, v2
	s_cmp_lg_u64 s[24:25], 0
	s_addc_u32 s23, s23, s26
	s_mul_i32 s23, s23, 56
	s_add_i32 s24, s23, s64

.Lrx_2366_0:
	s_waitcnt vmcnt(16)
	s_waitcnt lgkmcnt(0)
	s_barrier
	v_mfma_scale_f32_16x16x128_f8f6f4 v[158:161], v[18:25], v[176:183], 0, v189, v190 op_sel_hi:[0,0,0]
	v_mfma_scale_f32_16x16x128_f8f6f4 v[150:153], v[26:33], v[176:183], 0, v189, v190 op_sel_hi:[0,0,0]
	v_mfma_scale_f32_16x16x128_f8f6f4 v[142:145], v[18:25], v[192:199], 0, v189, v190 op_sel_hi:[0,0,0]
	v_mfma_scale_f32_16x16x128_f8f6f4 v[134:137], v[26:33], v[192:199], 0, v189, v190 op_sel_hi:[0,0,0]
	v_mfma_scale_f32_16x16x128_f8f6f4 v[126:129], v[18:25], v[200:207], 0, v189, v190 op_sel_hi:[0,0,0]
	v_mfma_scale_f32_16x16x128_f8f6f4 v[118:121], v[26:33], v[200:207], 0, v189, v190 op_sel_hi:[0,0,0]
	v_mfma_scale_f32_16x16x128_f8f6f4 v[110:113], v[18:25], v[216:223], 0, v189, v190 op_sel_hi:[0,0,0]
	v_mfma_scale_f32_16x16x128_f8f6f4 v[102:105], v[26:33], v[216:223], 0, v189, v190 op_sel_hi:[0,0,0]
	v_mfma_scale_f32_16x16x128_f8f6f4 v[154:157], v[2:9], v[176:183], 0, v189, v190 op_sel_hi:[0,0,0]
	v_mfma_scale_f32_16x16x128_f8f6f4 v[146:149], v[10:17], v[176:183], 0, v189, v190 op_sel_hi:[0,0,0]
	v_mfma_scale_f32_16x16x128_f8f6f4 v[138:141], v[2:9], v[192:199], 0, v189, v190 op_sel_hi:[0,0,0]
	v_mfma_scale_f32_16x16x128_f8f6f4 v[130:133], v[10:17], v[192:199], 0, v189, v190 op_sel_hi:[0,0,0]
	v_mfma_scale_f32_16x16x128_f8f6f4 v[122:125], v[2:9], v[200:207], 0, v189, v190 op_sel_hi:[0,0,0]
	v_mfma_scale_f32_16x16x128_f8f6f4 v[114:117], v[10:17], v[200:207], 0, v189, v190 op_sel_hi:[0,0,0]
	v_mfma_scale_f32_16x16x128_f8f6f4 v[106:109], v[2:9], v[216:223], 0, v189, v190 op_sel_hi:[0,0,0]
	v_mfma_scale_f32_16x16x128_f8f6f4 v[98:101], v[10:17], v[216:223], 0, v189, v190 op_sel_hi:[0,0,0]
	s_barrier
	s_add_i32 s71, s60, s43
	v_lshl_add_u64 v[176:177], s[36:37], 0, v[166:167]
	s_mov_b32 m0, s71
	ds_read_b128 v[192:195], v188 offset:16384
	ds_read_b128 v[196:199], v188 offset:17408
	ds_read_b128 v[200:203], v188 offset:18432
	ds_read_b128 v[204:207], v188 offset:19456
	ds_read_b128 v[216:219], v188 offset:20480
	ds_read_b128 v[220:223], v188 offset:21504
	ds_read_b128 v[224:227], v188 offset:22528
	ds_read_b128 v[228:231], v188 offset:23552
	global_load_lds_dwordx4 v[176:177], off
	s_add_i32 m0, s71, 0x2000
	s_add_u32 s72, s36, 0x40000
	v_lshl_add_u64 v[178:179], s[36:37], 0, v[162:163]
	s_addc_u32 s73, s37, 0
	s_add_i32 s71, s61, s43
	global_load_lds_dwordx4 v[178:179], off
	v_lshl_add_u64 v[180:181], s[72:73], 0, v[166:167]
	s_mov_b32 m0, s71
	v_lshl_add_u64 v[182:183], s[38:39], 0, v[164:165]
	global_load_lds_dwordx4 v[180:181], off
	v_lshl_add_u64 v[180:181], s[72:73], 0, v[162:163]
	s_add_i32 m0, s71, 0x2000
	s_nop 0
	global_load_lds_dwordx4 v[180:181], off
	v_lshl_add_u64 v[180:181], s[38:39], 0, v[168:169]
	s_mov_b32 m0, s31
	s_nop 0
	global_load_lds_dwordx4 v[180:181], off
	s_mov_b32 m0, s47
	s_nop 0
	global_load_lds_dwordx4 v[182:183], off
	s_cmp_lg_u32 s100, 0
	s_cbranch_scc1 .Lrx_2366_1
	s_waitcnt vmcnt(8)
.Lrx_2366_1:
	s_waitcnt vmcnt(16)
	s_mov_b32 s100, 1
	s_waitcnt lgkmcnt(0)
	s_barrier
	v_mfma_scale_f32_16x16x128_f8f6f4 v[94:97], v[18:25], v[192:199], 0, v189, v190 op_sel_hi:[0,0,0]
	v_mfma_scale_f32_16x16x128_f8f6f4 v[86:89], v[26:33], v[192:199], 0, v189, v190 op_sel_hi:[0,0,0]
	v_mfma_scale_f32_16x16x128_f8f6f4 v[78:81], v[18:25], v[200:207], 0, v189, v190 op_sel_hi:[0,0,0]
	v_mfma_scale_f32_16x16x128_f8f6f4 v[70:73], v[26:33], v[200:207], 0, v189, v190 op_sel_hi:[0,0,0]
	v_mfma_scale_f32_16x16x128_f8f6f4 v[62:65], v[18:25], v[216:223], 0, v189, v190 op_sel_hi:[0,0,0]
	v_mfma_scale_f32_16x16x128_f8f6f4 v[54:57], v[26:33], v[216:223], 0, v189, v190 op_sel_hi:[0,0,0]
	v_mfma_scale_f32_16x16x128_f8f6f4 v[46:49], v[18:25], v[224:231], 0, v189, v190 op_sel_hi:[0,0,0]
	v_mfma_scale_f32_16x16x128_f8f6f4 v[38:41], v[26:33], v[224:231], 0, v189, v190 op_sel_hi:[0,0,0]
	v_mfma_scale_f32_16x16x128_f8f6f4 v[90:93], v[2:9], v[192:199], 0, v189, v190 op_sel_hi:[0,0,0]
	v_mfma_scale_f32_16x16x128_f8f6f4 v[82:85], v[10:17], v[192:199], 0, v189, v190 op_sel_hi:[0,0,0]
	v_mfma_scale_f32_16x16x128_f8f6f4 v[74:77], v[2:9], v[200:207], 0, v189, v190 op_sel_hi:[0,0,0]
	v_mfma_scale_f32_16x16x128_f8f6f4 v[66:69], v[10:17], v[200:207], 0, v189, v190 op_sel_hi:[0,0,0]
	v_mfma_scale_f32_16x16x128_f8f6f4 v[58:61], v[2:9], v[216:223], 0, v189, v190 op_sel_hi:[0,0,0]
	v_mfma_scale_f32_16x16x128_f8f6f4 v[50:53], v[10:17], v[216:223], 0, v189, v190 op_sel_hi:[0,0,0]
	v_mfma_scale_f32_16x16x128_f8f6f4 v[42:45], v[2:9], v[224:231], 0, v189, v190 op_sel_hi:[0,0,0]
	v_mfma_scale_f32_16x16x128_f8f6f4 v[34:37], v[10:17], v[224:231], 0, v189, v190 op_sel_hi:[0,0,0]
	s_barrier
	s_add_i32 s71, 0, 0x18000
	s_add_i32 s72, 0, 0x1c000
	v_add_u32_e32 v14, s71, v184
	v_add_u32_e32 v30, s72, v184
	ds_read_b128 v[2:5], v14
	ds_read_b128 v[6:9], v14 offset:1024
	ds_read_b128 v[10:13], v14 offset:2048
	ds_read_b128 v[14:17], v14 offset:3072
	ds_read_b128 v[18:21], v30
	ds_read_b128 v[22:25], v30 offset:1024
	ds_read_b128 v[26:29], v30 offset:2048
	ds_read_b128 v[30:33], v30 offset:3072
	s_add_u32 s38, s38, 0x40000
	s_addc_u32 s39, s39, 0
	s_mov_b32 m0, s48
	v_lshl_add_u64 v[208:209], s[38:39], 0, v[168:169]
	ds_read_b128 v[192:195], v188 offset:32768
	ds_read_b128 v[196:199], v188 offset:33792
	ds_read_b128 v[200:203], v188 offset:34816
	ds_read_b128 v[204:207], v188 offset:35840
	ds_read_b128 v[216:219], v188 offset:36864
	ds_read_b128 v[220:223], v188 offset:37888
	ds_read_b128 v[224:227], v188 offset:38912
	ds_read_b128 v[228:231], v188 offset:39936
	global_load_lds_dwordx4 v[208:209], off
	v_lshl_add_u64 v[208:209], s[38:39], 0, v[164:165]
	s_mov_b32 m0, s49
	s_nop 0
	global_load_lds_dwordx4 v[208:209], off
	s_waitcnt vmcnt(8)
	s_waitcnt lgkmcnt(0)
	s_barrier
	v_mfma_scale_f32_16x16x128_f8f6f4 v[158:161], v[2:9], v[192:199], v[158:161], v189, v190 op_sel_hi:[0,0,0]
	v_mfma_scale_f32_16x16x128_f8f6f4 v[150:153], v[10:17], v[192:199], v[150:153], v189, v190 op_sel_hi:[0,0,0]
	v_mfma_scale_f32_16x16x128_f8f6f4 v[142:145], v[2:9], v[200:207], v[142:145], v189, v190 op_sel_hi:[0,0,0]
	v_mfma_scale_f32_16x16x128_f8f6f4 v[134:137], v[10:17], v[200:207], v[134:137], v189, v190 op_sel_hi:[0,0,0]
	v_mfma_scale_f32_16x16x128_f8f6f4 v[126:129], v[2:9], v[216:223], v[126:129], v189, v190 op_sel_hi:[0,0,0]
	v_mfma_scale_f32_16x16x128_f8f6f4 v[118:121], v[10:17], v[216:223], v[118:121], v189, v190 op_sel_hi:[0,0,0]
	v_mfma_scale_f32_16x16x128_f8f6f4 v[110:113], v[2:9], v[224:231], v[110:113], v189, v190 op_sel_hi:[0,0,0]
	v_mfma_scale_f32_16x16x128_f8f6f4 v[102:105], v[10:17], v[224:231], v[102:105], v189, v190 op_sel_hi:[0,0,0]
	v_mfma_scale_f32_16x16x128_f8f6f4 v[154:157], v[18:25], v[192:199], v[154:157], v189, v190 op_sel_hi:[0,0,0]
	v_mfma_scale_f32_16x16x128_f8f6f4 v[146:149], v[26:33], v[192:199], v[146:149], v189, v190 op_sel_hi:[0,0,0]
	v_mfma_scale_f32_16x16x128_f8f6f4 v[138:141], v[18:25], v[200:207], v[138:141], v189, v190 op_sel_hi:[0,0,0]
	v_mfma_scale_f32_16x16x128_f8f6f4 v[130:133], v[26:33], v[200:207], v[130:133], v189, v190 op_sel_hi:[0,0,0]
	v_mfma_scale_f32_16x16x128_f8f6f4 v[122:125], v[18:25], v[216:223], v[122:125], v189, v190 op_sel_hi:[0,0,0]
	v_mfma_scale_f32_16x16x128_f8f6f4 v[114:117], v[26:33], v[216:223], v[114:117], v189, v190 op_sel_hi:[0,0,0]
	v_mfma_scale_f32_16x16x128_f8f6f4 v[106:109], v[18:25], v[224:231], v[106:109], v189, v190 op_sel_hi:[0,0,0]
	v_mfma_scale_f32_16x16x128_f8f6f4 v[98:101], v[26:33], v[224:231], v[98:101], v189, v190 op_sel_hi:[0,0,0]
	s_barrier
	s_add_i32 s38, s71, s43
	v_lshl_add_u64 v[176:177], v[176:177], 0, s[12:13]
	s_mov_b32 m0, s38
	ds_read_b128 v[192:195], v188 offset:49152
	ds_read_b128 v[196:199], v188 offset:50176
	ds_read_b128 v[200:203], v188 offset:51200
	ds_read_b128 v[204:207], v188 offset:52224
	ds_read_b128 v[216:219], v188 offset:53248
	ds_read_b128 v[220:223], v188 offset:54272
	ds_read_b128 v[224:227], v188 offset:55296
	ds_read_b128 v[228:231], v188 offset:56320
	global_load_lds_dwordx4 v[176:177], off
	s_add_i32 m0, s38, 0x2000
	s_add_u32 s36, s36, 0x40080
	v_lshl_add_u64 v[176:177], v[178:179], 0, s[12:13]
	s_addc_u32 s37, s37, 0
	s_add_i32 s38, s72, s43
	global_load_lds_dwordx4 v[176:177], off
	v_lshl_add_u64 v[176:177], s[36:37], 0, v[166:167]
	s_mov_b32 m0, s38
	s_nop 0
	global_load_lds_dwordx4 v[176:177], off
	v_lshl_add_u64 v[176:177], s[36:37], 0, v[162:163]
	s_add_i32 m0, s38, 0x2000
	s_nop 0
	global_load_lds_dwordx4 v[176:177], off
	v_lshl_add_u64 v[176:177], v[180:181], 0, s[12:13]
	s_mov_b32 m0, s50
	s_nop 0
	global_load_lds_dwordx4 v[176:177], off
	v_lshl_add_u64 v[176:177], v[182:183], 0, s[12:13]
	s_mov_b32 m0, s51
	s_nop 0
	global_load_lds_dwordx4 v[176:177], off
	s_waitcnt vmcnt(8)
	s_waitcnt lgkmcnt(0)
	s_barrier
	v_mfma_scale_f32_16x16x128_f8f6f4 v[94:97], v[2:9], v[192:199], v[94:97], v189, v190 op_sel_hi:[0,0,0]
	v_mfma_scale_f32_16x16x128_f8f6f4 v[86:89], v[10:17], v[192:199], v[86:89], v189, v190 op_sel_hi:[0,0,0]
	v_mfma_scale_f32_16x16x128_f8f6f4 v[78:81], v[2:9], v[200:207], v[78:81], v189, v190 op_sel_hi:[0,0,0]
	v_mfma_scale_f32_16x16x128_f8f6f4 v[70:73], v[10:17], v[200:207], v[70:73], v189, v190 op_sel_hi:[0,0,0]
	v_mfma_scale_f32_16x16x128_f8f6f4 v[62:65], v[2:9], v[216:223], v[62:65], v189, v190 op_sel_hi:[0,0,0]
	v_mfma_scale_f32_16x16x128_f8f6f4 v[54:57], v[10:17], v[216:223], v[54:57], v189, v190 op_sel_hi:[0,0,0]
	v_mfma_scale_f32_16x16x128_f8f6f4 v[46:49], v[2:9], v[224:231], v[46:49], v189, v190 op_sel_hi:[0,0,0]
	v_mfma_scale_f32_16x16x128_f8f6f4 v[38:41], v[10:17], v[224:231], v[38:41], v189, v190 op_sel_hi:[0,0,0]
	v_mfma_scale_f32_16x16x128_f8f6f4 v[90:93], v[18:25], v[192:199], v[90:93], v189, v190 op_sel_hi:[0,0,0]
	v_mfma_scale_f32_16x16x128_f8f6f4 v[82:85], v[26:33], v[192:199], v[82:85], v189, v190 op_sel_hi:[0,0,0]
	v_mfma_scale_f32_16x16x128_f8f6f4 v[74:77], v[18:25], v[200:207], v[74:77], v189, v190 op_sel_hi:[0,0,0]
	v_mfma_scale_f32_16x16x128_f8f6f4 v[66:69], v[26:33], v[200:207], v[66:69], v189, v190 op_sel_hi:[0,0,0]
	v_mfma_scale_f32_16x16x128_f8f6f4 v[58:61], v[18:25], v[216:223], v[58:61], v189, v190 op_sel_hi:[0,0,0]
	v_mfma_scale_f32_16x16x128_f8f6f4 v[50:53], v[26:33], v[216:223], v[50:53], v189, v190 op_sel_hi:[0,0,0]
	v_mfma_scale_f32_16x16x128_f8f6f4 v[42:45], v[18:25], v[224:231], v[42:45], v189, v190 op_sel_hi:[0,0,0]
	v_mfma_scale_f32_16x16x128_f8f6f4 v[34:37], v[26:33], v[224:231], v[34:37], v189, v190 op_sel_hi:[0,0,0]
	s_barrier
	s_add_i32 s70, s70, 2
	s_add_u32 s34, s34, 0x100
	s_addc_u32 s35, s35, 0
	s_add_u32 s68, s68, 0x100
	s_addc_u32 s69, s69, 0
	s_cmp_gt_u32 s70, 13
.LBB0_2366:
	ds_read_b128 v[18:21], v186
	ds_read_b128 v[22:25], v186 offset:1024
	ds_read_b128 v[26:29], v186 offset:2048
	ds_read_b128 v[30:33], v186 offset:3072
	ds_read_b128 v[2:5], v187
	ds_read_b128 v[6:9], v187 offset:1024
	ds_read_b128 v[10:13], v187 offset:2048
	ds_read_b128 v[14:17], v187 offset:3072
	s_add_u32 s36, s34, 0xfffc0080
	s_addc_u32 s37, s35, -1
	s_cmp_eq_u32 s70, 12
	s_cselect_b32 s39, s23, s37
	s_cselect_b32 s38, s66, s36
	s_cselect_b32 s37, s25, s69
	s_cselect_b32 s36, s67, s68
	v_lshl_add_u64 v[208:209], s[34:35], 0, v[170:171]
	s_add_i32 m0, s31, 0xc000
	ds_read_b128 v[176:179], v188
	ds_read_b128 v[180:183], v188 offset:1024
	ds_read_b128 v[192:195], v188 offset:2048
	ds_read_b128 v[196:199], v188 offset:3072
	ds_read_b128 v[200:203], v188 offset:4096
	ds_read_b128 v[204:207], v188 offset:5120
	ds_read_b128 v[216:219], v188 offset:6144
	ds_read_b128 v[220:223], v188 offset:7168
	global_load_lds_dwordx4 v[208:209], off
	v_lshl_add_u64 v[208:209], s[34:35], 0, v[172:173]
	s_add_i32 m0, s31, 0xe000
	s_nop 0
	global_load_lds_dwordx4 v[208:209], off
	s_waitcnt vmcnt(8)
	s_waitcnt lgkmcnt(0)
	s_barrier
	v_mfma_scale_f32_16x16x128_f8f6f4 v[158:161], v[18:25], v[176:183], v[158:161], v189, v190 op_sel_hi:[0,0,0]
	v_mfma_scale_f32_16x16x128_f8f6f4 v[150:153], v[26:33], v[176:183], v[150:153], v189, v190 op_sel_hi:[0,0,0]
	v_mfma_scale_f32_16x16x128_f8f6f4 v[142:145], v[18:25], v[192:199], v[142:145], v189, v190 op_sel_hi:[0,0,0]
	v_mfma_scale_f32_16x16x128_f8f6f4 v[134:137], v[26:33], v[192:199], v[134:137], v189, v190 op_sel_hi:[0,0,0]
	v_mfma_scale_f32_16x16x128_f8f6f4 v[126:129], v[18:25], v[200:207], v[126:129], v189, v190 op_sel_hi:[0,0,0]
	v_mfma_scale_f32_16x16x128_f8f6f4 v[118:121], v[26:33], v[200:207], v[118:121], v189, v190 op_sel_hi:[0,0,0]
	v_mfma_scale_f32_16x16x128_f8f6f4 v[110:113], v[18:25], v[216:223], v[110:113], v189, v190 op_sel_hi:[0,0,0]
	v_mfma_scale_f32_16x16x128_f8f6f4 v[102:105], v[26:33], v[216:223], v[102:105], v189, v190 op_sel_hi:[0,0,0]
	v_mfma_scale_f32_16x16x128_f8f6f4 v[154:157], v[2:9], v[176:183], v[154:157], v189, v190 op_sel_hi:[0,0,0]
	v_mfma_scale_f32_16x16x128_f8f6f4 v[146:149], v[10:17], v[176:183], v[146:149], v189, v190 op_sel_hi:[0,0,0]
	v_mfma_scale_f32_16x16x128_f8f6f4 v[138:141], v[2:9], v[192:199], v[138:141], v189, v190 op_sel_hi:[0,0,0]
	v_mfma_scale_f32_16x16x128_f8f6f4 v[130:133], v[10:17], v[192:199], v[130:133], v189, v190 op_sel_hi:[0,0,0]
	v_mfma_scale_f32_16x16x128_f8f6f4 v[122:125], v[2:9], v[200:207], v[122:125], v189, v190 op_sel_hi:[0,0,0]
	v_mfma_scale_f32_16x16x128_f8f6f4 v[114:117], v[10:17], v[200:207], v[114:117], v189, v190 op_sel_hi:[0,0,0]
	v_mfma_scale_f32_16x16x128_f8f6f4 v[106:109], v[2:9], v[216:223], v[106:109], v189, v190 op_sel_hi:[0,0,0]
	v_mfma_scale_f32_16x16x128_f8f6f4 v[98:101], v[10:17], v[216:223], v[98:101], v189, v190 op_sel_hi:[0,0,0]
	s_barrier
	s_add_i32 s71, s60, s43
	v_lshl_add_u64 v[176:177], s[36:37], 0, v[166:167]
	s_mov_b32 m0, s71
	ds_read_b128 v[192:195], v188 offset:16384
	ds_read_b128 v[196:199], v188 offset:17408
	ds_read_b128 v[200:203], v188 offset:18432
	ds_read_b128 v[204:207], v188 offset:19456
	ds_read_b128 v[216:219], v188 offset:20480
	ds_read_b128 v[220:223], v188 offset:21504
	ds_read_b128 v[224:227], v188 offset:22528
	ds_read_b128 v[228:231], v188 offset:23552
	global_load_lds_dwordx4 v[176:177], off
	s_add_i32 m0, s71, 0x2000
	s_add_u32 s72, s36, 0x40000
	v_lshl_add_u64 v[178:179], s[36:37], 0, v[162:163]
	s_addc_u32 s73, s37, 0
	s_add_i32 s71, s61, s43
	global_load_lds_dwordx4 v[178:179], off
	v_lshl_add_u64 v[180:181], s[72:73], 0, v[166:167]
	s_mov_b32 m0, s71
	v_lshl_add_u64 v[182:183], s[38:39], 0, v[164:165]
	global_load_lds_dwordx4 v[180:181], off
	v_lshl_add_u64 v[180:181], s[72:73], 0, v[162:163]
	s_add_i32 m0, s71, 0x2000
	s_nop 0
	global_load_lds_dwordx4 v[180:181], off
	v_lshl_add_u64 v[180:181], s[38:39], 0, v[168:169]
	s_mov_b32 m0, s31
	s_nop 0
	global_load_lds_dwordx4 v[180:181], off
	s_mov_b32 m0, s47
	s_nop 0
	global_load_lds_dwordx4 v[182:183], off
	s_waitcnt vmcnt(8)
	s_waitcnt lgkmcnt(0)
	s_barrier
	v_mfma_scale_f32_16x16x128_f8f6f4 v[94:97], v[18:25], v[192:199], v[94:97], v189, v190 op_sel_hi:[0,0,0]
	v_mfma_scale_f32_16x16x128_f8f6f4 v[86:89], v[26:33], v[192:199], v[86:89], v189, v190 op_sel_hi:[0,0,0]
	v_mfma_scale_f32_16x16x128_f8f6f4 v[78:81], v[18:25], v[200:207], v[78:81], v189, v190 op_sel_hi:[0,0,0]
	v_mfma_scale_f32_16x16x128_f8f6f4 v[70:73], v[26:33], v[200:207], v[70:73], v189, v190 op_sel_hi:[0,0,0]
	v_mfma_scale_f32_16x16x128_f8f6f4 v[62:65], v[18:25], v[216:223], v[62:65], v189, v190 op_sel_hi:[0,0,0]
	v_mfma_scale_f32_16x16x128_f8f6f4 v[54:57], v[26:33], v[216:223], v[54:57], v189, v190 op_sel_hi:[0,0,0]
	v_mfma_scale_f32_16x16x128_f8f6f4 v[46:49], v[18:25], v[224:231], v[46:49], v189, v190 op_sel_hi:[0,0,0]
	v_mfma_scale_f32_16x16x128_f8f6f4 v[38:41], v[26:33], v[224:231], v[38:41], v189, v190 op_sel_hi:[0,0,0]
	v_mfma_scale_f32_16x16x128_f8f6f4 v[90:93], v[2:9], v[192:199], v[90:93], v189, v190 op_sel_hi:[0,0,0]
	v_mfma_scale_f32_16x16x128_f8f6f4 v[82:85], v[10:17], v[192:199], v[82:85], v189, v190 op_sel_hi:[0,0,0]
	v_mfma_scale_f32_16x16x128_f8f6f4 v[74:77], v[2:9], v[200:207], v[74:77], v189, v190 op_sel_hi:[0,0,0]
	v_mfma_scale_f32_16x16x128_f8f6f4 v[66:69], v[10:17], v[200:207], v[66:69], v189, v190 op_sel_hi:[0,0,0]
	v_mfma_scale_f32_16x16x128_f8f6f4 v[58:61], v[2:9], v[216:223], v[58:61], v189, v190 op_sel_hi:[0,0,0]
	v_mfma_scale_f32_16x16x128_f8f6f4 v[50:53], v[10:17], v[216:223], v[50:53], v189, v190 op_sel_hi:[0,0,0]
	v_mfma_scale_f32_16x16x128_f8f6f4 v[42:45], v[2:9], v[224:231], v[42:45], v189, v190 op_sel_hi:[0,0,0]
	v_mfma_scale_f32_16x16x128_f8f6f4 v[34:37], v[10:17], v[224:231], v[34:37], v189, v190 op_sel_hi:[0,0,0]
	s_barrier
	s_add_i32 s71, 0, 0x18000
	s_add_i32 s72, 0, 0x1c000
	v_add_u32_e32 v14, s71, v184
	v_add_u32_e32 v30, s72, v184
	ds_read_b128 v[2:5], v14
	ds_read_b128 v[6:9], v14 offset:1024
	ds_read_b128 v[10:13], v14 offset:2048
	ds_read_b128 v[14:17], v14 offset:3072
	ds_read_b128 v[18:21], v30
	ds_read_b128 v[22:25], v30 offset:1024
	ds_read_b128 v[26:29], v30 offset:2048
	ds_read_b128 v[30:33], v30 offset:3072
	s_add_u32 s38, s38, 0x40000
	s_addc_u32 s39, s39, 0
	s_mov_b32 m0, s48
	v_lshl_add_u64 v[208:209], s[38:39], 0, v[168:169]
	ds_read_b128 v[192:195], v188 offset:32768
	ds_read_b128 v[196:199], v188 offset:33792
	ds_read_b128 v[200:203], v188 offset:34816
	ds_read_b128 v[204:207], v188 offset:35840
	ds_read_b128 v[216:219], v188 offset:36864
	ds_read_b128 v[220:223], v188 offset:37888
	ds_read_b128 v[224:227], v188 offset:38912
	ds_read_b128 v[228:231], v188 offset:39936
	global_load_lds_dwordx4 v[208:209], off
	v_lshl_add_u64 v[208:209], s[38:39], 0, v[164:165]
	s_mov_b32 m0, s49
	s_nop 0
	global_load_lds_dwordx4 v[208:209], off
	s_waitcnt vmcnt(8)
	s_waitcnt lgkmcnt(0)
	s_barrier
	v_mfma_scale_f32_16x16x128_f8f6f4 v[158:161], v[2:9], v[192:199], v[158:161], v189, v190 op_sel_hi:[0,0,0]
	v_mfma_scale_f32_16x16x128_f8f6f4 v[150:153], v[10:17], v[192:199], v[150:153], v189, v190 op_sel_hi:[0,0,0]
	v_mfma_scale_f32_16x16x128_f8f6f4 v[142:145], v[2:9], v[200:207], v[142:145], v189, v190 op_sel_hi:[0,0,0]
	v_mfma_scale_f32_16x16x128_f8f6f4 v[134:137], v[10:17], v[200:207], v[134:137], v189, v190 op_sel_hi:[0,0,0]
	v_mfma_scale_f32_16x16x128_f8f6f4 v[126:129], v[2:9], v[216:223], v[126:129], v189, v190 op_sel_hi:[0,0,0]
	v_mfma_scale_f32_16x16x128_f8f6f4 v[118:121], v[10:17], v[216:223], v[118:121], v189, v190 op_sel_hi:[0,0,0]
	v_mfma_scale_f32_16x16x128_f8f6f4 v[110:113], v[2:9], v[224:231], v[110:113], v189, v190 op_sel_hi:[0,0,0]
	v_mfma_scale_f32_16x16x128_f8f6f4 v[102:105], v[10:17], v[224:231], v[102:105], v189, v190 op_sel_hi:[0,0,0]
	v_mfma_scale_f32_16x16x128_f8f6f4 v[154:157], v[18:25], v[192:199], v[154:157], v189, v190 op_sel_hi:[0,0,0]
	v_mfma_scale_f32_16x16x128_f8f6f4 v[146:149], v[26:33], v[192:199], v[146:149], v189, v190 op_sel_hi:[0,0,0]
	v_mfma_scale_f32_16x16x128_f8f6f4 v[138:141], v[18:25], v[200:207], v[138:141], v189, v190 op_sel_hi:[0,0,0]
	v_mfma_scale_f32_16x16x128_f8f6f4 v[130:133], v[26:33], v[200:207], v[130:133], v189, v190 op_sel_hi:[0,0,0]
	v_mfma_scale_f32_16x16x128_f8f6f4 v[122:125], v[18:25], v[216:223], v[122:125], v189, v190 op_sel_hi:[0,0,0]
	v_mfma_scale_f32_16x16x128_f8f6f4 v[114:117], v[26:33], v[216:223], v[114:117], v189, v190 op_sel_hi:[0,0,0]
	v_mfma_scale_f32_16x16x128_f8f6f4 v[106:109], v[18:25], v[224:231], v[106:109], v189, v190 op_sel_hi:[0,0,0]
	v_mfma_scale_f32_16x16x128_f8f6f4 v[98:101], v[26:33], v[224:231], v[98:101], v189, v190 op_sel_hi:[0,0,0]
	s_barrier
	s_add_i32 s38, s71, s43
	v_lshl_add_u64 v[176:177], v[176:177], 0, s[12:13]
	s_mov_b32 m0, s38
	ds_read_b128 v[192:195], v188 offset:49152
	ds_read_b128 v[196:199], v188 offset:50176
	ds_read_b128 v[200:203], v188 offset:51200
	ds_read_b128 v[204:207], v188 offset:52224
	ds_read_b128 v[216:219], v188 offset:53248
	ds_read_b128 v[220:223], v188 offset:54272
	ds_read_b128 v[224:227], v188 offset:55296
	ds_read_b128 v[228:231], v188 offset:56320
	global_load_lds_dwordx4 v[176:177], off
	s_add_i32 m0, s38, 0x2000
	s_add_u32 s36, s36, 0x40080
	v_lshl_add_u64 v[176:177], v[178:179], 0, s[12:13]
	s_addc_u32 s37, s37, 0
	s_add_i32 s38, s72, s43
	global_load_lds_dwordx4 v[176:177], off
	v_lshl_add_u64 v[176:177], s[36:37], 0, v[166:167]
	s_mov_b32 m0, s38
	s_nop 0
	global_load_lds_dwordx4 v[176:177], off
	v_lshl_add_u64 v[176:177], s[36:37], 0, v[162:163]
	s_add_i32 m0, s38, 0x2000
	s_nop 0
	global_load_lds_dwordx4 v[176:177], off
	v_lshl_add_u64 v[176:177], v[180:181], 0, s[12:13]
	s_mov_b32 m0, s50
	s_nop 0
	global_load_lds_dwordx4 v[176:177], off
	v_lshl_add_u64 v[176:177], v[182:183], 0, s[12:13]
	s_mov_b32 m0, s51
	s_nop 0
	global_load_lds_dwordx4 v[176:177], off
	s_waitcnt vmcnt(8)
	s_waitcnt lgkmcnt(0)
	s_barrier
	v_mfma_scale_f32_16x16x128_f8f6f4 v[94:97], v[2:9], v[192:199], v[94:97], v189, v190 op_sel_hi:[0,0,0]
	v_mfma_scale_f32_16x16x128_f8f6f4 v[86:89], v[10:17], v[192:199], v[86:89], v189, v190 op_sel_hi:[0,0,0]
	v_mfma_scale_f32_16x16x128_f8f6f4 v[78:81], v[2:9], v[200:207], v[78:81], v189, v190 op_sel_hi:[0,0,0]
	v_mfma_scale_f32_16x16x128_f8f6f4 v[70:73], v[10:17], v[200:207], v[70:73], v189, v190 op_sel_hi:[0,0,0]
	v_mfma_scale_f32_16x16x128_f8f6f4 v[62:65], v[2:9], v[216:223], v[62:65], v189, v190 op_sel_hi:[0,0,0]
	v_mfma_scale_f32_16x16x128_f8f6f4 v[54:57], v[10:17], v[216:223], v[54:57], v189, v190 op_sel_hi:[0,0,0]
	v_mfma_scale_f32_16x16x128_f8f6f4 v[46:49], v[2:9], v[224:231], v[46:49], v189, v190 op_sel_hi:[0,0,0]
	v_mfma_scale_f32_16x16x128_f8f6f4 v[38:41], v[10:17], v[224:231], v[38:41], v189, v190 op_sel_hi:[0,0,0]
	v_mfma_scale_f32_16x16x128_f8f6f4 v[90:93], v[18:25], v[192:199], v[90:93], v189, v190 op_sel_hi:[0,0,0]
	v_mfma_scale_f32_16x16x128_f8f6f4 v[82:85], v[26:33], v[192:199], v[82:85], v189, v190 op_sel_hi:[0,0,0]
	v_mfma_scale_f32_16x16x128_f8f6f4 v[74:77], v[18:25], v[200:207], v[74:77], v189, v190 op_sel_hi:[0,0,0]
	v_mfma_scale_f32_16x16x128_f8f6f4 v[66:69], v[26:33], v[200:207], v[66:69], v189, v190 op_sel_hi:[0,0,0]
	v_mfma_scale_f32_16x16x128_f8f6f4 v[58:61], v[18:25], v[216:223], v[58:61], v189, v190 op_sel_hi:[0,0,0]
	v_mfma_scale_f32_16x16x128_f8f6f4 v[50:53], v[26:33], v[216:223], v[50:53], v189, v190 op_sel_hi:[0,0,0]
	v_mfma_scale_f32_16x16x128_f8f6f4 v[42:45], v[18:25], v[224:231], v[42:45], v189, v190 op_sel_hi:[0,0,0]
	v_mfma_scale_f32_16x16x128_f8f6f4 v[34:37], v[26:33], v[224:231], v[34:37], v189, v190 op_sel_hi:[0,0,0]
	s_barrier
	s_add_i32 s70, s70, 2
	s_add_u32 s34, s34, 0x100
	s_addc_u32 s35, s35, 0
	s_add_u32 s68, s68, 0x100
	s_addc_u32 s69, s69, 0
	s_cmp_gt_u32 s70, 13
	s_cbranch_scc0 .LBB0_2366
	s_and_b64 vcc, exec, s[16:17]
	s_cbranch_vccz .LBB0_2369
	s_barrier

.LBB0_2434:
	s_setprio 0
	v_readlane_b32 s4, v254, 1
	v_readlane_b32 s5, v254, 2
	s_mov_b32 s4, s99
	s_add_i32 s7, s7, 1
	s_mul_i32 s0, s7, s61
	s_waitcnt lgkmcnt(0)
	s_mul_hi_u32 s1, s7, s4
	s_add_i32 s1, s1, s0
	s_mul_i32 s0, s7, s4
	v_readlane_b32 s4, v254, 14
	s_add_u32 s4, s0, s4
	s_addc_u32 s5, s1, s45
	v_cmp_ge_i64_e32 vcc, s[4:5], v[172:173]
	v_cmp_lt_i64_e64 s[0:1], s[4:5], v[172:173]
	s_cbranch_vccnz .LBB0_2436
	s_ashr_i32 s5, s4, 31
	s_lshr_b32 s5, s5, 29
	s_add_i32 s5, s4, s5
	s_ashr_i32 s40, s5, 3
	s_and_b32 s5, s5, -8
	s_sub_i32 s4, s4, s5
	s_cmp_lt_i32 s4, 0
	s_cselect_b32 s5, s46, s58
	s_mul_i32 s4, s5, s4
	s_add_i32 s4, s4, s40
	s_ashr_i32 s5, s4, 31
	s_lshr_b32 s5, s5, 26
	s_add_i32 s5, s4, s5
	s_ashr_i32 s40, s5, 6
	s_lshl_b32 s40, s40, 3
	s_sub_i32 s41, s58, s40
	s_min_i32 s41, s41, 8
	s_abs_i32 s67, s41
	v_cvt_f32_u32_e32 v2, s67
	s_sub_i32 s71, 0, s67
	s_andn2_b32 s5, s5, 63
	s_sub_i32 s4, s4, s5
	v_rcp_iflag_f32_e32 v2, v2
	s_abs_i32 s5, s4
	s_xor_b32 s68, s4, s41
	s_ashr_i32 s68, s68, 31
	v_mul_f32_e32 v2, 0x4f7ffffe, v2
	v_cvt_u32_f32_e32 v2, v2
	s_nop 0
	v_readfirstlane_b32 s72, v2
	s_mul_i32 s71, s71, s72
	s_mul_hi_u32 s71, s72, s71
	s_add_i32 s72, s72, s71
	s_mul_hi_u32 s71, s5, s72
	s_mul_i32 s72, s71, s67
	s_sub_i32 s5, s5, s72
	s_add_i32 s73, s71, 1
	s_sub_i32 s72, s5, s67
	s_cmp_ge_u32 s5, s67
	s_cselect_b32 s71, s73, s71
	s_cselect_b32 s5, s72, s5
	s_add_i32 s72, s71, 1
	s_cmp_ge_u32 s5, s67
	s_cselect_b32 s5, s72, s71
	s_xor_b32 s5, s5, s68
	s_sub_i32 s67, s5, s68
	s_mul_i32 s5, s67, s41
	s_sub_i32 s4, s4, s5
	s_add_i32 s68, s4, s40
	s_cmp_ge_i32 s68, s57
	s_cselect_b64 s[4:5], -1, 0
	s_cmp_ge_i32 s68, s33
	v_cndmask_b32_e64 v2, 0, 1, s[4:5]
	s_cselect_b64 s[4:5], -1, 0
	s_cmp_ge_i32 s68, s52
	v_cndmask_b32_e64 v3, 0, 1, s[4:5]
	s_cselect_b64 vcc, -1, 0
	s_cmp_ge_i32 s68, s53
	v_addc_co_u32_e32 v2, vcc, v3, v2, vcc
	s_cselect_b64 s[4:5], -1, 0
	s_cmp_ge_i32 s68, s54
	v_cndmask_b32_e64 v3, 0, 1, s[4:5]
	s_cselect_b64 vcc, -1, 0
	s_cmp_ge_i32 s68, s55
	v_addc_co_u32_e32 v2, vcc, v2, v3, vcc
	s_cselect_b64 s[4:5], -1, 0
	s_cmp_ge_i32 s68, s56
	v_cndmask_b32_e64 v3, 0, 1, s[4:5]
	s_cselect_b64 vcc, -1, 0
	v_addc_co_u32_e32 v2, vcc, v2, v3, vcc
	v_lshlrev_b32_e32 v2, 3, v2
	v_add_u32_e32 v196, s67, v2

.Lrx_2441_0:
	s_waitcnt vmcnt(24)
	s_waitcnt lgkmcnt(0)
	s_barrier
	v_mfma_scale_f32_16x16x128_f8f6f4 v[156:159], v[16:23], v[180:187], 0, v194, v195 op_sel_hi:[0,0,0]
	v_mfma_scale_f32_16x16x128_f8f6f4 v[152:155], v[24:31], v[180:187], 0, v194, v195 op_sel_hi:[0,0,0]
	v_mfma_scale_f32_16x16x128_f8f6f4 v[148:151], v[16:23], v[198:205], 0, v194, v195 op_sel_hi:[0,0,0]
	v_mfma_scale_f32_16x16x128_f8f6f4 v[140:143], v[24:31], v[198:205], 0, v194, v195 op_sel_hi:[0,0,0]
	v_mfma_scale_f32_16x16x128_f8f6f4 v[132:135], v[16:23], v[206:213], 0, v194, v195 op_sel_hi:[0,0,0]
	v_mfma_scale_f32_16x16x128_f8f6f4 v[124:127], v[24:31], v[206:213], 0, v194, v195 op_sel_hi:[0,0,0]
	v_mfma_scale_f32_16x16x128_f8f6f4 v[116:119], v[16:23], v[216:223], 0, v194, v195 op_sel_hi:[0,0,0]
	v_mfma_scale_f32_16x16x128_f8f6f4 v[108:111], v[24:31], v[216:223], 0, v194, v195 op_sel_hi:[0,0,0]
	v_mfma_scale_f32_16x16x128_f8f6f4 v[144:147], v[0:7], v[180:187], 0, v194, v195 op_sel_hi:[0,0,0]
	v_mfma_scale_f32_16x16x128_f8f6f4 v[136:139], v[8:15], v[180:187], 0, v194, v195 op_sel_hi:[0,0,0]
	v_mfma_scale_f32_16x16x128_f8f6f4 v[128:131], v[0:7], v[198:205], 0, v194, v195 op_sel_hi:[0,0,0]
	v_mfma_scale_f32_16x16x128_f8f6f4 v[120:123], v[8:15], v[198:205], 0, v194, v195 op_sel_hi:[0,0,0]
	v_mfma_scale_f32_16x16x128_f8f6f4 v[112:115], v[0:7], v[206:213], 0, v194, v195 op_sel_hi:[0,0,0]
	v_mfma_scale_f32_16x16x128_f8f6f4 v[104:107], v[8:15], v[206:213], 0, v194, v195 op_sel_hi:[0,0,0]
	v_mfma_scale_f32_16x16x128_f8f6f4 v[100:103], v[0:7], v[216:223], 0, v194, v195 op_sel_hi:[0,0,0]
	v_mfma_scale_f32_16x16x128_f8f6f4 v[96:99], v[8:15], v[216:223], 0, v194, v195 op_sel_hi:[0,0,0]
	s_barrier
	s_add_i32 s72, s6, s44
	v_lshl_add_u64 v[180:181], v[178:179], 0, v[164:165]
	s_mov_b32 m0, s72
	ds_read_b128 v[198:201], v193 offset:16384
	ds_read_b128 v[202:205], v193 offset:17408
	ds_read_b128 v[206:209], v193 offset:18432
	ds_read_b128 v[210:213], v193 offset:19456
	ds_read_b128 v[216:219], v193 offset:20480
	ds_read_b128 v[220:223], v193 offset:21504
	ds_read_b128 v[224:227], v193 offset:22528
	ds_read_b128 v[228:231], v193 offset:23552
	global_load_lds_dwordx4 v[180:181], off
	v_lshl_add_u64 v[182:183], v[178:179], 0, v[160:161]
	s_add_i32 m0, s72, 0x2000
	v_lshl_add_u64 v[184:185], v[178:179], 0, s[10:11]
	s_add_i32 s72, s62, s44
	global_load_lds_dwordx4 v[182:183], off
	v_lshl_add_u64 v[186:187], v[184:185], 0, v[164:165]
	s_mov_b32 m0, s72
	v_lshl_add_u64 v[184:185], v[184:185], 0, v[160:161]
	global_load_lds_dwordx4 v[186:187], off
	s_add_i32 m0, s72, 0x2000
	v_lshl_add_u64 v[186:187], s[40:41], 0, v[162:163]
	global_load_lds_dwordx4 v[184:185], off
	v_lshl_add_u64 v[184:185], s[40:41], 0, v[166:167]
	s_mov_b32 m0, s47
	s_nop 0
	global_load_lds_dwordx4 v[184:185], off
	s_mov_b32 m0, s48
	s_nop 0
	global_load_lds_dwordx4 v[186:187], off
	s_cmp_lg_u32 s100, 0
	s_cbranch_scc1 .Lrx_2441_1
	s_waitcnt vmcnt(8)
.Lrx_2441_1:
	s_waitcnt vmcnt(24)
	s_mov_b32 s100, 1
	s_waitcnt lgkmcnt(0)
	s_barrier
	v_mfma_scale_f32_16x16x128_f8f6f4 v[92:95], v[16:23], v[198:205], 0, v194, v195 op_sel_hi:[0,0,0]
	v_mfma_scale_f32_16x16x128_f8f6f4 v[88:91], v[24:31], v[198:205], 0, v194, v195 op_sel_hi:[0,0,0]
	v_mfma_scale_f32_16x16x128_f8f6f4 v[84:87], v[16:23], v[206:213], 0, v194, v195 op_sel_hi:[0,0,0]
	v_mfma_scale_f32_16x16x128_f8f6f4 v[76:79], v[24:31], v[206:213], 0, v194, v195 op_sel_hi:[0,0,0]
	v_mfma_scale_f32_16x16x128_f8f6f4 v[68:71], v[16:23], v[216:223], 0, v194, v195 op_sel_hi:[0,0,0]
	v_mfma_scale_f32_16x16x128_f8f6f4 v[60:63], v[24:31], v[216:223], 0, v194, v195 op_sel_hi:[0,0,0]
	v_mfma_scale_f32_16x16x128_f8f6f4 v[52:55], v[16:23], v[224:231], 0, v194, v195 op_sel_hi:[0,0,0]
	v_mfma_scale_f32_16x16x128_f8f6f4 v[44:47], v[24:31], v[224:231], 0, v194, v195 op_sel_hi:[0,0,0]
	v_mfma_scale_f32_16x16x128_f8f6f4 v[80:83], v[0:7], v[198:205], 0, v194, v195 op_sel_hi:[0,0,0]
	v_mfma_scale_f32_16x16x128_f8f6f4 v[72:75], v[8:15], v[198:205], 0, v194, v195 op_sel_hi:[0,0,0]
	v_mfma_scale_f32_16x16x128_f8f6f4 v[64:67], v[0:7], v[206:213], 0, v194, v195 op_sel_hi:[0,0,0]
	v_mfma_scale_f32_16x16x128_f8f6f4 v[56:59], v[8:15], v[206:213], 0, v194, v195 op_sel_hi:[0,0,0]
	v_mfma_scale_f32_16x16x128_f8f6f4 v[48:51], v[0:7], v[216:223], 0, v194, v195 op_sel_hi:[0,0,0]
	v_mfma_scale_f32_16x16x128_f8f6f4 v[40:43], v[8:15], v[216:223], 0, v194, v195 op_sel_hi:[0,0,0]
	v_mfma_scale_f32_16x16x128_f8f6f4 v[36:39], v[0:7], v[224:231], 0, v194, v195 op_sel_hi:[0,0,0]
	v_mfma_scale_f32_16x16x128_f8f6f4 v[32:35], v[8:15], v[224:231], 0, v194, v195 op_sel_hi:[0,0,0]
	s_barrier
	s_add_i32 s72, 0, 0x18000
	s_add_i32 s73, 0, 0x1c000
	v_add_u32_e32 v12, s72, v189
	v_add_u32_e32 v28, s73, v189
	ds_read_b128 v[0:3], v12
	ds_read_b128 v[4:7], v12 offset:1024
	ds_read_b128 v[8:11], v12 offset:2048
	ds_read_b128 v[12:15], v12 offset:3072
	ds_read_b128 v[16:19], v28
	ds_read_b128 v[20:23], v28 offset:1024
	ds_read_b128 v[24:27], v28 offset:2048
	ds_read_b128 v[28:31], v28 offset:3072
	s_add_u32 s40, s40, 0xe0000
	s_addc_u32 s41, s41, 0
	s_mov_b32 m0, s49
	v_lshl_add_u64 v[214:215], s[40:41], 0, v[166:167]
	ds_read_b128 v[198:201], v193 offset:32768
	ds_read_b128 v[202:205], v193 offset:33792
	ds_read_b128 v[206:209], v193 offset:34816
	ds_read_b128 v[210:213], v193 offset:35840
	ds_read_b128 v[216:219], v193 offset:36864
	ds_read_b128 v[220:223], v193 offset:37888
	ds_read_b128 v[224:227], v193 offset:38912
	ds_read_b128 v[228:231], v193 offset:39936
	global_load_lds_dwordx4 v[214:215], off
	v_lshl_add_u64 v[214:215], s[40:41], 0, v[162:163]
	s_mov_b32 m0, s50
	s_nop 0
	global_load_lds_dwordx4 v[214:215], off
	s_waitcnt vmcnt(8)
	s_waitcnt lgkmcnt(0)
	s_barrier
	v_mfma_scale_f32_16x16x128_f8f6f4 v[156:159], v[0:7], v[198:205], v[156:159], v194, v195 op_sel_hi:[0,0,0]
	v_mfma_scale_f32_16x16x128_f8f6f4 v[152:155], v[8:15], v[198:205], v[152:155], v194, v195 op_sel_hi:[0,0,0]
	v_mfma_scale_f32_16x16x128_f8f6f4 v[148:151], v[0:7], v[206:213], v[148:151], v194, v195 op_sel_hi:[0,0,0]
	v_mfma_scale_f32_16x16x128_f8f6f4 v[140:143], v[8:15], v[206:213], v[140:143], v194, v195 op_sel_hi:[0,0,0]
	v_mfma_scale_f32_16x16x128_f8f6f4 v[132:135], v[0:7], v[216:223], v[132:135], v194, v195 op_sel_hi:[0,0,0]
	v_mfma_scale_f32_16x16x128_f8f6f4 v[124:127], v[8:15], v[216:223], v[124:127], v194, v195 op_sel_hi:[0,0,0]
	v_mfma_scale_f32_16x16x128_f8f6f4 v[116:119], v[0:7], v[224:231], v[116:119], v194, v195 op_sel_hi:[0,0,0]
	v_mfma_scale_f32_16x16x128_f8f6f4 v[108:111], v[8:15], v[224:231], v[108:111], v194, v195 op_sel_hi:[0,0,0]
	v_mfma_scale_f32_16x16x128_f8f6f4 v[144:147], v[16:23], v[198:205], v[144:147], v194, v195 op_sel_hi:[0,0,0]
	v_mfma_scale_f32_16x16x128_f8f6f4 v[136:139], v[24:31], v[198:205], v[136:139], v194, v195 op_sel_hi:[0,0,0]
	v_mfma_scale_f32_16x16x128_f8f6f4 v[128:131], v[16:23], v[206:213], v[128:131], v194, v195 op_sel_hi:[0,0,0]
	v_mfma_scale_f32_16x16x128_f8f6f4 v[120:123], v[24:31], v[206:213], v[120:123], v194, v195 op_sel_hi:[0,0,0]
	v_mfma_scale_f32_16x16x128_f8f6f4 v[112:115], v[16:23], v[216:223], v[112:115], v194, v195 op_sel_hi:[0,0,0]
	v_mfma_scale_f32_16x16x128_f8f6f4 v[104:107], v[24:31], v[216:223], v[104:107], v194, v195 op_sel_hi:[0,0,0]
	v_mfma_scale_f32_16x16x128_f8f6f4 v[100:103], v[16:23], v[224:231], v[100:103], v194, v195 op_sel_hi:[0,0,0]
	v_mfma_scale_f32_16x16x128_f8f6f4 v[96:99], v[24:31], v[224:231], v[96:99], v194, v195 op_sel_hi:[0,0,0]
	s_barrier
	s_add_i32 s40, s72, s44
	v_lshl_add_u64 v[180:181], v[180:181], 0, s[18:19]
	s_mov_b32 m0, s40
	ds_read_b128 v[198:201], v193 offset:49152
	ds_read_b128 v[202:205], v193 offset:50176
	ds_read_b128 v[206:209], v193 offset:51200
	ds_read_b128 v[210:213], v193 offset:52224
	ds_read_b128 v[216:219], v193 offset:53248
	ds_read_b128 v[220:223], v193 offset:54272
	ds_read_b128 v[224:227], v193 offset:55296
	ds_read_b128 v[228:231], v193 offset:56320
	global_load_lds_dwordx4 v[180:181], off
	v_lshl_add_u64 v[180:181], v[182:183], 0, s[18:19]
	s_add_i32 m0, s40, 0x2000
	v_lshl_add_u64 v[178:179], v[178:179], 0, s[22:23]
	s_add_i32 s40, s73, s44
	global_load_lds_dwordx4 v[180:181], off
	v_lshl_add_u64 v[180:181], v[178:179], 0, v[164:165]
	s_mov_b32 m0, s40
	v_lshl_add_u64 v[178:179], v[178:179], 0, v[160:161]
	global_load_lds_dwordx4 v[180:181], off
	s_add_i32 m0, s40, 0x2000
	s_nop 0
	global_load_lds_dwordx4 v[178:179], off
	v_lshl_add_u64 v[178:179], v[184:185], 0, s[18:19]
	s_mov_b32 m0, s59
	s_nop 0
	global_load_lds_dwordx4 v[178:179], off
	v_lshl_add_u64 v[178:179], v[186:187], 0, s[18:19]
	s_mov_b32 m0, s60
	s_nop 0
	global_load_lds_dwordx4 v[178:179], off
	s_waitcnt vmcnt(8)
	s_waitcnt lgkmcnt(0)
	s_barrier
	v_mfma_scale_f32_16x16x128_f8f6f4 v[92:95], v[0:7], v[198:205], v[92:95], v194, v195 op_sel_hi:[0,0,0]
	v_mfma_scale_f32_16x16x128_f8f6f4 v[88:91], v[8:15], v[198:205], v[88:91], v194, v195 op_sel_hi:[0,0,0]
	v_mfma_scale_f32_16x16x128_f8f6f4 v[84:87], v[0:7], v[206:213], v[84:87], v194, v195 op_sel_hi:[0,0,0]
	v_mfma_scale_f32_16x16x128_f8f6f4 v[76:79], v[8:15], v[206:213], v[76:79], v194, v195 op_sel_hi:[0,0,0]
	v_mfma_scale_f32_16x16x128_f8f6f4 v[68:71], v[0:7], v[216:223], v[68:71], v194, v195 op_sel_hi:[0,0,0]
	v_mfma_scale_f32_16x16x128_f8f6f4 v[60:63], v[8:15], v[216:223], v[60:63], v194, v195 op_sel_hi:[0,0,0]
	v_mfma_scale_f32_16x16x128_f8f6f4 v[52:55], v[0:7], v[224:231], v[52:55], v194, v195 op_sel_hi:[0,0,0]
	v_mfma_scale_f32_16x16x128_f8f6f4 v[44:47], v[8:15], v[224:231], v[44:47], v194, v195 op_sel_hi:[0,0,0]
	v_mfma_scale_f32_16x16x128_f8f6f4 v[80:83], v[16:23], v[198:205], v[80:83], v194, v195 op_sel_hi:[0,0,0]
	v_mfma_scale_f32_16x16x128_f8f6f4 v[72:75], v[24:31], v[198:205], v[72:75], v194, v195 op_sel_hi:[0,0,0]
	v_mfma_scale_f32_16x16x128_f8f6f4 v[64:67], v[16:23], v[206:213], v[64:67], v194, v195 op_sel_hi:[0,0,0]
	v_mfma_scale_f32_16x16x128_f8f6f4 v[56:59], v[24:31], v[206:213], v[56:59], v194, v195 op_sel_hi:[0,0,0]
	v_mfma_scale_f32_16x16x128_f8f6f4 v[48:51], v[16:23], v[216:223], v[48:51], v194, v195 op_sel_hi:[0,0,0]
	v_mfma_scale_f32_16x16x128_f8f6f4 v[40:43], v[24:31], v[216:223], v[40:43], v194, v195 op_sel_hi:[0,0,0]
	v_mfma_scale_f32_16x16x128_f8f6f4 v[36:39], v[16:23], v[224:231], v[36:39], v194, v195 op_sel_hi:[0,0,0]
	v_mfma_scale_f32_16x16x128_f8f6f4 v[32:35], v[24:31], v[224:231], v[32:35], v194, v195 op_sel_hi:[0,0,0]
	s_barrier
	s_add_i32 s71, s71, 2
	s_add_u32 s38, s38, 0x100
	s_addc_u32 s39, s39, 0
	s_cmp_gt_u32 s71, 53
	v_lshl_add_u64 v[176:177], v[176:177], 0, s[26:27]
.LBB0_2441:
	ds_read_b128 v[16:19], v191
	ds_read_b128 v[20:23], v191 offset:1024
	ds_read_b128 v[24:27], v191 offset:2048
	ds_read_b128 v[28:31], v191 offset:3072
	ds_read_b128 v[0:3], v192
	ds_read_b128 v[4:7], v192 offset:1024
	ds_read_b128 v[8:11], v192 offset:2048
	ds_read_b128 v[12:15], v192 offset:3072
	s_add_u32 s40, s38, 0xfff20080
	s_addc_u32 s41, s39, -1
	s_cmp_eq_u32 s71, 52
	s_cselect_b64 vcc, -1, 0
	s_cselect_b32 s41, s1, s41
	s_cselect_b32 s40, s0, s40
	v_cndmask_b32_e32 v179, v177, v175, vcc
	v_cndmask_b32_e32 v178, v176, v174, vcc
	v_lshl_add_u64 v[214:215], s[38:39], 0, v[168:169]
	s_add_i32 m0, s47, 0xc000
	ds_read_b128 v[180:183], v193
	ds_read_b128 v[184:187], v193 offset:1024
	ds_read_b128 v[198:201], v193 offset:2048
	ds_read_b128 v[202:205], v193 offset:3072
	ds_read_b128 v[206:209], v193 offset:4096
	ds_read_b128 v[210:213], v193 offset:5120
	ds_read_b128 v[216:219], v193 offset:6144
	ds_read_b128 v[220:223], v193 offset:7168
	global_load_lds_dwordx4 v[214:215], off
	v_lshl_add_u64 v[214:215], s[38:39], 0, v[170:171]
	s_add_i32 m0, s47, 0xe000
	s_nop 0
	global_load_lds_dwordx4 v[214:215], off
	s_waitcnt vmcnt(8)
	s_waitcnt lgkmcnt(0)
	s_barrier
	v_mfma_scale_f32_16x16x128_f8f6f4 v[156:159], v[16:23], v[180:187], v[156:159], v194, v195 op_sel_hi:[0,0,0]
	v_mfma_scale_f32_16x16x128_f8f6f4 v[152:155], v[24:31], v[180:187], v[152:155], v194, v195 op_sel_hi:[0,0,0]
	v_mfma_scale_f32_16x16x128_f8f6f4 v[148:151], v[16:23], v[198:205], v[148:151], v194, v195 op_sel_hi:[0,0,0]
	v_mfma_scale_f32_16x16x128_f8f6f4 v[140:143], v[24:31], v[198:205], v[140:143], v194, v195 op_sel_hi:[0,0,0]
	v_mfma_scale_f32_16x16x128_f8f6f4 v[132:135], v[16:23], v[206:213], v[132:135], v194, v195 op_sel_hi:[0,0,0]
	v_mfma_scale_f32_16x16x128_f8f6f4 v[124:127], v[24:31], v[206:213], v[124:127], v194, v195 op_sel_hi:[0,0,0]
	v_mfma_scale_f32_16x16x128_f8f6f4 v[116:119], v[16:23], v[216:223], v[116:119], v194, v195 op_sel_hi:[0,0,0]
	v_mfma_scale_f32_16x16x128_f8f6f4 v[108:111], v[24:31], v[216:223], v[108:111], v194, v195 op_sel_hi:[0,0,0]
	v_mfma_scale_f32_16x16x128_f8f6f4 v[144:147], v[0:7], v[180:187], v[144:147], v194, v195 op_sel_hi:[0,0,0]
	v_mfma_scale_f32_16x16x128_f8f6f4 v[136:139], v[8:15], v[180:187], v[136:139], v194, v195 op_sel_hi:[0,0,0]
	v_mfma_scale_f32_16x16x128_f8f6f4 v[128:131], v[0:7], v[198:205], v[128:131], v194, v195 op_sel_hi:[0,0,0]
	v_mfma_scale_f32_16x16x128_f8f6f4 v[120:123], v[8:15], v[198:205], v[120:123], v194, v195 op_sel_hi:[0,0,0]
	v_mfma_scale_f32_16x16x128_f8f6f4 v[112:115], v[0:7], v[206:213], v[112:115], v194, v195 op_sel_hi:[0,0,0]
	v_mfma_scale_f32_16x16x128_f8f6f4 v[104:107], v[8:15], v[206:213], v[104:107], v194, v195 op_sel_hi:[0,0,0]
	v_mfma_scale_f32_16x16x128_f8f6f4 v[100:103], v[0:7], v[216:223], v[100:103], v194, v195 op_sel_hi:[0,0,0]
	v_mfma_scale_f32_16x16x128_f8f6f4 v[96:99], v[8:15], v[216:223], v[96:99], v194, v195 op_sel_hi:[0,0,0]
	s_barrier
	s_add_i32 s72, s6, s44
	v_lshl_add_u64 v[180:181], v[178:179], 0, v[164:165]
	s_mov_b32 m0, s72
	ds_read_b128 v[198:201], v193 offset:16384
	ds_read_b128 v[202:205], v193 offset:17408
	ds_read_b128 v[206:209], v193 offset:18432
	ds_read_b128 v[210:213], v193 offset:19456
	ds_read_b128 v[216:219], v193 offset:20480
	ds_read_b128 v[220:223], v193 offset:21504
	ds_read_b128 v[224:227], v193 offset:22528
	ds_read_b128 v[228:231], v193 offset:23552
	global_load_lds_dwordx4 v[180:181], off
	v_lshl_add_u64 v[182:183], v[178:179], 0, v[160:161]
	s_add_i32 m0, s72, 0x2000
	v_lshl_add_u64 v[184:185], v[178:179], 0, s[10:11]
	s_add_i32 s72, s62, s44
	global_load_lds_dwordx4 v[182:183], off
	v_lshl_add_u64 v[186:187], v[184:185], 0, v[164:165]
	s_mov_b32 m0, s72
	v_lshl_add_u64 v[184:185], v[184:185], 0, v[160:161]
	global_load_lds_dwordx4 v[186:187], off
	s_add_i32 m0, s72, 0x2000
	v_lshl_add_u64 v[186:187], s[40:41], 0, v[162:163]
	global_load_lds_dwordx4 v[184:185], off
	v_lshl_add_u64 v[184:185], s[40:41], 0, v[166:167]
	s_mov_b32 m0, s47
	s_nop 0
	global_load_lds_dwordx4 v[184:185], off
	s_mov_b32 m0, s48
	s_nop 0
	global_load_lds_dwordx4 v[186:187], off
	s_waitcnt vmcnt(8)
	s_waitcnt lgkmcnt(0)
	s_barrier
	v_mfma_scale_f32_16x16x128_f8f6f4 v[92:95], v[16:23], v[198:205], v[92:95], v194, v195 op_sel_hi:[0,0,0]
	v_mfma_scale_f32_16x16x128_f8f6f4 v[88:91], v[24:31], v[198:205], v[88:91], v194, v195 op_sel_hi:[0,0,0]
	v_mfma_scale_f32_16x16x128_f8f6f4 v[84:87], v[16:23], v[206:213], v[84:87], v194, v195 op_sel_hi:[0,0,0]
	v_mfma_scale_f32_16x16x128_f8f6f4 v[76:79], v[24:31], v[206:213], v[76:79], v194, v195 op_sel_hi:[0,0,0]
	v_mfma_scale_f32_16x16x128_f8f6f4 v[68:71], v[16:23], v[216:223], v[68:71], v194, v195 op_sel_hi:[0,0,0]
	v_mfma_scale_f32_16x16x128_f8f6f4 v[60:63], v[24:31], v[216:223], v[60:63], v194, v195 op_sel_hi:[0,0,0]
	v_mfma_scale_f32_16x16x128_f8f6f4 v[52:55], v[16:23], v[224:231], v[52:55], v194, v195 op_sel_hi:[0,0,0]
	v_mfma_scale_f32_16x16x128_f8f6f4 v[44:47], v[24:31], v[224:231], v[44:47], v194, v195 op_sel_hi:[0,0,0]
	v_mfma_scale_f32_16x16x128_f8f6f4 v[80:83], v[0:7], v[198:205], v[80:83], v194, v195 op_sel_hi:[0,0,0]
	v_mfma_scale_f32_16x16x128_f8f6f4 v[72:75], v[8:15], v[198:205], v[72:75], v194, v195 op_sel_hi:[0,0,0]
	v_mfma_scale_f32_16x16x128_f8f6f4 v[64:67], v[0:7], v[206:213], v[64:67], v194, v195 op_sel_hi:[0,0,0]
	v_mfma_scale_f32_16x16x128_f8f6f4 v[56:59], v[8:15], v[206:213], v[56:59], v194, v195 op_sel_hi:[0,0,0]
	v_mfma_scale_f32_16x16x128_f8f6f4 v[48:51], v[0:7], v[216:223], v[48:51], v194, v195 op_sel_hi:[0,0,0]
	v_mfma_scale_f32_16x16x128_f8f6f4 v[40:43], v[8:15], v[216:223], v[40:43], v194, v195 op_sel_hi:[0,0,0]
	v_mfma_scale_f32_16x16x128_f8f6f4 v[36:39], v[0:7], v[224:231], v[36:39], v194, v195 op_sel_hi:[0,0,0]
	v_mfma_scale_f32_16x16x128_f8f6f4 v[32:35], v[8:15], v[224:231], v[32:35], v194, v195 op_sel_hi:[0,0,0]
	s_barrier
	s_add_i32 s72, 0, 0x18000
	s_add_i32 s73, 0, 0x1c000
	v_add_u32_e32 v12, s72, v189
	v_add_u32_e32 v28, s73, v189
	ds_read_b128 v[0:3], v12
	ds_read_b128 v[4:7], v12 offset:1024
	ds_read_b128 v[8:11], v12 offset:2048
	ds_read_b128 v[12:15], v12 offset:3072
	ds_read_b128 v[16:19], v28
	ds_read_b128 v[20:23], v28 offset:1024
	ds_read_b128 v[24:27], v28 offset:2048
	ds_read_b128 v[28:31], v28 offset:3072
	s_add_u32 s40, s40, 0xe0000
	s_addc_u32 s41, s41, 0
	s_mov_b32 m0, s49
	v_lshl_add_u64 v[214:215], s[40:41], 0, v[166:167]
	ds_read_b128 v[198:201], v193 offset:32768
	ds_read_b128 v[202:205], v193 offset:33792
	ds_read_b128 v[206:209], v193 offset:34816
	ds_read_b128 v[210:213], v193 offset:35840
	ds_read_b128 v[216:219], v193 offset:36864
	ds_read_b128 v[220:223], v193 offset:37888
	ds_read_b128 v[224:227], v193 offset:38912
	ds_read_b128 v[228:231], v193 offset:39936
	global_load_lds_dwordx4 v[214:215], off
	v_lshl_add_u64 v[214:215], s[40:41], 0, v[162:163]
	s_mov_b32 m0, s50
	s_nop 0
	global_load_lds_dwordx4 v[214:215], off
	s_waitcnt vmcnt(8)
	s_waitcnt lgkmcnt(0)
	s_barrier
	v_mfma_scale_f32_16x16x128_f8f6f4 v[156:159], v[0:7], v[198:205], v[156:159], v194, v195 op_sel_hi:[0,0,0]
	v_mfma_scale_f32_16x16x128_f8f6f4 v[152:155], v[8:15], v[198:205], v[152:155], v194, v195 op_sel_hi:[0,0,0]
	v_mfma_scale_f32_16x16x128_f8f6f4 v[148:151], v[0:7], v[206:213], v[148:151], v194, v195 op_sel_hi:[0,0,0]
	v_mfma_scale_f32_16x16x128_f8f6f4 v[140:143], v[8:15], v[206:213], v[140:143], v194, v195 op_sel_hi:[0,0,0]
	v_mfma_scale_f32_16x16x128_f8f6f4 v[132:135], v[0:7], v[216:223], v[132:135], v194, v195 op_sel_hi:[0,0,0]
	v_mfma_scale_f32_16x16x128_f8f6f4 v[124:127], v[8:15], v[216:223], v[124:127], v194, v195 op_sel_hi:[0,0,0]
	v_mfma_scale_f32_16x16x128_f8f6f4 v[116:119], v[0:7], v[224:231], v[116:119], v194, v195 op_sel_hi:[0,0,0]
	v_mfma_scale_f32_16x16x128_f8f6f4 v[108:111], v[8:15], v[224:231], v[108:111], v194, v195 op_sel_hi:[0,0,0]
	v_mfma_scale_f32_16x16x128_f8f6f4 v[144:147], v[16:23], v[198:205], v[144:147], v194, v195 op_sel_hi:[0,0,0]
	v_mfma_scale_f32_16x16x128_f8f6f4 v[136:139], v[24:31], v[198:205], v[136:139], v194, v195 op_sel_hi:[0,0,0]
	v_mfma_scale_f32_16x16x128_f8f6f4 v[128:131], v[16:23], v[206:213], v[128:131], v194, v195 op_sel_hi:[0,0,0]
	v_mfma_scale_f32_16x16x128_f8f6f4 v[120:123], v[24:31], v[206:213], v[120:123], v194, v195 op_sel_hi:[0,0,0]
	v_mfma_scale_f32_16x16x128_f8f6f4 v[112:115], v[16:23], v[216:223], v[112:115], v194, v195 op_sel_hi:[0,0,0]
	v_mfma_scale_f32_16x16x128_f8f6f4 v[104:107], v[24:31], v[216:223], v[104:107], v194, v195 op_sel_hi:[0,0,0]
	v_mfma_scale_f32_16x16x128_f8f6f4 v[100:103], v[16:23], v[224:231], v[100:103], v194, v195 op_sel_hi:[0,0,0]
	v_mfma_scale_f32_16x16x128_f8f6f4 v[96:99], v[24:31], v[224:231], v[96:99], v194, v195 op_sel_hi:[0,0,0]
	s_barrier
	s_add_i32 s40, s72, s44
	v_lshl_add_u64 v[180:181], v[180:181], 0, s[18:19]
	s_mov_b32 m0, s40
	ds_read_b128 v[198:201], v193 offset:49152
	ds_read_b128 v[202:205], v193 offset:50176
	ds_read_b128 v[206:209], v193 offset:51200
	ds_read_b128 v[210:213], v193 offset:52224
	ds_read_b128 v[216:219], v193 offset:53248
	ds_read_b128 v[220:223], v193 offset:54272
	ds_read_b128 v[224:227], v193 offset:55296
	ds_read_b128 v[228:231], v193 offset:56320
	global_load_lds_dwordx4 v[180:181], off
	v_lshl_add_u64 v[180:181], v[182:183], 0, s[18:19]
	s_add_i32 m0, s40, 0x2000
	v_lshl_add_u64 v[178:179], v[178:179], 0, s[22:23]
	s_add_i32 s40, s73, s44
	global_load_lds_dwordx4 v[180:181], off
	v_lshl_add_u64 v[180:181], v[178:179], 0, v[164:165]
	s_mov_b32 m0, s40
	v_lshl_add_u64 v[178:179], v[178:179], 0, v[160:161]
	global_load_lds_dwordx4 v[180:181], off
	s_add_i32 m0, s40, 0x2000
	s_nop 0
	global_load_lds_dwordx4 v[178:179], off
	v_lshl_add_u64 v[178:179], v[184:185], 0, s[18:19]
	s_mov_b32 m0, s59
	s_nop 0
	global_load_lds_dwordx4 v[178:179], off
	v_lshl_add_u64 v[178:179], v[186:187], 0, s[18:19]
	s_mov_b32 m0, s60
	s_nop 0
	global_load_lds_dwordx4 v[178:179], off
	s_waitcnt vmcnt(8)
	s_waitcnt lgkmcnt(0)
	s_barrier
	v_mfma_scale_f32_16x16x128_f8f6f4 v[92:95], v[0:7], v[198:205], v[92:95], v194, v195 op_sel_hi:[0,0,0]
	v_mfma_scale_f32_16x16x128_f8f6f4 v[88:91], v[8:15], v[198:205], v[88:91], v194, v195 op_sel_hi:[0,0,0]
	v_mfma_scale_f32_16x16x128_f8f6f4 v[84:87], v[0:7], v[206:213], v[84:87], v194, v195 op_sel_hi:[0,0,0]
	v_mfma_scale_f32_16x16x128_f8f6f4 v[76:79], v[8:15], v[206:213], v[76:79], v194, v195 op_sel_hi:[0,0,0]
	v_mfma_scale_f32_16x16x128_f8f6f4 v[68:71], v[0:7], v[216:223], v[68:71], v194, v195 op_sel_hi:[0,0,0]
	v_mfma_scale_f32_16x16x128_f8f6f4 v[60:63], v[8:15], v[216:223], v[60:63], v194, v195 op_sel_hi:[0,0,0]
	v_mfma_scale_f32_16x16x128_f8f6f4 v[52:55], v[0:7], v[224:231], v[52:55], v194, v195 op_sel_hi:[0,0,0]
	v_mfma_scale_f32_16x16x128_f8f6f4 v[44:47], v[8:15], v[224:231], v[44:47], v194, v195 op_sel_hi:[0,0,0]
	v_mfma_scale_f32_16x16x128_f8f6f4 v[80:83], v[16:23], v[198:205], v[80:83], v194, v195 op_sel_hi:[0,0,0]
	v_mfma_scale_f32_16x16x128_f8f6f4 v[72:75], v[24:31], v[198:205], v[72:75], v194, v195 op_sel_hi:[0,0,0]
	v_mfma_scale_f32_16x16x128_f8f6f4 v[64:67], v[16:23], v[206:213], v[64:67], v194, v195 op_sel_hi:[0,0,0]
	v_mfma_scale_f32_16x16x128_f8f6f4 v[56:59], v[24:31], v[206:213], v[56:59], v194, v195 op_sel_hi:[0,0,0]
	v_mfma_scale_f32_16x16x128_f8f6f4 v[48:51], v[16:23], v[216:223], v[48:51], v194, v195 op_sel_hi:[0,0,0]
	v_mfma_scale_f32_16x16x128_f8f6f4 v[40:43], v[24:31], v[216:223], v[40:43], v194, v195 op_sel_hi:[0,0,0]
	v_mfma_scale_f32_16x16x128_f8f6f4 v[36:39], v[16:23], v[224:231], v[36:39], v194, v195 op_sel_hi:[0,0,0]
	v_mfma_scale_f32_16x16x128_f8f6f4 v[32:35], v[24:31], v[224:231], v[32:35], v194, v195 op_sel_hi:[0,0,0]
	s_barrier
	s_add_i32 s71, s71, 2
	s_add_u32 s38, s38, 0x100
	s_addc_u32 s39, s39, 0
	s_cmp_gt_u32 s71, 53
	v_lshl_add_u64 v[176:177], v[176:177], 0, s[26:27]
	s_cbranch_scc0 .LBB0_2441
	s_and_b64 vcc, exec, s[24:25]
	s_cbranch_vccz .LBB0_2444
	s_barrier
